# phase 5: gate tiles touched up front (discarded loads) before the serialized mid()/epilogue iterations (on top of v23)
# baseline (speedup 1.0000x reference)
; __device__ __forceinline__ float bf_lo(unsigned w) { return __uint_as_float(w << 16); }
; __device__ __forceinline__ float bf_hi(unsigned w) { return __uint_as_float(w & 0xffff0000u); }
;     static __device__ __forceinline__ float ex(float x) { return __expf(fminf(-x, 60.f)); }
;     __device__ __forceinline__ void mid(f32x4 (&acc)[2][2][4][2], const Unit& u, int wr, int wc, int fr, int fq) const {
;         const int row0 = u.pm * BM + wr * 64 + fr, col0 = u.pn * BM + wc * 32 + 8 * fq;
;         const bf16_t* rp0 = R + (size_t)row0 * R_LD + col0;
; #pragma unroll
;         for (int ai = 0; ai < 2; ++ai)
; #pragma unroll
;             for (int m = 0; m < 4; ++m) {
;                 int off = (ai * HALF + m * 16) * R_LD; asm volatile("" : "+s"(off) :: "memory");
;                 const bf16_t* rp = rp0 + off;
; #pragma unroll
;                 for (int bj = 0; bj < 2; ++bj) {
;                     const u32x4 ga = *(const u32x4*)(rp + 6144 + bj * HALF), gc = *(const u32x4*)(rp + 8192 + bj * HALF);
;                     f32x4 r0, r1;
;                     r0[0] = (1.0f + ex(bf_lo(gc.x))) * __builtin_amdgcn_rcpf(1.0f + ex(bf_lo(ga.x))); r0[1] = (1.0f + ex(bf_hi(gc.x))) * __builtin_amdgcn_rcpf(1.0f + ex(bf_hi(ga.x)));
;                     r0[2] = (1.0f + ex(bf_lo(gc.y))) * __builtin_amdgcn_rcpf(1.0f + ex(bf_lo(ga.y))); r0[3] = (1.0f + ex(bf_hi(gc.y))) * __builtin_amdgcn_rcpf(1.0f + ex(bf_hi(ga.y)));
;                     r1[0] = (1.0f + ex(bf_lo(gc.z))) * __builtin_amdgcn_rcpf(1.0f + ex(bf_lo(ga.z))); r1[1] = (1.0f + ex(bf_hi(gc.z))) * __builtin_amdgcn_rcpf(1.0f + ex(bf_hi(ga.z)));
;                     r1[2] = (1.0f + ex(bf_lo(gc.w))) * __builtin_amdgcn_rcpf(1.0f + ex(bf_lo(ga.w))); r1[3] = (1.0f + ex(bf_hi(gc.w))) * __builtin_amdgcn_rcpf(1.0f + ex(bf_hi(ga.w)));
;                     acc[ai][bj][m][0] *= r0; acc[ai][bj][m][1] *= r1; }
;                 asm volatile("" : "+v"(acc[ai][0][m][0]), "+v"(acc[ai][0][m][1]), "+v"(acc[ai][1][m][0]), "+v"(acc[ai][1][m][1]) :: "memory"); }
.LBB0_784:
	s_andn2_b64 vcc, exec, s[46:47]
	s_mov_b32 s4, 0
	s_cbranch_vccnz .LBB0_786
	s_mov_b32 s4, s3
	s_ashr_i32 s5, s4, 31
	v_lshl_add_u64 v[2:3], s[4:5], 1, v[154:155]
	s_mov_b64 s[18:19], 0x4000
	v_lshl_add_u64 v[196:197], v[2:3], 0, s[18:19]
	global_load_dwordx4 v[192:195], v[196:197], off offset:-4096
	global_load_dwordx4 v[192:195], v[196:197], off offset:-3840
	global_load_dwordx4 v[192:195], v[196:197], off
	global_load_dwordx4 v[192:195], v[196:197], off offset:256
	s_mov_b64 s[18:19], 0x54000
	v_lshl_add_u64 v[196:197], v[2:3], 0, s[18:19]
	global_load_dwordx4 v[192:195], v[196:197], off offset:-4096
	global_load_dwordx4 v[192:195], v[196:197], off offset:-3840
	global_load_dwordx4 v[192:195], v[196:197], off
	global_load_dwordx4 v[192:195], v[196:197], off offset:256
	s_mov_b64 s[18:19], 0xa4000
	v_lshl_add_u64 v[196:197], v[2:3], 0, s[18:19]
	global_load_dwordx4 v[192:195], v[196:197], off offset:-4096
	global_load_dwordx4 v[192:195], v[196:197], off offset:-3840
	global_load_dwordx4 v[192:195], v[196:197], off
	global_load_dwordx4 v[192:195], v[196:197], off offset:256
	s_mov_b64 s[18:19], 0xf4000
	v_lshl_add_u64 v[196:197], v[2:3], 0, s[18:19]
	global_load_dwordx4 v[192:195], v[196:197], off offset:-4096
	global_load_dwordx4 v[192:195], v[196:197], off offset:-3840
	global_load_dwordx4 v[192:195], v[196:197], off
	global_load_dwordx4 v[192:195], v[196:197], off offset:256
	s_mov_b64 s[18:19], 0x284000
	v_lshl_add_u64 v[196:197], v[2:3], 0, s[18:19]
	global_load_dwordx4 v[192:195], v[196:197], off offset:-4096
	global_load_dwordx4 v[192:195], v[196:197], off offset:-3840
	global_load_dwordx4 v[192:195], v[196:197], off
	global_load_dwordx4 v[192:195], v[196:197], off offset:256
	s_mov_b64 s[18:19], 0x2d4000
	v_lshl_add_u64 v[196:197], v[2:3], 0, s[18:19]
	global_load_dwordx4 v[192:195], v[196:197], off offset:-4096
	global_load_dwordx4 v[192:195], v[196:197], off offset:-3840
	global_load_dwordx4 v[192:195], v[196:197], off
	global_load_dwordx4 v[192:195], v[196:197], off offset:256
	s_mov_b64 s[18:19], 0x324000
	v_lshl_add_u64 v[196:197], v[2:3], 0, s[18:19]
	global_load_dwordx4 v[192:195], v[196:197], off offset:-4096
	global_load_dwordx4 v[192:195], v[196:197], off offset:-3840
	global_load_dwordx4 v[192:195], v[196:197], off
	global_load_dwordx4 v[192:195], v[196:197], off offset:256
	s_mov_b64 s[18:19], 0x374000
	v_lshl_add_u64 v[196:197], v[2:3], 0, s[18:19]
	global_load_dwordx4 v[192:195], v[196:197], off offset:-4096
	global_load_dwordx4 v[192:195], v[196:197], off offset:-3840
	global_load_dwordx4 v[192:195], v[196:197], off
	global_load_dwordx4 v[192:195], v[196:197], off offset:256
	v_add_co_u32_e32 v160, vcc, 0x3000, v2
	s_mov_b32 s4, 0x28000
	s_nop 0
	v_addc_co_u32_e32 v161, vcc, 0, v3, vcc
	global_load_dwordx4 v[166:169], v[160:161], off
	v_add_co_u32_e32 v2, vcc, 0x4000, v2
	s_waitcnt vmcnt(0)
	v_lshlrev_b32_e32 v1, 16, v166
	v_addc_co_u32_e32 v3, vcc, 0, v3, vcc
	global_load_dwordx4 v[170:173], v[2:3], off
	global_load_dwordx4 v[174:177], v[160:161], off offset:256
	global_load_dwordx4 v[178:181], v[2:3], off offset:256
	v_and_b32_e32 v2, 0xffff0000, v166
	v_max_f32_e64 v1, -v1, -v1
	v_max_f32_e64 v2, -v2, -v2
	v_min_f32_e32 v1, 0x42700000, v1
	v_min_f32_e32 v2, 0x42700000, v2
	v_mul_f32_e32 v1, 0x3fb8aa3b, v1
	v_mul_f32_e32 v2, 0x3fb8aa3b, v2
	v_lshlrev_b32_e32 v3, 16, v167
	v_lshlrev_b32_e32 v161, 16, v168
	v_and_b32_e32 v166, 0xffff0000, v168
	v_exp_f32_e32 v1, v1
	v_exp_f32_e32 v185, v2
	v_max_f32_e64 v3, -v3, -v3
	v_max_f32_e64 v161, -v161, -v161
	v_min_f32_e32 v3, 0x42700000, v3
	v_min_f32_e32 v161, 0x42700000, v161
	v_mul_f32_e32 v3, 0x3fb8aa3b, v3
	v_and_b32_e32 v160, 0xffff0000, v167
	v_lshlrev_b32_e32 v167, 16, v169
	v_mul_f32_e32 v161, 0x3fb8aa3b, v161
	v_exp_f32_e32 v186, v3
	v_add_f32_e32 v1, 1.0, v1
	v_max_f32_e64 v167, -v167, -v167
	v_exp_f32_e32 v188, v161
	v_and_b32_e32 v169, 0xffff0000, v169
	v_min_f32_e32 v167, 0x42700000, v167
	v_max_f32_e64 v169, -v169, -v169
	v_mul_f32_e32 v167, 0x3fb8aa3b, v167
	v_min_f32_e32 v169, 0x42700000, v169
	v_exp_f32_e32 v191, v167
	v_mul_f32_e32 v169, 0x3fb8aa3b, v169
	v_max_f32_e64 v160, -v160, -v160
	v_max_f32_e64 v166, -v166, -v166
	v_min_f32_e32 v160, 0x42700000, v160
	v_min_f32_e32 v166, 0x42700000, v166
	v_mul_f32_e32 v160, 0x3fb8aa3b, v160
	v_mul_f32_e32 v166, 0x3fb8aa3b, v166
	v_exp_f32_e32 v187, v160
	v_exp_f32_e32 v189, v166
	s_waitcnt vmcnt(0)
; __device__ __forceinline__ float bf_lo(unsigned w) { return __uint_as_float(w << 16); }
; __device__ __forceinline__ float bf_hi(unsigned w) { return __uint_as_float(w & 0xffff0000u); }
;     static __device__ __forceinline__ float ex(float x) { return __expf(fminf(-x, 60.f)); }
;     __device__ __forceinline__ void mid(f32x4 (&acc)[2][2][4][2], const Unit& u, int wr, int wc, int fr, int fq) const {
;     ...
;                 int off = (ai * HALF + m * 16) * R_LD; asm volatile("" : "+s"(off) :: "memory");
;                 const bf16_t* rp = rp0 + off;
; #pragma unroll
;                 for (int bj = 0; bj < 2; ++bj) {
;                     const u32x4 ga = *(const u32x4*)(rp + 6144 + bj * HALF), gc = *(const u32x4*)(rp + 8192 + bj * HALF);
;                     f32x4 r0, r1;
;                     r0[0] = (1.0f + ex(bf_lo(gc.x))) * __builtin_amdgcn_rcpf(1.0f + ex(bf_lo(ga.x))); r0[1] = (1.0f + ex(bf_hi(gc.x))) * __builtin_amdgcn_rcpf(1.0f + ex(bf_hi(ga.x)));
;                     r0[2] = (1.0f + ex(bf_lo(gc.y))) * __builtin_amdgcn_rcpf(1.0f + ex(bf_lo(ga.y))); r0[3] = (1.0f + ex(bf_hi(gc.y))) * __builtin_amdgcn_rcpf(1.0f + ex(bf_hi(ga.y)));
;                     r1[0] = (1.0f + ex(bf_lo(gc.z))) * __builtin_amdgcn_rcpf(1.0f + ex(bf_lo(ga.z))); r1[1] = (1.0f + ex(bf_hi(gc.z))) * __builtin_amdgcn_rcpf(1.0f + ex(bf_hi(ga.z)));
;                     r1[2] = (1.0f + ex(bf_lo(gc.w))) * __builtin_amdgcn_rcpf(1.0f + ex(bf_lo(ga.w))); r1[3] = (1.0f + ex(bf_hi(gc.w))) * __builtin_amdgcn_rcpf(1.0f + ex(bf_hi(ga.w)));
;                     acc[ai][bj][m][0] *= r0; acc[ai][bj][m][1] *= r1; }
	v_lshlrev_b32_e32 v168, 16, v170
	v_and_b32_e32 v170, 0xffff0000, v170
	v_lshlrev_b32_e32 v182, 16, v171
	v_and_b32_e32 v171, 0xffff0000, v171
	v_max_f32_e64 v168, -v168, -v168
	v_max_f32_e64 v170, -v170, -v170
	v_max_f32_e64 v171, -v171, -v171
	v_min_f32_e32 v168, 0x42700000, v168
	v_min_f32_e32 v170, 0x42700000, v170
	v_min_f32_e32 v171, 0x42700000, v171
	v_mul_f32_e32 v168, 0x3fb8aa3b, v168
	v_mul_f32_e32 v170, 0x3fb8aa3b, v170
	v_mul_f32_e32 v171, 0x3fb8aa3b, v171
	v_exp_f32_e32 v2, v168
	v_exp_f32_e32 v3, v170
	v_add_f32_e32 v168, 1.0, v185
	v_exp_f32_e32 v161, v171
	v_rcp_f32_e32 v170, v1
	v_rcp_f32_e32 v171, v168
	v_pk_add_f32 v[2:3], v[2:3], 1.0 op_sel_hi:[1,0]
	v_lshlrev_b32_e32 v183, 16, v172
	v_and_b32_e32 v172, 0xffff0000, v172
	v_pk_mul_f32 v[2:3], v[2:3], v[170:171]
	v_exp_f32_e32 v171, v169
	v_and_b32_e32 v170, 0xffff0000, v173
	v_pk_mul_f32 v[128:129], v[128:129], v[2:3]
	v_lshlrev_b32_e32 v2, 16, v174
	v_max_f32_e64 v170, -v170, -v170
	v_max_f32_e64 v2, -v2, -v2
	v_add_f32_e32 v1, 1.0, v191
	v_min_f32_e32 v170, 0x42700000, v170
	v_min_f32_e32 v2, 0x42700000, v2
	v_max_f32_e64 v182, -v182, -v182
	v_max_f32_e64 v183, -v183, -v183
	v_max_f32_e64 v172, -v172, -v172
	v_mul_f32_e32 v169, 0x3fb8aa3b, v170
	v_rcp_f32_e32 v170, v1
	v_add_f32_e32 v1, 1.0, v171
	v_mul_f32_e32 v2, 0x3fb8aa3b, v2
	v_lshlrev_b32_e32 v184, 16, v173
	v_min_f32_e32 v182, 0x42700000, v182
	v_min_f32_e32 v183, 0x42700000, v183
	v_min_f32_e32 v172, 0x42700000, v172
	v_rcp_f32_e32 v171, v1
	v_lshlrev_b32_e32 v1, 16, v178
	v_exp_f32_e32 v3, v2
	v_max_f32_e64 v184, -v184, -v184
	v_mul_f32_e32 v182, 0x3fb8aa3b, v182
	v_mul_f32_e32 v183, 0x3fb8aa3b, v183
	v_mul_f32_e32 v172, 0x3fb8aa3b, v172
	v_max_f32_e64 v1, -v1, -v1
	v_min_f32_e32 v184, 0x42700000, v184
	v_exp_f32_e32 v160, v182
	v_exp_f32_e32 v166, v183
	v_exp_f32_e32 v167, v172
	v_add_f32_e32 v172, 1.0, v186
	v_add_f32_e32 v183, 1.0, v187
	v_min_f32_e32 v1, 0x42700000, v1
	v_mul_f32_e32 v190, 0x3fb8aa3b, v184
	v_add_f32_e32 v184, 1.0, v188
	v_add_f32_e32 v185, 1.0, v189
	v_rcp_f32_e32 v182, v172
	v_rcp_f32_e32 v183, v183
	v_mul_f32_e32 v1, 0x3fb8aa3b, v1
	v_rcp_f32_e32 v184, v184
	v_rcp_f32_e32 v185, v185
	v_exp_f32_e32 v2, v1
	v_add_f32_e32 v1, 1.0, v3
	v_and_b32_e32 v3, 0xffff0000, v174
	v_max_f32_e64 v3, -v3, -v3
	v_pk_add_f32 v[160:161], v[160:161], 1.0 op_sel_hi:[1,0]
	v_min_f32_e32 v3, 0x42700000, v3
	v_pk_mul_f32 v[160:161], v[160:161], v[182:183]
	v_exp_f32_e32 v168, v190
	v_exp_f32_e32 v169, v169
	v_pk_add_f32 v[166:167], v[166:167], 1.0 op_sel_hi:[1,0]
	v_mul_f32_e32 v3, 0x3fb8aa3b, v3
	v_pk_mul_f32 v[166:167], v[166:167], v[184:185]
	v_pk_mul_f32 v[130:131], v[130:131], v[160:161]
	v_rcp_f32_e32 v160, v1
	v_and_b32_e32 v1, 0xffff0000, v178
	v_exp_f32_e32 v161, v3
	v_pk_mul_f32 v[124:125], v[124:125], v[166:167]
	v_max_f32_e64 v1, -v1, -v1
	v_lshlrev_b32_e32 v166, 16, v175
	v_min_f32_e32 v1, 0x42700000, v1
	v_max_f32_e64 v166, -v166, -v166
	v_pk_add_f32 v[168:169], v[168:169], 1.0 op_sel_hi:[1,0]
	v_mul_f32_e32 v1, 0x3fb8aa3b, v1
	v_min_f32_e32 v166, 0x42700000, v166
	v_pk_mul_f32 v[168:169], v[168:169], v[170:171]
	v_exp_f32_e32 v3, v1
	v_add_f32_e32 v1, 1.0, v161
	v_mul_f32_e32 v166, 0x3fb8aa3b, v166
	v_pk_mul_f32 v[126:127], v[126:127], v[168:169]
	v_rcp_f32_e32 v161, v1
	v_lshlrev_b32_e32 v1, 16, v179
	v_exp_f32_e32 v167, v166
	v_and_b32_e32 v168, 0xffff0000, v175
	v_max_f32_e64 v1, -v1, -v1
	v_max_f32_e64 v168, -v168, -v168
	v_min_f32_e32 v1, 0x42700000, v1
	v_min_f32_e32 v168, 0x42700000, v168
	v_mul_f32_e32 v1, 0x3fb8aa3b, v1
	v_mul_f32_e32 v168, 0x3fb8aa3b, v168
	v_exp_f32_e32 v166, v1
	v_add_f32_e32 v1, 1.0, v167
	v_and_b32_e32 v167, 0xffff0000, v179
	v_exp_f32_e32 v169, v168
	v_max_f32_e64 v167, -v167, -v167
	v_min_f32_e32 v167, 0x42700000, v167
	v_mul_f32_e32 v167, 0x3fb8aa3b, v167
	v_exp_f32_e32 v167, v167
	v_rcp_f32_e32 v168, v1
	v_add_f32_e32 v1, 1.0, v169
	v_rcp_f32_e32 v169, v1
	v_pk_add_f32 v[166:167], v[166:167], 1.0 op_sel_hi:[1,0]
	v_pk_add_f32 v[2:3], v[2:3], 1.0 op_sel_hi:[1,0]
	v_lshlrev_b32_e32 v1, 16, v180
	v_pk_mul_f32 v[2:3], v[2:3], v[160:161]
	v_pk_mul_f32 v[160:161], v[166:167], v[168:169]
	v_lshlrev_b32_e32 v166, 16, v176
	v_max_f32_e64 v166, -v166, -v166
	v_min_f32_e32 v166, 0x42700000, v166
	v_mul_f32_e32 v166, 0x3fb8aa3b, v166
	v_exp_f32_e32 v167, v166
	v_max_f32_e64 v1, -v1, -v1
	v_min_f32_e32 v1, 0x42700000, v1
	v_mul_f32_e32 v1, 0x3fb8aa3b, v1
	v_exp_f32_e32 v166, v1
	v_add_f32_e32 v1, 1.0, v167
	v_and_b32_e32 v167, 0xffff0000, v176
	v_max_f32_e64 v167, -v167, -v167
	v_min_f32_e32 v167, 0x42700000, v167
	v_mul_f32_e32 v167, 0x3fb8aa3b, v167
	v_rcp_f32_e32 v168, v1
	v_and_b32_e32 v1, 0xffff0000, v180
	v_exp_f32_e32 v169, v167
	v_max_f32_e64 v1, -v1, -v1
	v_lshlrev_b32_e32 v170, 16, v177
	v_min_f32_e32 v1, 0x42700000, v1
	v_max_f32_e64 v170, -v170, -v170
	v_mul_f32_e32 v1, 0x3fb8aa3b, v1
	v_min_f32_e32 v170, 0x42700000, v170
	v_exp_f32_e32 v167, v1
	v_add_f32_e32 v1, 1.0, v169
	v_mul_f32_e32 v170, 0x3fb8aa3b, v170
	v_rcp_f32_e32 v169, v1
	v_lshlrev_b32_e32 v1, 16, v181
	v_exp_f32_e32 v171, v170
	v_and_b32_e32 v172, 0xffff0000, v177
	v_max_f32_e64 v1, -v1, -v1
	v_max_f32_e64 v172, -v172, -v172
	v_min_f32_e32 v1, 0x42700000, v1
	v_min_f32_e32 v172, 0x42700000, v172
	v_mul_f32_e32 v1, 0x3fb8aa3b, v1
	v_mul_f32_e32 v172, 0x3fb8aa3b, v172
	v_exp_f32_e32 v170, v1
	v_add_f32_e32 v1, 1.0, v171
	v_and_b32_e32 v171, 0xffff0000, v181
	v_exp_f32_e32 v173, v172
	v_max_f32_e64 v171, -v171, -v171
	v_min_f32_e32 v171, 0x42700000, v171
	v_mul_f32_e32 v171, 0x3fb8aa3b, v171
	v_exp_f32_e32 v171, v171
	v_rcp_f32_e32 v172, v1
	v_add_f32_e32 v1, 1.0, v173
	v_rcp_f32_e32 v173, v1
	v_pk_add_f32 v[170:171], v[170:171], 1.0 op_sel_hi:[1,0]
	v_pk_add_f32 v[166:167], v[166:167], 1.0 op_sel_hi:[1,0]
	v_pk_mul_f32 v[122:123], v[122:123], v[160:161]
	v_pk_mul_f32 v[166:167], v[166:167], v[168:169]
	v_pk_mul_f32 v[168:169], v[170:171], v[172:173]
	v_pk_mul_f32 v[120:121], v[120:121], v[2:3]
	v_pk_mul_f32 v[118:119], v[118:119], v[168:169]
	v_pk_mul_f32 v[116:117], v[116:117], v[166:167]
	s_nop 0
	s_ashr_i32 s5, s4, 31
	v_lshl_add_u64 v[2:3], s[4:5], 1, v[154:155]
	v_add_co_u32_e32 v160, vcc, s63, v2
	s_mov_b32 s4, 0x50000
	s_nop 0
	v_addc_co_u32_e32 v161, vcc, 0, v3, vcc
	global_load_dwordx4 v[166:169], v[160:161], off
	global_load_dwordx4 v[170:173], v[160:161], off offset:-4096
	v_add_co_u32_e32 v2, vcc, s70, v2
	global_load_dwordx4 v[174:177], v[160:161], off offset:256
	s_nop 0
	v_addc_co_u32_e32 v3, vcc, 0, v3, vcc
	global_load_dwordx4 v[178:181], v[2:3], off offset:256
	s_waitcnt vmcnt(0)
; __device__ __forceinline__ float bf_lo(unsigned w) { return __uint_as_float(w << 16); }
; __device__ __forceinline__ float bf_hi(unsigned w) { return __uint_as_float(w & 0xffff0000u); }
;     static __device__ __forceinline__ float ex(float x) { return __expf(fminf(-x, 60.f)); }
;     __device__ __forceinline__ void mid(f32x4 (&acc)[2][2][4][2], const Unit& u, int wr, int wc, int fr, int fq) const {
;     ...
;                 int off = (ai * HALF + m * 16) * R_LD; asm volatile("" : "+s"(off) :: "memory");
;                 const bf16_t* rp = rp0 + off;
; #pragma unroll
;                 for (int bj = 0; bj < 2; ++bj) {
;                     const u32x4 ga = *(const u32x4*)(rp + 6144 + bj * HALF), gc = *(const u32x4*)(rp + 8192 + bj * HALF);
;                     f32x4 r0, r1;
;                     r0[0] = (1.0f + ex(bf_lo(gc.x))) * __builtin_amdgcn_rcpf(1.0f + ex(bf_lo(ga.x))); r0[1] = (1.0f + ex(bf_hi(gc.x))) * __builtin_amdgcn_rcpf(1.0f + ex(bf_hi(ga.x)));
;                     r0[2] = (1.0f + ex(bf_lo(gc.y))) * __builtin_amdgcn_rcpf(1.0f + ex(bf_lo(ga.y))); r0[3] = (1.0f + ex(bf_hi(gc.y))) * __builtin_amdgcn_rcpf(1.0f + ex(bf_hi(ga.y)));
;                     r1[0] = (1.0f + ex(bf_lo(gc.z))) * __builtin_amdgcn_rcpf(1.0f + ex(bf_lo(ga.z))); r1[1] = (1.0f + ex(bf_hi(gc.z))) * __builtin_amdgcn_rcpf(1.0f + ex(bf_hi(ga.z)));
;                     r1[2] = (1.0f + ex(bf_lo(gc.w))) * __builtin_amdgcn_rcpf(1.0f + ex(bf_lo(ga.w))); r1[3] = (1.0f + ex(bf_hi(gc.w))) * __builtin_amdgcn_rcpf(1.0f + ex(bf_hi(ga.w)));
;                     acc[ai][bj][m][0] *= r0; acc[ai][bj][m][1] *= r1; }
	v_lshlrev_b32_e32 v1, 16, v166
	v_lshlrev_b32_e32 v2, 16, v170
	v_max_f32_e64 v2, -v2, -v2
	v_min_f32_e32 v2, 0x42700000, v2
	v_mul_f32_e32 v2, 0x3fb8aa3b, v2
	v_exp_f32_e32 v3, v2
	v_max_f32_e64 v1, -v1, -v1
	v_min_f32_e32 v1, 0x42700000, v1
	v_mul_f32_e32 v1, 0x3fb8aa3b, v1
	v_exp_f32_e32 v2, v1
	v_add_f32_e32 v1, 1.0, v3
	v_and_b32_e32 v3, 0xffff0000, v170
	v_max_f32_e64 v3, -v3, -v3
	v_min_f32_e32 v3, 0x42700000, v3
	v_mul_f32_e32 v3, 0x3fb8aa3b, v3
	v_rcp_f32_e32 v160, v1
	v_and_b32_e32 v1, 0xffff0000, v166
	v_exp_f32_e32 v161, v3
	v_max_f32_e64 v1, -v1, -v1
	v_lshlrev_b32_e32 v166, 16, v171
	v_min_f32_e32 v1, 0x42700000, v1
	v_max_f32_e64 v166, -v166, -v166
	v_mul_f32_e32 v1, 0x3fb8aa3b, v1
	v_min_f32_e32 v166, 0x42700000, v166
	v_exp_f32_e32 v3, v1
	v_add_f32_e32 v1, 1.0, v161
	v_mul_f32_e32 v166, 0x3fb8aa3b, v166
	v_rcp_f32_e32 v161, v1
	v_lshlrev_b32_e32 v1, 16, v167
	v_exp_f32_e32 v170, v166
	v_max_f32_e64 v1, -v1, -v1
	v_min_f32_e32 v1, 0x42700000, v1
	v_mul_f32_e32 v1, 0x3fb8aa3b, v1
	v_exp_f32_e32 v166, v1
	v_add_f32_e32 v1, 1.0, v170
	v_and_b32_e32 v170, 0xffff0000, v171
	v_max_f32_e64 v170, -v170, -v170
	v_min_f32_e32 v170, 0x42700000, v170
	v_mul_f32_e32 v170, 0x3fb8aa3b, v170
	v_and_b32_e32 v167, 0xffff0000, v167
	v_exp_f32_e32 v171, v170
	v_max_f32_e64 v167, -v167, -v167
	v_min_f32_e32 v167, 0x42700000, v167
	v_mul_f32_e32 v167, 0x3fb8aa3b, v167
	v_exp_f32_e32 v167, v167
	v_rcp_f32_e32 v170, v1
	v_add_f32_e32 v1, 1.0, v171
	v_rcp_f32_e32 v171, v1
	v_pk_add_f32 v[166:167], v[166:167], 1.0 op_sel_hi:[1,0]
	v_pk_add_f32 v[2:3], v[2:3], 1.0 op_sel_hi:[1,0]
	v_lshlrev_b32_e32 v1, 16, v168
	v_pk_mul_f32 v[2:3], v[2:3], v[160:161]
	v_pk_mul_f32 v[160:161], v[166:167], v[170:171]
	v_lshlrev_b32_e32 v166, 16, v172
	v_max_f32_e64 v166, -v166, -v166
	v_min_f32_e32 v166, 0x42700000, v166
	v_mul_f32_e32 v166, 0x3fb8aa3b, v166
	v_exp_f32_e32 v167, v166
	v_max_f32_e64 v1, -v1, -v1
	v_min_f32_e32 v1, 0x42700000, v1
	v_mul_f32_e32 v1, 0x3fb8aa3b, v1
	v_exp_f32_e32 v166, v1
	v_add_f32_e32 v1, 1.0, v167
	v_and_b32_e32 v167, 0xffff0000, v172
	v_max_f32_e64 v167, -v167, -v167
	v_min_f32_e32 v167, 0x42700000, v167
	v_mul_f32_e32 v167, 0x3fb8aa3b, v167
	v_rcp_f32_e32 v170, v1
	v_and_b32_e32 v1, 0xffff0000, v168
	v_exp_f32_e32 v168, v167
	v_max_f32_e64 v1, -v1, -v1
	v_min_f32_e32 v1, 0x42700000, v1
	v_mul_f32_e32 v1, 0x3fb8aa3b, v1
	v_exp_f32_e32 v167, v1
	v_add_f32_e32 v1, 1.0, v168
	v_lshlrev_b32_e32 v168, 16, v173
	v_max_f32_e64 v168, -v168, -v168
	v_min_f32_e32 v168, 0x42700000, v168
	v_mul_f32_e32 v168, 0x3fb8aa3b, v168
	v_rcp_f32_e32 v171, v1
	v_lshlrev_b32_e32 v1, 16, v169
	v_exp_f32_e32 v172, v168
	v_max_f32_e64 v1, -v1, -v1
	v_min_f32_e32 v1, 0x42700000, v1
	v_mul_f32_e32 v1, 0x3fb8aa3b, v1
	v_exp_f32_e32 v168, v1
	v_add_f32_e32 v1, 1.0, v172
	v_and_b32_e32 v172, 0xffff0000, v173
	v_max_f32_e64 v172, -v172, -v172
	v_min_f32_e32 v172, 0x42700000, v172
	v_mul_f32_e32 v172, 0x3fb8aa3b, v172
	v_exp_f32_e32 v173, v172
	v_pk_mul_f32 v[112:113], v[112:113], v[2:3]
	v_lshlrev_b32_e32 v2, 16, v178
	v_max_f32_e64 v2, -v2, -v2
	v_min_f32_e32 v2, 0x42700000, v2
	v_rcp_f32_e32 v172, v1
	v_add_f32_e32 v1, 1.0, v173
	v_mul_f32_e32 v2, 0x3fb8aa3b, v2
	v_rcp_f32_e32 v173, v1
	v_lshlrev_b32_e32 v1, 16, v174
	v_exp_f32_e32 v3, v2
	v_max_f32_e64 v1, -v1, -v1
	v_min_f32_e32 v1, 0x42700000, v1
	v_and_b32_e32 v169, 0xffff0000, v169
	v_mul_f32_e32 v1, 0x3fb8aa3b, v1
	v_max_f32_e64 v169, -v169, -v169
	v_exp_f32_e32 v2, v1
	v_add_f32_e32 v1, 1.0, v3
	v_and_b32_e32 v3, 0xffff0000, v178
	v_min_f32_e32 v169, 0x42700000, v169
	v_max_f32_e64 v3, -v3, -v3
	v_mul_f32_e32 v169, 0x3fb8aa3b, v169
	v_min_f32_e32 v3, 0x42700000, v3
	v_exp_f32_e32 v169, v169
	v_pk_add_f32 v[166:167], v[166:167], 1.0 op_sel_hi:[1,0]
	v_mul_f32_e32 v3, 0x3fb8aa3b, v3
	v_pk_mul_f32 v[166:167], v[166:167], v[170:171]
	v_pk_mul_f32 v[114:115], v[114:115], v[160:161]
	v_rcp_f32_e32 v160, v1
	v_and_b32_e32 v1, 0xffff0000, v174
	v_exp_f32_e32 v161, v3
	v_pk_mul_f32 v[108:109], v[108:109], v[166:167]
	v_max_f32_e64 v1, -v1, -v1
	v_lshlrev_b32_e32 v166, 16, v179
	v_min_f32_e32 v1, 0x42700000, v1
	v_max_f32_e64 v166, -v166, -v166
	v_pk_add_f32 v[168:169], v[168:169], 1.0 op_sel_hi:[1,0]
	v_mul_f32_e32 v1, 0x3fb8aa3b, v1
	v_min_f32_e32 v166, 0x42700000, v166
	v_pk_mul_f32 v[168:169], v[168:169], v[172:173]
	v_exp_f32_e32 v3, v1
	v_add_f32_e32 v1, 1.0, v161
	v_mul_f32_e32 v166, 0x3fb8aa3b, v166
	v_pk_mul_f32 v[110:111], v[110:111], v[168:169]
	v_rcp_f32_e32 v161, v1
	v_lshlrev_b32_e32 v1, 16, v175
	v_exp_f32_e32 v167, v166
	v_and_b32_e32 v168, 0xffff0000, v179
	v_max_f32_e64 v1, -v1, -v1
	v_max_f32_e64 v168, -v168, -v168
	v_min_f32_e32 v1, 0x42700000, v1
	v_min_f32_e32 v168, 0x42700000, v168
	v_mul_f32_e32 v1, 0x3fb8aa3b, v1
	v_mul_f32_e32 v168, 0x3fb8aa3b, v168
	v_exp_f32_e32 v166, v1
	v_add_f32_e32 v1, 1.0, v167
	v_and_b32_e32 v167, 0xffff0000, v175
	v_exp_f32_e32 v169, v168
	v_max_f32_e64 v167, -v167, -v167
	v_min_f32_e32 v167, 0x42700000, v167
	v_mul_f32_e32 v167, 0x3fb8aa3b, v167
	v_exp_f32_e32 v167, v167
	v_rcp_f32_e32 v168, v1
	v_add_f32_e32 v1, 1.0, v169
	v_rcp_f32_e32 v169, v1
	v_pk_add_f32 v[166:167], v[166:167], 1.0 op_sel_hi:[1,0]
	v_pk_add_f32 v[2:3], v[2:3], 1.0 op_sel_hi:[1,0]
	v_lshlrev_b32_e32 v1, 16, v176
	v_pk_mul_f32 v[2:3], v[2:3], v[160:161]
	v_pk_mul_f32 v[160:161], v[166:167], v[168:169]
	v_lshlrev_b32_e32 v166, 16, v180
	v_max_f32_e64 v166, -v166, -v166
	v_min_f32_e32 v166, 0x42700000, v166
	v_mul_f32_e32 v166, 0x3fb8aa3b, v166
	v_exp_f32_e32 v167, v166
	v_max_f32_e64 v1, -v1, -v1
	v_min_f32_e32 v1, 0x42700000, v1
	v_mul_f32_e32 v1, 0x3fb8aa3b, v1
	v_exp_f32_e32 v166, v1
; __device__ __forceinline__ float bf_lo(unsigned w) { return __uint_as_float(w << 16); }
; __device__ __forceinline__ float bf_hi(unsigned w) { return __uint_as_float(w & 0xffff0000u); }
;     static __device__ __forceinline__ float ex(float x) { return __expf(fminf(-x, 60.f)); }
;     __device__ __forceinline__ void mid(f32x4 (&acc)[2][2][4][2], const Unit& u, int wr, int wc, int fr, int fq) const {
;     ...
;                 int off = (ai * HALF + m * 16) * R_LD; asm volatile("" : "+s"(off) :: "memory");
;                 const bf16_t* rp = rp0 + off;
; #pragma unroll
;                 for (int bj = 0; bj < 2; ++bj) {
;                     const u32x4 ga = *(const u32x4*)(rp + 6144 + bj * HALF), gc = *(const u32x4*)(rp + 8192 + bj * HALF);
;                     f32x4 r0, r1;
;                     r0[0] = (1.0f + ex(bf_lo(gc.x))) * __builtin_amdgcn_rcpf(1.0f + ex(bf_lo(ga.x))); r0[1] = (1.0f + ex(bf_hi(gc.x))) * __builtin_amdgcn_rcpf(1.0f + ex(bf_hi(ga.x)));
;                     r0[2] = (1.0f + ex(bf_lo(gc.y))) * __builtin_amdgcn_rcpf(1.0f + ex(bf_lo(ga.y))); r0[3] = (1.0f + ex(bf_hi(gc.y))) * __builtin_amdgcn_rcpf(1.0f + ex(bf_hi(ga.y)));
;                     r1[0] = (1.0f + ex(bf_lo(gc.z))) * __builtin_amdgcn_rcpf(1.0f + ex(bf_lo(ga.z))); r1[1] = (1.0f + ex(bf_hi(gc.z))) * __builtin_amdgcn_rcpf(1.0f + ex(bf_hi(ga.z)));
;                     r1[2] = (1.0f + ex(bf_lo(gc.w))) * __builtin_amdgcn_rcpf(1.0f + ex(bf_lo(ga.w))); r1[3] = (1.0f + ex(bf_hi(gc.w))) * __builtin_amdgcn_rcpf(1.0f + ex(bf_hi(ga.w)));
;                     acc[ai][bj][m][0] *= r0; acc[ai][bj][m][1] *= r1; }
	v_add_f32_e32 v1, 1.0, v167
	v_and_b32_e32 v167, 0xffff0000, v180
	v_max_f32_e64 v167, -v167, -v167
	v_min_f32_e32 v167, 0x42700000, v167
	v_mul_f32_e32 v167, 0x3fb8aa3b, v167
	v_rcp_f32_e32 v168, v1
	v_and_b32_e32 v1, 0xffff0000, v176
	v_exp_f32_e32 v169, v167
	v_max_f32_e64 v1, -v1, -v1
	v_lshlrev_b32_e32 v170, 16, v181
	v_min_f32_e32 v1, 0x42700000, v1
	v_max_f32_e64 v170, -v170, -v170
	v_mul_f32_e32 v1, 0x3fb8aa3b, v1
	v_min_f32_e32 v170, 0x42700000, v170
	v_exp_f32_e32 v167, v1
	v_add_f32_e32 v1, 1.0, v169
	v_mul_f32_e32 v170, 0x3fb8aa3b, v170
	v_rcp_f32_e32 v169, v1
	v_lshlrev_b32_e32 v1, 16, v177
	v_exp_f32_e32 v171, v170
	v_and_b32_e32 v172, 0xffff0000, v181
	v_max_f32_e64 v1, -v1, -v1
	v_max_f32_e64 v172, -v172, -v172
	v_min_f32_e32 v1, 0x42700000, v1
	v_min_f32_e32 v172, 0x42700000, v172
	v_mul_f32_e32 v1, 0x3fb8aa3b, v1
	v_mul_f32_e32 v172, 0x3fb8aa3b, v172
	v_exp_f32_e32 v170, v1
	v_add_f32_e32 v1, 1.0, v171
	v_and_b32_e32 v171, 0xffff0000, v177
	v_exp_f32_e32 v173, v172
	v_max_f32_e64 v171, -v171, -v171
	v_min_f32_e32 v171, 0x42700000, v171
	v_mul_f32_e32 v171, 0x3fb8aa3b, v171
	v_exp_f32_e32 v171, v171
	v_rcp_f32_e32 v172, v1
	v_add_f32_e32 v1, 1.0, v173
	v_rcp_f32_e32 v173, v1
	v_pk_add_f32 v[170:171], v[170:171], 1.0 op_sel_hi:[1,0]
	v_pk_add_f32 v[166:167], v[166:167], 1.0 op_sel_hi:[1,0]
	v_pk_mul_f32 v[106:107], v[106:107], v[160:161]
	v_pk_mul_f32 v[166:167], v[166:167], v[168:169]
	v_pk_mul_f32 v[168:169], v[170:171], v[172:173]
	v_pk_mul_f32 v[104:105], v[104:105], v[2:3]
	v_pk_mul_f32 v[102:103], v[102:103], v[168:169]
	v_pk_mul_f32 v[100:101], v[100:101], v[166:167]
	s_nop 0
	s_ashr_i32 s5, s4, 31
	v_lshl_add_u64 v[2:3], s[4:5], 1, v[154:155]
	v_add_co_u32_e32 v160, vcc, s63, v2
	s_mov_b32 s4, 0x78000
	s_nop 0
	v_addc_co_u32_e32 v161, vcc, 0, v3, vcc
	global_load_dwordx4 v[166:169], v[160:161], off
	global_load_dwordx4 v[170:173], v[160:161], off offset:-4096
	v_add_co_u32_e32 v2, vcc, s70, v2
	global_load_dwordx4 v[174:177], v[160:161], off offset:256
	s_nop 0
	v_addc_co_u32_e32 v3, vcc, 0, v3, vcc
	global_load_dwordx4 v[178:181], v[2:3], off offset:256
	s_waitcnt vmcnt(0)
	v_lshlrev_b32_e32 v1, 16, v166
	v_lshlrev_b32_e32 v2, 16, v170
	v_max_f32_e64 v2, -v2, -v2
	v_min_f32_e32 v2, 0x42700000, v2
	v_mul_f32_e32 v2, 0x3fb8aa3b, v2
	v_exp_f32_e32 v3, v2
	v_max_f32_e64 v1, -v1, -v1
	v_min_f32_e32 v1, 0x42700000, v1
	v_mul_f32_e32 v1, 0x3fb8aa3b, v1
	v_exp_f32_e32 v2, v1
	v_add_f32_e32 v1, 1.0, v3
	v_and_b32_e32 v3, 0xffff0000, v170
	v_max_f32_e64 v3, -v3, -v3
	v_min_f32_e32 v3, 0x42700000, v3
	v_mul_f32_e32 v3, 0x3fb8aa3b, v3
	v_rcp_f32_e32 v160, v1
	v_and_b32_e32 v1, 0xffff0000, v166
	v_exp_f32_e32 v161, v3
	v_max_f32_e64 v1, -v1, -v1
	v_lshlrev_b32_e32 v166, 16, v171
	v_min_f32_e32 v1, 0x42700000, v1
	v_max_f32_e64 v166, -v166, -v166
	v_mul_f32_e32 v1, 0x3fb8aa3b, v1
	v_min_f32_e32 v166, 0x42700000, v166
	v_exp_f32_e32 v3, v1
	v_add_f32_e32 v1, 1.0, v161
	v_mul_f32_e32 v166, 0x3fb8aa3b, v166
	v_rcp_f32_e32 v161, v1
	v_lshlrev_b32_e32 v1, 16, v167
	v_exp_f32_e32 v170, v166
	v_max_f32_e64 v1, -v1, -v1
	v_min_f32_e32 v1, 0x42700000, v1
	v_mul_f32_e32 v1, 0x3fb8aa3b, v1
	v_exp_f32_e32 v166, v1
	v_add_f32_e32 v1, 1.0, v170
	v_and_b32_e32 v170, 0xffff0000, v171
	v_max_f32_e64 v170, -v170, -v170
	v_min_f32_e32 v170, 0x42700000, v170
	v_mul_f32_e32 v170, 0x3fb8aa3b, v170
	v_and_b32_e32 v167, 0xffff0000, v167
	v_exp_f32_e32 v171, v170
	v_max_f32_e64 v167, -v167, -v167
	v_min_f32_e32 v167, 0x42700000, v167
	v_mul_f32_e32 v167, 0x3fb8aa3b, v167
	v_exp_f32_e32 v167, v167
	v_rcp_f32_e32 v170, v1
	v_add_f32_e32 v1, 1.0, v171
	v_rcp_f32_e32 v171, v1
	v_pk_add_f32 v[166:167], v[166:167], 1.0 op_sel_hi:[1,0]
	v_pk_add_f32 v[2:3], v[2:3], 1.0 op_sel_hi:[1,0]
	v_lshlrev_b32_e32 v1, 16, v168
	v_pk_mul_f32 v[2:3], v[2:3], v[160:161]
	v_pk_mul_f32 v[160:161], v[166:167], v[170:171]
	v_lshlrev_b32_e32 v166, 16, v172
	v_max_f32_e64 v166, -v166, -v166
	v_min_f32_e32 v166, 0x42700000, v166
	v_mul_f32_e32 v166, 0x3fb8aa3b, v166
	v_exp_f32_e32 v167, v166
	v_max_f32_e64 v1, -v1, -v1
	v_min_f32_e32 v1, 0x42700000, v1
	v_mul_f32_e32 v1, 0x3fb8aa3b, v1
	v_exp_f32_e32 v166, v1
	v_add_f32_e32 v1, 1.0, v167
	v_and_b32_e32 v167, 0xffff0000, v172
	v_max_f32_e64 v167, -v167, -v167
	v_min_f32_e32 v167, 0x42700000, v167
	v_mul_f32_e32 v167, 0x3fb8aa3b, v167
	v_rcp_f32_e32 v170, v1
	v_and_b32_e32 v1, 0xffff0000, v168
	v_exp_f32_e32 v168, v167
	v_max_f32_e64 v1, -v1, -v1
	v_min_f32_e32 v1, 0x42700000, v1
	v_mul_f32_e32 v1, 0x3fb8aa3b, v1
	v_exp_f32_e32 v167, v1
	v_add_f32_e32 v1, 1.0, v168
	v_lshlrev_b32_e32 v168, 16, v173
	v_max_f32_e64 v168, -v168, -v168
	v_min_f32_e32 v168, 0x42700000, v168
	v_mul_f32_e32 v168, 0x3fb8aa3b, v168
	v_rcp_f32_e32 v171, v1
	v_lshlrev_b32_e32 v1, 16, v169
	v_exp_f32_e32 v172, v168
	v_max_f32_e64 v1, -v1, -v1
	v_min_f32_e32 v1, 0x42700000, v1
	v_mul_f32_e32 v1, 0x3fb8aa3b, v1
	v_exp_f32_e32 v168, v1
	v_add_f32_e32 v1, 1.0, v172
	v_and_b32_e32 v172, 0xffff0000, v173
	v_max_f32_e64 v172, -v172, -v172
	v_min_f32_e32 v172, 0x42700000, v172
	v_mul_f32_e32 v172, 0x3fb8aa3b, v172
	v_exp_f32_e32 v173, v172
	v_pk_mul_f32 v[96:97], v[96:97], v[2:3]
	v_lshlrev_b32_e32 v2, 16, v178
	v_max_f32_e64 v2, -v2, -v2
	v_min_f32_e32 v2, 0x42700000, v2
	v_rcp_f32_e32 v172, v1
	v_add_f32_e32 v1, 1.0, v173
	v_mul_f32_e32 v2, 0x3fb8aa3b, v2
	v_rcp_f32_e32 v173, v1
	v_lshlrev_b32_e32 v1, 16, v174
	v_exp_f32_e32 v3, v2
	v_max_f32_e64 v1, -v1, -v1
	v_min_f32_e32 v1, 0x42700000, v1
	v_and_b32_e32 v169, 0xffff0000, v169
	v_mul_f32_e32 v1, 0x3fb8aa3b, v1
	v_max_f32_e64 v169, -v169, -v169
	v_exp_f32_e32 v2, v1
	v_add_f32_e32 v1, 1.0, v3
; __device__ __forceinline__ float bf_lo(unsigned w) { return __uint_as_float(w << 16); }
; __device__ __forceinline__ float bf_hi(unsigned w) { return __uint_as_float(w & 0xffff0000u); }
;     static __device__ __forceinline__ float ex(float x) { return __expf(fminf(-x, 60.f)); }
;     __device__ __forceinline__ void mid(f32x4 (&acc)[2][2][4][2], const Unit& u, int wr, int wc, int fr, int fq) const {
;     ...
;                 int off = (ai * HALF + m * 16) * R_LD; asm volatile("" : "+s"(off) :: "memory");
;                 const bf16_t* rp = rp0 + off;
; #pragma unroll
;                 for (int bj = 0; bj < 2; ++bj) {
;                     const u32x4 ga = *(const u32x4*)(rp + 6144 + bj * HALF), gc = *(const u32x4*)(rp + 8192 + bj * HALF);
;                     f32x4 r0, r1;
;                     r0[0] = (1.0f + ex(bf_lo(gc.x))) * __builtin_amdgcn_rcpf(1.0f + ex(bf_lo(ga.x))); r0[1] = (1.0f + ex(bf_hi(gc.x))) * __builtin_amdgcn_rcpf(1.0f + ex(bf_hi(ga.x)));
;                     r0[2] = (1.0f + ex(bf_lo(gc.y))) * __builtin_amdgcn_rcpf(1.0f + ex(bf_lo(ga.y))); r0[3] = (1.0f + ex(bf_hi(gc.y))) * __builtin_amdgcn_rcpf(1.0f + ex(bf_hi(ga.y)));
;                     r1[0] = (1.0f + ex(bf_lo(gc.z))) * __builtin_amdgcn_rcpf(1.0f + ex(bf_lo(ga.z))); r1[1] = (1.0f + ex(bf_hi(gc.z))) * __builtin_amdgcn_rcpf(1.0f + ex(bf_hi(ga.z)));
;                     r1[2] = (1.0f + ex(bf_lo(gc.w))) * __builtin_amdgcn_rcpf(1.0f + ex(bf_lo(ga.w))); r1[3] = (1.0f + ex(bf_hi(gc.w))) * __builtin_amdgcn_rcpf(1.0f + ex(bf_hi(ga.w)));
;                     acc[ai][bj][m][0] *= r0; acc[ai][bj][m][1] *= r1; }
	v_and_b32_e32 v3, 0xffff0000, v178
	v_min_f32_e32 v169, 0x42700000, v169
	v_max_f32_e64 v3, -v3, -v3
	v_mul_f32_e32 v169, 0x3fb8aa3b, v169
	v_min_f32_e32 v3, 0x42700000, v3
	v_exp_f32_e32 v169, v169
	v_pk_add_f32 v[166:167], v[166:167], 1.0 op_sel_hi:[1,0]
	v_mul_f32_e32 v3, 0x3fb8aa3b, v3
	v_pk_mul_f32 v[166:167], v[166:167], v[170:171]
	v_pk_mul_f32 v[98:99], v[98:99], v[160:161]
	v_rcp_f32_e32 v160, v1
	v_and_b32_e32 v1, 0xffff0000, v174
	v_exp_f32_e32 v161, v3
	v_pk_mul_f32 v[92:93], v[92:93], v[166:167]
	v_max_f32_e64 v1, -v1, -v1
	v_lshlrev_b32_e32 v166, 16, v179
	v_min_f32_e32 v1, 0x42700000, v1
	v_max_f32_e64 v166, -v166, -v166
	v_pk_add_f32 v[168:169], v[168:169], 1.0 op_sel_hi:[1,0]
	v_mul_f32_e32 v1, 0x3fb8aa3b, v1
	v_min_f32_e32 v166, 0x42700000, v166
	v_pk_mul_f32 v[168:169], v[168:169], v[172:173]
	v_exp_f32_e32 v3, v1
	v_add_f32_e32 v1, 1.0, v161
	v_mul_f32_e32 v166, 0x3fb8aa3b, v166
	v_pk_mul_f32 v[94:95], v[94:95], v[168:169]
	v_rcp_f32_e32 v161, v1
	v_lshlrev_b32_e32 v1, 16, v175
	v_exp_f32_e32 v167, v166
	v_and_b32_e32 v168, 0xffff0000, v179
	v_max_f32_e64 v1, -v1, -v1
	v_max_f32_e64 v168, -v168, -v168
	v_min_f32_e32 v1, 0x42700000, v1
	v_min_f32_e32 v168, 0x42700000, v168
	v_mul_f32_e32 v1, 0x3fb8aa3b, v1
	v_mul_f32_e32 v168, 0x3fb8aa3b, v168
	v_exp_f32_e32 v166, v1
	v_add_f32_e32 v1, 1.0, v167
	v_and_b32_e32 v167, 0xffff0000, v175
	v_exp_f32_e32 v169, v168
	v_max_f32_e64 v167, -v167, -v167
	v_min_f32_e32 v167, 0x42700000, v167
	v_mul_f32_e32 v167, 0x3fb8aa3b, v167
	v_exp_f32_e32 v167, v167
	v_rcp_f32_e32 v168, v1
	v_add_f32_e32 v1, 1.0, v169
	v_rcp_f32_e32 v169, v1
	v_pk_add_f32 v[166:167], v[166:167], 1.0 op_sel_hi:[1,0]
	v_pk_add_f32 v[2:3], v[2:3], 1.0 op_sel_hi:[1,0]
	v_lshlrev_b32_e32 v1, 16, v176
	v_pk_mul_f32 v[2:3], v[2:3], v[160:161]
	v_pk_mul_f32 v[160:161], v[166:167], v[168:169]
	v_lshlrev_b32_e32 v166, 16, v180
	v_max_f32_e64 v166, -v166, -v166
	v_min_f32_e32 v166, 0x42700000, v166
	v_mul_f32_e32 v166, 0x3fb8aa3b, v166
	v_exp_f32_e32 v167, v166
	v_max_f32_e64 v1, -v1, -v1
	v_min_f32_e32 v1, 0x42700000, v1
	v_mul_f32_e32 v1, 0x3fb8aa3b, v1
	v_exp_f32_e32 v166, v1
	v_add_f32_e32 v1, 1.0, v167
	v_and_b32_e32 v167, 0xffff0000, v180
	v_max_f32_e64 v167, -v167, -v167
	v_min_f32_e32 v167, 0x42700000, v167
	v_mul_f32_e32 v167, 0x3fb8aa3b, v167
	v_rcp_f32_e32 v168, v1
	v_and_b32_e32 v1, 0xffff0000, v176
	v_exp_f32_e32 v169, v167
	v_max_f32_e64 v1, -v1, -v1
	v_lshlrev_b32_e32 v170, 16, v181
	v_min_f32_e32 v1, 0x42700000, v1
	v_max_f32_e64 v170, -v170, -v170
	v_mul_f32_e32 v1, 0x3fb8aa3b, v1
	v_min_f32_e32 v170, 0x42700000, v170
	v_exp_f32_e32 v167, v1
	v_add_f32_e32 v1, 1.0, v169
	v_mul_f32_e32 v170, 0x3fb8aa3b, v170
	v_rcp_f32_e32 v169, v1
	v_lshlrev_b32_e32 v1, 16, v177
	v_exp_f32_e32 v171, v170
	v_and_b32_e32 v172, 0xffff0000, v181
	v_max_f32_e64 v1, -v1, -v1
	v_max_f32_e64 v172, -v172, -v172
	v_min_f32_e32 v1, 0x42700000, v1
	v_min_f32_e32 v172, 0x42700000, v172
	v_mul_f32_e32 v1, 0x3fb8aa3b, v1
	v_mul_f32_e32 v172, 0x3fb8aa3b, v172
	v_exp_f32_e32 v170, v1
	v_add_f32_e32 v1, 1.0, v171
	v_and_b32_e32 v171, 0xffff0000, v177
	v_exp_f32_e32 v173, v172
	v_max_f32_e64 v171, -v171, -v171
	v_min_f32_e32 v171, 0x42700000, v171
	v_mul_f32_e32 v171, 0x3fb8aa3b, v171
	v_exp_f32_e32 v171, v171
	v_rcp_f32_e32 v172, v1
	v_add_f32_e32 v1, 1.0, v173
	v_rcp_f32_e32 v173, v1
	v_pk_add_f32 v[170:171], v[170:171], 1.0 op_sel_hi:[1,0]
	v_pk_add_f32 v[166:167], v[166:167], 1.0 op_sel_hi:[1,0]
	v_pk_mul_f32 v[90:91], v[90:91], v[160:161]
	v_pk_mul_f32 v[166:167], v[166:167], v[168:169]
	v_pk_mul_f32 v[168:169], v[170:171], v[172:173]
	v_pk_mul_f32 v[88:89], v[88:89], v[2:3]
	v_pk_mul_f32 v[86:87], v[86:87], v[168:169]
	v_pk_mul_f32 v[84:85], v[84:85], v[166:167]
	s_nop 0
	s_ashr_i32 s5, s4, 31
	v_lshl_add_u64 v[2:3], s[4:5], 1, v[154:155]
	v_add_co_u32_e32 v160, vcc, s63, v2
	s_mov_b32 s4, 0x140000
	s_nop 0
	v_addc_co_u32_e32 v161, vcc, 0, v3, vcc
	global_load_dwordx4 v[166:169], v[160:161], off
	global_load_dwordx4 v[170:173], v[160:161], off offset:-4096
	v_add_co_u32_e32 v2, vcc, s70, v2
	global_load_dwordx4 v[174:177], v[160:161], off offset:256
	s_nop 0
	v_addc_co_u32_e32 v3, vcc, 0, v3, vcc
	global_load_dwordx4 v[178:181], v[2:3], off offset:256
	s_waitcnt vmcnt(0)
; __device__ __forceinline__ float bf_lo(unsigned w) { return __uint_as_float(w << 16); }
; __device__ __forceinline__ float bf_hi(unsigned w) { return __uint_as_float(w & 0xffff0000u); }
;     static __device__ __forceinline__ float ex(float x) { return __expf(fminf(-x, 60.f)); }
;     __device__ __forceinline__ void mid(f32x4 (&acc)[2][2][4][2], const Unit& u, int wr, int wc, int fr, int fq) const {
;     ...
;                 int off = (ai * HALF + m * 16) * R_LD; asm volatile("" : "+s"(off) :: "memory");
;                 const bf16_t* rp = rp0 + off;
; #pragma unroll
;                 for (int bj = 0; bj < 2; ++bj) {
;                     const u32x4 ga = *(const u32x4*)(rp + 6144 + bj * HALF), gc = *(const u32x4*)(rp + 8192 + bj * HALF);
;                     f32x4 r0, r1;
;                     r0[0] = (1.0f + ex(bf_lo(gc.x))) * __builtin_amdgcn_rcpf(1.0f + ex(bf_lo(ga.x))); r0[1] = (1.0f + ex(bf_hi(gc.x))) * __builtin_amdgcn_rcpf(1.0f + ex(bf_hi(ga.x)));
;                     r0[2] = (1.0f + ex(bf_lo(gc.y))) * __builtin_amdgcn_rcpf(1.0f + ex(bf_lo(ga.y))); r0[3] = (1.0f + ex(bf_hi(gc.y))) * __builtin_amdgcn_rcpf(1.0f + ex(bf_hi(ga.y)));
;                     r1[0] = (1.0f + ex(bf_lo(gc.z))) * __builtin_amdgcn_rcpf(1.0f + ex(bf_lo(ga.z))); r1[1] = (1.0f + ex(bf_hi(gc.z))) * __builtin_amdgcn_rcpf(1.0f + ex(bf_hi(ga.z)));
;                     r1[2] = (1.0f + ex(bf_lo(gc.w))) * __builtin_amdgcn_rcpf(1.0f + ex(bf_lo(ga.w))); r1[3] = (1.0f + ex(bf_hi(gc.w))) * __builtin_amdgcn_rcpf(1.0f + ex(bf_hi(ga.w)));
;                     acc[ai][bj][m][0] *= r0; acc[ai][bj][m][1] *= r1; }
	v_lshlrev_b32_e32 v1, 16, v166
	v_lshlrev_b32_e32 v2, 16, v170
	v_max_f32_e64 v2, -v2, -v2
	v_min_f32_e32 v2, 0x42700000, v2
	v_mul_f32_e32 v2, 0x3fb8aa3b, v2
	v_exp_f32_e32 v3, v2
	v_max_f32_e64 v1, -v1, -v1
	v_min_f32_e32 v1, 0x42700000, v1
	v_mul_f32_e32 v1, 0x3fb8aa3b, v1
	v_exp_f32_e32 v2, v1
	v_add_f32_e32 v1, 1.0, v3
	v_and_b32_e32 v3, 0xffff0000, v170
	v_max_f32_e64 v3, -v3, -v3
	v_min_f32_e32 v3, 0x42700000, v3
	v_mul_f32_e32 v3, 0x3fb8aa3b, v3
	v_rcp_f32_e32 v160, v1
	v_and_b32_e32 v1, 0xffff0000, v166
	v_exp_f32_e32 v161, v3
	v_max_f32_e64 v1, -v1, -v1
	v_lshlrev_b32_e32 v166, 16, v171
	v_min_f32_e32 v1, 0x42700000, v1
	v_max_f32_e64 v166, -v166, -v166
	v_mul_f32_e32 v1, 0x3fb8aa3b, v1
	v_min_f32_e32 v166, 0x42700000, v166
	v_exp_f32_e32 v3, v1
	v_add_f32_e32 v1, 1.0, v161
	v_mul_f32_e32 v166, 0x3fb8aa3b, v166
	v_rcp_f32_e32 v161, v1
	v_lshlrev_b32_e32 v1, 16, v167
	v_exp_f32_e32 v170, v166
	v_max_f32_e64 v1, -v1, -v1
	v_min_f32_e32 v1, 0x42700000, v1
	v_mul_f32_e32 v1, 0x3fb8aa3b, v1
	v_exp_f32_e32 v166, v1
	v_add_f32_e32 v1, 1.0, v170
	v_and_b32_e32 v170, 0xffff0000, v171
	v_max_f32_e64 v170, -v170, -v170
	v_min_f32_e32 v170, 0x42700000, v170
	v_mul_f32_e32 v170, 0x3fb8aa3b, v170
	v_and_b32_e32 v167, 0xffff0000, v167
	v_exp_f32_e32 v171, v170
	v_max_f32_e64 v167, -v167, -v167
	v_min_f32_e32 v167, 0x42700000, v167
	v_mul_f32_e32 v167, 0x3fb8aa3b, v167
	v_exp_f32_e32 v167, v167
	v_rcp_f32_e32 v170, v1
	v_add_f32_e32 v1, 1.0, v171
	v_rcp_f32_e32 v171, v1
	v_pk_add_f32 v[166:167], v[166:167], 1.0 op_sel_hi:[1,0]
	v_pk_add_f32 v[2:3], v[2:3], 1.0 op_sel_hi:[1,0]
	v_lshlrev_b32_e32 v1, 16, v168
	v_pk_mul_f32 v[2:3], v[2:3], v[160:161]
	v_pk_mul_f32 v[160:161], v[166:167], v[170:171]
	v_lshlrev_b32_e32 v166, 16, v172
	v_max_f32_e64 v166, -v166, -v166
	v_min_f32_e32 v166, 0x42700000, v166
	v_mul_f32_e32 v166, 0x3fb8aa3b, v166
	v_exp_f32_e32 v167, v166
	v_max_f32_e64 v1, -v1, -v1
	v_min_f32_e32 v1, 0x42700000, v1
	v_mul_f32_e32 v1, 0x3fb8aa3b, v1
	v_exp_f32_e32 v166, v1
	v_add_f32_e32 v1, 1.0, v167
	v_and_b32_e32 v167, 0xffff0000, v172
	v_max_f32_e64 v167, -v167, -v167
	v_min_f32_e32 v167, 0x42700000, v167
	v_mul_f32_e32 v167, 0x3fb8aa3b, v167
	v_rcp_f32_e32 v170, v1
	v_and_b32_e32 v1, 0xffff0000, v168
	v_exp_f32_e32 v168, v167
	v_max_f32_e64 v1, -v1, -v1
	v_min_f32_e32 v1, 0x42700000, v1
	v_mul_f32_e32 v1, 0x3fb8aa3b, v1
	v_exp_f32_e32 v167, v1
	v_add_f32_e32 v1, 1.0, v168
	v_lshlrev_b32_e32 v168, 16, v173
	v_max_f32_e64 v168, -v168, -v168
	v_min_f32_e32 v168, 0x42700000, v168
	v_mul_f32_e32 v168, 0x3fb8aa3b, v168
	v_rcp_f32_e32 v171, v1
	v_lshlrev_b32_e32 v1, 16, v169
	v_exp_f32_e32 v172, v168
	v_max_f32_e64 v1, -v1, -v1
	v_min_f32_e32 v1, 0x42700000, v1
	v_mul_f32_e32 v1, 0x3fb8aa3b, v1
	v_exp_f32_e32 v168, v1
	v_add_f32_e32 v1, 1.0, v172
	v_and_b32_e32 v172, 0xffff0000, v173
	v_max_f32_e64 v172, -v172, -v172
	v_min_f32_e32 v172, 0x42700000, v172
	v_mul_f32_e32 v172, 0x3fb8aa3b, v172
	v_exp_f32_e32 v173, v172
	v_pk_mul_f32 v[80:81], v[80:81], v[2:3]
	v_lshlrev_b32_e32 v2, 16, v178
	v_max_f32_e64 v2, -v2, -v2
	v_min_f32_e32 v2, 0x42700000, v2
	v_rcp_f32_e32 v172, v1
	v_add_f32_e32 v1, 1.0, v173
	v_mul_f32_e32 v2, 0x3fb8aa3b, v2
	v_rcp_f32_e32 v173, v1
	v_lshlrev_b32_e32 v1, 16, v174
	v_exp_f32_e32 v3, v2
	v_max_f32_e64 v1, -v1, -v1
	v_min_f32_e32 v1, 0x42700000, v1
	v_and_b32_e32 v169, 0xffff0000, v169
	v_mul_f32_e32 v1, 0x3fb8aa3b, v1
	v_max_f32_e64 v169, -v169, -v169
	v_exp_f32_e32 v2, v1
	v_add_f32_e32 v1, 1.0, v3
	v_and_b32_e32 v3, 0xffff0000, v178
	v_min_f32_e32 v169, 0x42700000, v169
	v_max_f32_e64 v3, -v3, -v3
	v_mul_f32_e32 v169, 0x3fb8aa3b, v169
	v_min_f32_e32 v3, 0x42700000, v3
	v_exp_f32_e32 v169, v169
	v_pk_add_f32 v[166:167], v[166:167], 1.0 op_sel_hi:[1,0]
	v_mul_f32_e32 v3, 0x3fb8aa3b, v3
	v_pk_mul_f32 v[166:167], v[166:167], v[170:171]
	v_pk_mul_f32 v[82:83], v[82:83], v[160:161]
	v_rcp_f32_e32 v160, v1
	v_and_b32_e32 v1, 0xffff0000, v174
	v_exp_f32_e32 v161, v3
	v_pk_mul_f32 v[76:77], v[76:77], v[166:167]
	v_max_f32_e64 v1, -v1, -v1
	v_lshlrev_b32_e32 v166, 16, v179
	v_min_f32_e32 v1, 0x42700000, v1
	v_max_f32_e64 v166, -v166, -v166
	v_pk_add_f32 v[168:169], v[168:169], 1.0 op_sel_hi:[1,0]
	v_mul_f32_e32 v1, 0x3fb8aa3b, v1
	v_min_f32_e32 v166, 0x42700000, v166
	v_pk_mul_f32 v[168:169], v[168:169], v[172:173]
	v_exp_f32_e32 v3, v1
	v_add_f32_e32 v1, 1.0, v161
	v_mul_f32_e32 v166, 0x3fb8aa3b, v166
	v_pk_mul_f32 v[78:79], v[78:79], v[168:169]
	v_rcp_f32_e32 v161, v1
	v_lshlrev_b32_e32 v1, 16, v175
	v_exp_f32_e32 v167, v166
	v_and_b32_e32 v168, 0xffff0000, v179
	v_max_f32_e64 v1, -v1, -v1
	v_max_f32_e64 v168, -v168, -v168
	v_min_f32_e32 v1, 0x42700000, v1
	v_min_f32_e32 v168, 0x42700000, v168
	v_mul_f32_e32 v1, 0x3fb8aa3b, v1
	v_mul_f32_e32 v168, 0x3fb8aa3b, v168
	v_exp_f32_e32 v166, v1
	v_add_f32_e32 v1, 1.0, v167
	v_and_b32_e32 v167, 0xffff0000, v175
	v_exp_f32_e32 v169, v168
	v_max_f32_e64 v167, -v167, -v167
	v_min_f32_e32 v167, 0x42700000, v167
	v_mul_f32_e32 v167, 0x3fb8aa3b, v167
	v_exp_f32_e32 v167, v167
	v_rcp_f32_e32 v168, v1
	v_add_f32_e32 v1, 1.0, v169
	v_rcp_f32_e32 v169, v1
	v_pk_add_f32 v[166:167], v[166:167], 1.0 op_sel_hi:[1,0]
	v_pk_add_f32 v[2:3], v[2:3], 1.0 op_sel_hi:[1,0]
	v_lshlrev_b32_e32 v1, 16, v176
	v_pk_mul_f32 v[2:3], v[2:3], v[160:161]
	v_pk_mul_f32 v[160:161], v[166:167], v[168:169]
	v_lshlrev_b32_e32 v166, 16, v180
	v_max_f32_e64 v166, -v166, -v166
	v_min_f32_e32 v166, 0x42700000, v166
	v_mul_f32_e32 v166, 0x3fb8aa3b, v166
	v_exp_f32_e32 v167, v166
	v_max_f32_e64 v1, -v1, -v1
	v_min_f32_e32 v1, 0x42700000, v1
	v_mul_f32_e32 v1, 0x3fb8aa3b, v1
	v_exp_f32_e32 v166, v1
	v_add_f32_e32 v1, 1.0, v167
; __device__ __forceinline__ float bf_lo(unsigned w) { return __uint_as_float(w << 16); }
; __device__ __forceinline__ float bf_hi(unsigned w) { return __uint_as_float(w & 0xffff0000u); }
;     static __device__ __forceinline__ float ex(float x) { return __expf(fminf(-x, 60.f)); }
;     __device__ __forceinline__ void mid(f32x4 (&acc)[2][2][4][2], const Unit& u, int wr, int wc, int fr, int fq) const {
;     ...
;                 int off = (ai * HALF + m * 16) * R_LD; asm volatile("" : "+s"(off) :: "memory");
;                 const bf16_t* rp = rp0 + off;
; #pragma unroll
;                 for (int bj = 0; bj < 2; ++bj) {
;                     const u32x4 ga = *(const u32x4*)(rp + 6144 + bj * HALF), gc = *(const u32x4*)(rp + 8192 + bj * HALF);
;                     f32x4 r0, r1;
;                     r0[0] = (1.0f + ex(bf_lo(gc.x))) * __builtin_amdgcn_rcpf(1.0f + ex(bf_lo(ga.x))); r0[1] = (1.0f + ex(bf_hi(gc.x))) * __builtin_amdgcn_rcpf(1.0f + ex(bf_hi(ga.x)));
;                     r0[2] = (1.0f + ex(bf_lo(gc.y))) * __builtin_amdgcn_rcpf(1.0f + ex(bf_lo(ga.y))); r0[3] = (1.0f + ex(bf_hi(gc.y))) * __builtin_amdgcn_rcpf(1.0f + ex(bf_hi(ga.y)));
;                     r1[0] = (1.0f + ex(bf_lo(gc.z))) * __builtin_amdgcn_rcpf(1.0f + ex(bf_lo(ga.z))); r1[1] = (1.0f + ex(bf_hi(gc.z))) * __builtin_amdgcn_rcpf(1.0f + ex(bf_hi(ga.z)));
;                     r1[2] = (1.0f + ex(bf_lo(gc.w))) * __builtin_amdgcn_rcpf(1.0f + ex(bf_lo(ga.w))); r1[3] = (1.0f + ex(bf_hi(gc.w))) * __builtin_amdgcn_rcpf(1.0f + ex(bf_hi(ga.w)));
;                     acc[ai][bj][m][0] *= r0; acc[ai][bj][m][1] *= r1; }
	v_and_b32_e32 v167, 0xffff0000, v180
	v_max_f32_e64 v167, -v167, -v167
	v_min_f32_e32 v167, 0x42700000, v167
	v_mul_f32_e32 v167, 0x3fb8aa3b, v167
	v_rcp_f32_e32 v168, v1
	v_and_b32_e32 v1, 0xffff0000, v176
	v_exp_f32_e32 v169, v167
	v_max_f32_e64 v1, -v1, -v1
	v_lshlrev_b32_e32 v170, 16, v181
	v_min_f32_e32 v1, 0x42700000, v1
	v_max_f32_e64 v170, -v170, -v170
	v_mul_f32_e32 v1, 0x3fb8aa3b, v1
	v_min_f32_e32 v170, 0x42700000, v170
	v_exp_f32_e32 v167, v1
	v_add_f32_e32 v1, 1.0, v169
	v_mul_f32_e32 v170, 0x3fb8aa3b, v170
	v_rcp_f32_e32 v169, v1
	v_lshlrev_b32_e32 v1, 16, v177
	v_exp_f32_e32 v171, v170
	v_and_b32_e32 v172, 0xffff0000, v181
	v_max_f32_e64 v1, -v1, -v1
	v_max_f32_e64 v172, -v172, -v172
	v_min_f32_e32 v1, 0x42700000, v1
	v_min_f32_e32 v172, 0x42700000, v172
	v_mul_f32_e32 v1, 0x3fb8aa3b, v1
	v_mul_f32_e32 v172, 0x3fb8aa3b, v172
	v_exp_f32_e32 v170, v1
	v_add_f32_e32 v1, 1.0, v171
	v_and_b32_e32 v171, 0xffff0000, v177
	v_exp_f32_e32 v173, v172
	v_max_f32_e64 v171, -v171, -v171
	v_min_f32_e32 v171, 0x42700000, v171
	v_mul_f32_e32 v171, 0x3fb8aa3b, v171
	v_exp_f32_e32 v171, v171
	v_rcp_f32_e32 v172, v1
	v_add_f32_e32 v1, 1.0, v173
	v_rcp_f32_e32 v173, v1
	v_pk_add_f32 v[170:171], v[170:171], 1.0 op_sel_hi:[1,0]
	v_pk_add_f32 v[166:167], v[166:167], 1.0 op_sel_hi:[1,0]
	v_pk_mul_f32 v[74:75], v[74:75], v[160:161]
	v_pk_mul_f32 v[166:167], v[166:167], v[168:169]
	v_pk_mul_f32 v[168:169], v[170:171], v[172:173]
	v_pk_mul_f32 v[72:73], v[72:73], v[2:3]
	v_pk_mul_f32 v[70:71], v[70:71], v[168:169]
	v_pk_mul_f32 v[68:69], v[68:69], v[166:167]
	s_nop 0
	s_ashr_i32 s5, s4, 31
	v_lshl_add_u64 v[2:3], s[4:5], 1, v[154:155]
	v_add_co_u32_e32 v160, vcc, s63, v2
	s_mov_b32 s4, 0x168000
	s_nop 0
	v_addc_co_u32_e32 v161, vcc, 0, v3, vcc
	global_load_dwordx4 v[166:169], v[160:161], off
	global_load_dwordx4 v[170:173], v[160:161], off offset:-4096
	v_add_co_u32_e32 v2, vcc, s70, v2
	global_load_dwordx4 v[174:177], v[160:161], off offset:256
	s_nop 0
	v_addc_co_u32_e32 v3, vcc, 0, v3, vcc
	global_load_dwordx4 v[178:181], v[2:3], off offset:256
	s_waitcnt vmcnt(0)
	v_lshlrev_b32_e32 v1, 16, v166
	v_lshlrev_b32_e32 v2, 16, v170
	v_max_f32_e64 v2, -v2, -v2
	v_min_f32_e32 v2, 0x42700000, v2
	v_mul_f32_e32 v2, 0x3fb8aa3b, v2
	v_exp_f32_e32 v3, v2
	v_max_f32_e64 v1, -v1, -v1
	v_min_f32_e32 v1, 0x42700000, v1
	v_mul_f32_e32 v1, 0x3fb8aa3b, v1
	v_exp_f32_e32 v2, v1
	v_add_f32_e32 v1, 1.0, v3
	v_and_b32_e32 v3, 0xffff0000, v170
	v_max_f32_e64 v3, -v3, -v3
	v_min_f32_e32 v3, 0x42700000, v3
	v_mul_f32_e32 v3, 0x3fb8aa3b, v3
	v_rcp_f32_e32 v160, v1
	v_and_b32_e32 v1, 0xffff0000, v166
	v_exp_f32_e32 v161, v3
	v_max_f32_e64 v1, -v1, -v1
	v_lshlrev_b32_e32 v166, 16, v171
	v_min_f32_e32 v1, 0x42700000, v1
	v_max_f32_e64 v166, -v166, -v166
	v_mul_f32_e32 v1, 0x3fb8aa3b, v1
	v_min_f32_e32 v166, 0x42700000, v166
	v_exp_f32_e32 v3, v1
	v_add_f32_e32 v1, 1.0, v161
	v_mul_f32_e32 v166, 0x3fb8aa3b, v166
	v_rcp_f32_e32 v161, v1
	v_lshlrev_b32_e32 v1, 16, v167
	v_exp_f32_e32 v170, v166
	v_max_f32_e64 v1, -v1, -v1
	v_min_f32_e32 v1, 0x42700000, v1
	v_mul_f32_e32 v1, 0x3fb8aa3b, v1
	v_exp_f32_e32 v166, v1
	v_add_f32_e32 v1, 1.0, v170
	v_and_b32_e32 v170, 0xffff0000, v171
	v_max_f32_e64 v170, -v170, -v170
	v_min_f32_e32 v170, 0x42700000, v170
	v_mul_f32_e32 v170, 0x3fb8aa3b, v170
	v_and_b32_e32 v167, 0xffff0000, v167
	v_exp_f32_e32 v171, v170
	v_max_f32_e64 v167, -v167, -v167
	v_min_f32_e32 v167, 0x42700000, v167
	v_mul_f32_e32 v167, 0x3fb8aa3b, v167
	v_exp_f32_e32 v167, v167
	v_rcp_f32_e32 v170, v1
	v_add_f32_e32 v1, 1.0, v171
	v_rcp_f32_e32 v171, v1
	v_pk_add_f32 v[166:167], v[166:167], 1.0 op_sel_hi:[1,0]
	v_pk_add_f32 v[2:3], v[2:3], 1.0 op_sel_hi:[1,0]
	v_lshlrev_b32_e32 v1, 16, v168
	v_pk_mul_f32 v[2:3], v[2:3], v[160:161]
	v_pk_mul_f32 v[160:161], v[166:167], v[170:171]
	v_lshlrev_b32_e32 v166, 16, v172
	v_max_f32_e64 v166, -v166, -v166
	v_min_f32_e32 v166, 0x42700000, v166
	v_mul_f32_e32 v166, 0x3fb8aa3b, v166
	v_exp_f32_e32 v167, v166
	v_max_f32_e64 v1, -v1, -v1
	v_min_f32_e32 v1, 0x42700000, v1
	v_mul_f32_e32 v1, 0x3fb8aa3b, v1
	v_exp_f32_e32 v166, v1
	v_add_f32_e32 v1, 1.0, v167
	v_and_b32_e32 v167, 0xffff0000, v172
	v_max_f32_e64 v167, -v167, -v167
	v_min_f32_e32 v167, 0x42700000, v167
	v_mul_f32_e32 v167, 0x3fb8aa3b, v167
	v_rcp_f32_e32 v170, v1
	v_and_b32_e32 v1, 0xffff0000, v168
	v_exp_f32_e32 v168, v167
	v_max_f32_e64 v1, -v1, -v1
	v_min_f32_e32 v1, 0x42700000, v1
	v_mul_f32_e32 v1, 0x3fb8aa3b, v1
	v_exp_f32_e32 v167, v1
	v_add_f32_e32 v1, 1.0, v168
	v_lshlrev_b32_e32 v168, 16, v173
	v_max_f32_e64 v168, -v168, -v168
	v_min_f32_e32 v168, 0x42700000, v168
	v_mul_f32_e32 v168, 0x3fb8aa3b, v168
	v_rcp_f32_e32 v171, v1
	v_lshlrev_b32_e32 v1, 16, v169
	v_exp_f32_e32 v172, v168
	v_max_f32_e64 v1, -v1, -v1
	v_min_f32_e32 v1, 0x42700000, v1
	v_mul_f32_e32 v1, 0x3fb8aa3b, v1
	v_exp_f32_e32 v168, v1
	v_add_f32_e32 v1, 1.0, v172
	v_and_b32_e32 v172, 0xffff0000, v173
	v_max_f32_e64 v172, -v172, -v172
	v_min_f32_e32 v172, 0x42700000, v172
	v_mul_f32_e32 v172, 0x3fb8aa3b, v172
	v_exp_f32_e32 v173, v172
	v_pk_mul_f32 v[64:65], v[64:65], v[2:3]
	v_lshlrev_b32_e32 v2, 16, v178
	v_max_f32_e64 v2, -v2, -v2
	v_min_f32_e32 v2, 0x42700000, v2
	v_rcp_f32_e32 v172, v1
	v_add_f32_e32 v1, 1.0, v173
	v_mul_f32_e32 v2, 0x3fb8aa3b, v2
	v_rcp_f32_e32 v173, v1
	v_lshlrev_b32_e32 v1, 16, v174
	v_exp_f32_e32 v3, v2
	v_max_f32_e64 v1, -v1, -v1
	v_min_f32_e32 v1, 0x42700000, v1
	v_and_b32_e32 v169, 0xffff0000, v169
	v_mul_f32_e32 v1, 0x3fb8aa3b, v1
	v_max_f32_e64 v169, -v169, -v169
	v_exp_f32_e32 v2, v1
	v_add_f32_e32 v1, 1.0, v3
	v_and_b32_e32 v3, 0xffff0000, v178
	v_min_f32_e32 v169, 0x42700000, v169
; __device__ __forceinline__ float bf_lo(unsigned w) { return __uint_as_float(w << 16); }
; __device__ __forceinline__ float bf_hi(unsigned w) { return __uint_as_float(w & 0xffff0000u); }
;     static __device__ __forceinline__ float ex(float x) { return __expf(fminf(-x, 60.f)); }
;     __device__ __forceinline__ void mid(f32x4 (&acc)[2][2][4][2], const Unit& u, int wr, int wc, int fr, int fq) const {
;     ...
;                 int off = (ai * HALF + m * 16) * R_LD; asm volatile("" : "+s"(off) :: "memory");
;                 const bf16_t* rp = rp0 + off;
; #pragma unroll
;                 for (int bj = 0; bj < 2; ++bj) {
;                     const u32x4 ga = *(const u32x4*)(rp + 6144 + bj * HALF), gc = *(const u32x4*)(rp + 8192 + bj * HALF);
;                     f32x4 r0, r1;
;                     r0[0] = (1.0f + ex(bf_lo(gc.x))) * __builtin_amdgcn_rcpf(1.0f + ex(bf_lo(ga.x))); r0[1] = (1.0f + ex(bf_hi(gc.x))) * __builtin_amdgcn_rcpf(1.0f + ex(bf_hi(ga.x)));
;                     r0[2] = (1.0f + ex(bf_lo(gc.y))) * __builtin_amdgcn_rcpf(1.0f + ex(bf_lo(ga.y))); r0[3] = (1.0f + ex(bf_hi(gc.y))) * __builtin_amdgcn_rcpf(1.0f + ex(bf_hi(ga.y)));
;                     r1[0] = (1.0f + ex(bf_lo(gc.z))) * __builtin_amdgcn_rcpf(1.0f + ex(bf_lo(ga.z))); r1[1] = (1.0f + ex(bf_hi(gc.z))) * __builtin_amdgcn_rcpf(1.0f + ex(bf_hi(ga.z)));
;                     r1[2] = (1.0f + ex(bf_lo(gc.w))) * __builtin_amdgcn_rcpf(1.0f + ex(bf_lo(ga.w))); r1[3] = (1.0f + ex(bf_hi(gc.w))) * __builtin_amdgcn_rcpf(1.0f + ex(bf_hi(ga.w)));
;                     acc[ai][bj][m][0] *= r0; acc[ai][bj][m][1] *= r1; }
	v_max_f32_e64 v3, -v3, -v3
	v_mul_f32_e32 v169, 0x3fb8aa3b, v169
	v_min_f32_e32 v3, 0x42700000, v3
	v_exp_f32_e32 v169, v169
	v_pk_add_f32 v[166:167], v[166:167], 1.0 op_sel_hi:[1,0]
	v_mul_f32_e32 v3, 0x3fb8aa3b, v3
	v_pk_mul_f32 v[166:167], v[166:167], v[170:171]
	v_pk_mul_f32 v[66:67], v[66:67], v[160:161]
	v_rcp_f32_e32 v160, v1
	v_and_b32_e32 v1, 0xffff0000, v174
	v_exp_f32_e32 v161, v3
	v_pk_mul_f32 v[60:61], v[60:61], v[166:167]
	v_max_f32_e64 v1, -v1, -v1
	v_lshlrev_b32_e32 v166, 16, v179
	v_min_f32_e32 v1, 0x42700000, v1
	v_max_f32_e64 v166, -v166, -v166
	v_pk_add_f32 v[168:169], v[168:169], 1.0 op_sel_hi:[1,0]
	v_mul_f32_e32 v1, 0x3fb8aa3b, v1
	v_min_f32_e32 v166, 0x42700000, v166
	v_pk_mul_f32 v[168:169], v[168:169], v[172:173]
	v_exp_f32_e32 v3, v1
	v_add_f32_e32 v1, 1.0, v161
	v_mul_f32_e32 v166, 0x3fb8aa3b, v166
	v_pk_mul_f32 v[62:63], v[62:63], v[168:169]
	v_rcp_f32_e32 v161, v1
	v_lshlrev_b32_e32 v1, 16, v175
	v_exp_f32_e32 v167, v166
	v_and_b32_e32 v168, 0xffff0000, v179
	v_max_f32_e64 v1, -v1, -v1
	v_max_f32_e64 v168, -v168, -v168
	v_min_f32_e32 v1, 0x42700000, v1
	v_min_f32_e32 v168, 0x42700000, v168
	v_mul_f32_e32 v1, 0x3fb8aa3b, v1
	v_mul_f32_e32 v168, 0x3fb8aa3b, v168
	v_exp_f32_e32 v166, v1
	v_add_f32_e32 v1, 1.0, v167
	v_and_b32_e32 v167, 0xffff0000, v175
	v_exp_f32_e32 v169, v168
	v_max_f32_e64 v167, -v167, -v167
	v_min_f32_e32 v167, 0x42700000, v167
	v_mul_f32_e32 v167, 0x3fb8aa3b, v167
	v_exp_f32_e32 v167, v167
	v_rcp_f32_e32 v168, v1
	v_add_f32_e32 v1, 1.0, v169
	v_rcp_f32_e32 v169, v1
	v_pk_add_f32 v[166:167], v[166:167], 1.0 op_sel_hi:[1,0]
	v_pk_add_f32 v[2:3], v[2:3], 1.0 op_sel_hi:[1,0]
	v_lshlrev_b32_e32 v1, 16, v176
	v_pk_mul_f32 v[2:3], v[2:3], v[160:161]
	v_pk_mul_f32 v[160:161], v[166:167], v[168:169]
	v_lshlrev_b32_e32 v166, 16, v180
	v_max_f32_e64 v166, -v166, -v166
	v_min_f32_e32 v166, 0x42700000, v166
	v_mul_f32_e32 v166, 0x3fb8aa3b, v166
	v_exp_f32_e32 v167, v166
	v_max_f32_e64 v1, -v1, -v1
	v_min_f32_e32 v1, 0x42700000, v1
	v_mul_f32_e32 v1, 0x3fb8aa3b, v1
	v_exp_f32_e32 v166, v1
	v_add_f32_e32 v1, 1.0, v167
	v_and_b32_e32 v167, 0xffff0000, v180
	v_max_f32_e64 v167, -v167, -v167
	v_min_f32_e32 v167, 0x42700000, v167
	v_mul_f32_e32 v167, 0x3fb8aa3b, v167
	v_rcp_f32_e32 v168, v1
	v_and_b32_e32 v1, 0xffff0000, v176
	v_exp_f32_e32 v169, v167
	v_max_f32_e64 v1, -v1, -v1
	v_lshlrev_b32_e32 v170, 16, v181
	v_min_f32_e32 v1, 0x42700000, v1
	v_max_f32_e64 v170, -v170, -v170
	v_mul_f32_e32 v1, 0x3fb8aa3b, v1
	v_min_f32_e32 v170, 0x42700000, v170
	v_exp_f32_e32 v167, v1
	v_add_f32_e32 v1, 1.0, v169
	v_mul_f32_e32 v170, 0x3fb8aa3b, v170
	v_rcp_f32_e32 v169, v1
	v_lshlrev_b32_e32 v1, 16, v177
	v_exp_f32_e32 v171, v170
	v_and_b32_e32 v172, 0xffff0000, v181
	v_max_f32_e64 v1, -v1, -v1
	v_max_f32_e64 v172, -v172, -v172
	v_min_f32_e32 v1, 0x42700000, v1
	v_min_f32_e32 v172, 0x42700000, v172
	v_mul_f32_e32 v1, 0x3fb8aa3b, v1
	v_mul_f32_e32 v172, 0x3fb8aa3b, v172
	v_exp_f32_e32 v170, v1
	v_add_f32_e32 v1, 1.0, v171
	v_and_b32_e32 v171, 0xffff0000, v177
	v_exp_f32_e32 v173, v172
	v_max_f32_e64 v171, -v171, -v171
	v_min_f32_e32 v171, 0x42700000, v171
	v_mul_f32_e32 v171, 0x3fb8aa3b, v171
	v_exp_f32_e32 v171, v171
	v_rcp_f32_e32 v172, v1
	v_add_f32_e32 v1, 1.0, v173
	v_rcp_f32_e32 v173, v1
	v_pk_add_f32 v[170:171], v[170:171], 1.0 op_sel_hi:[1,0]
	v_pk_add_f32 v[166:167], v[166:167], 1.0 op_sel_hi:[1,0]
	v_pk_mul_f32 v[58:59], v[58:59], v[160:161]
	v_pk_mul_f32 v[166:167], v[166:167], v[168:169]
	v_pk_mul_f32 v[168:169], v[170:171], v[172:173]
	v_pk_mul_f32 v[56:57], v[56:57], v[2:3]
	v_pk_mul_f32 v[54:55], v[54:55], v[168:169]
	v_pk_mul_f32 v[52:53], v[52:53], v[166:167]
	s_nop 0
	s_ashr_i32 s5, s4, 31
	v_lshl_add_u64 v[2:3], s[4:5], 1, v[154:155]
	v_add_co_u32_e32 v160, vcc, s63, v2
	s_mov_b32 s4, 0x190000
	s_nop 0
	v_addc_co_u32_e32 v161, vcc, 0, v3, vcc
	global_load_dwordx4 v[166:169], v[160:161], off
	global_load_dwordx4 v[170:173], v[160:161], off offset:-4096
	v_add_co_u32_e32 v2, vcc, s70, v2
	global_load_dwordx4 v[174:177], v[160:161], off offset:256
	s_nop 0
	v_addc_co_u32_e32 v3, vcc, 0, v3, vcc
	global_load_dwordx4 v[178:181], v[2:3], off offset:256
	s_waitcnt vmcnt(0)
	v_lshlrev_b32_e32 v1, 16, v166
	v_lshlrev_b32_e32 v2, 16, v170
	v_max_f32_e64 v2, -v2, -v2
	v_min_f32_e32 v2, 0x42700000, v2
	v_mul_f32_e32 v2, 0x3fb8aa3b, v2
	v_exp_f32_e32 v3, v2
	v_max_f32_e64 v1, -v1, -v1
	v_min_f32_e32 v1, 0x42700000, v1
	v_mul_f32_e32 v1, 0x3fb8aa3b, v1
	v_exp_f32_e32 v2, v1
	v_add_f32_e32 v1, 1.0, v3
	v_and_b32_e32 v3, 0xffff0000, v170
	v_max_f32_e64 v3, -v3, -v3
	v_min_f32_e32 v3, 0x42700000, v3
	v_mul_f32_e32 v3, 0x3fb8aa3b, v3
	v_rcp_f32_e32 v160, v1
	v_and_b32_e32 v1, 0xffff0000, v166
	v_exp_f32_e32 v161, v3
	v_max_f32_e64 v1, -v1, -v1
	v_lshlrev_b32_e32 v166, 16, v171
	v_min_f32_e32 v1, 0x42700000, v1
	v_max_f32_e64 v166, -v166, -v166
	v_mul_f32_e32 v1, 0x3fb8aa3b, v1
	v_min_f32_e32 v166, 0x42700000, v166
	v_exp_f32_e32 v3, v1
	v_add_f32_e32 v1, 1.0, v161
	v_mul_f32_e32 v166, 0x3fb8aa3b, v166
	v_rcp_f32_e32 v161, v1
	v_lshlrev_b32_e32 v1, 16, v167
	v_exp_f32_e32 v170, v166
	v_max_f32_e64 v1, -v1, -v1
	v_min_f32_e32 v1, 0x42700000, v1
	v_mul_f32_e32 v1, 0x3fb8aa3b, v1
	v_exp_f32_e32 v166, v1
	v_add_f32_e32 v1, 1.0, v170
	v_and_b32_e32 v170, 0xffff0000, v171
	v_max_f32_e64 v170, -v170, -v170
	v_min_f32_e32 v170, 0x42700000, v170
	v_mul_f32_e32 v170, 0x3fb8aa3b, v170
	v_and_b32_e32 v167, 0xffff0000, v167
	v_exp_f32_e32 v171, v170
	v_max_f32_e64 v167, -v167, -v167
	v_min_f32_e32 v167, 0x42700000, v167
	v_mul_f32_e32 v167, 0x3fb8aa3b, v167
	v_exp_f32_e32 v167, v167
	v_rcp_f32_e32 v170, v1
	v_add_f32_e32 v1, 1.0, v171
; __device__ __forceinline__ float bf_lo(unsigned w) { return __uint_as_float(w << 16); }
; __device__ __forceinline__ float bf_hi(unsigned w) { return __uint_as_float(w & 0xffff0000u); }
;     static __device__ __forceinline__ float ex(float x) { return __expf(fminf(-x, 60.f)); }
;     __device__ __forceinline__ void mid(f32x4 (&acc)[2][2][4][2], const Unit& u, int wr, int wc, int fr, int fq) const {
;     ...
;                 int off = (ai * HALF + m * 16) * R_LD; asm volatile("" : "+s"(off) :: "memory");
;                 const bf16_t* rp = rp0 + off;
; #pragma unroll
;                 for (int bj = 0; bj < 2; ++bj) {
;                     const u32x4 ga = *(const u32x4*)(rp + 6144 + bj * HALF), gc = *(const u32x4*)(rp + 8192 + bj * HALF);
;                     f32x4 r0, r1;
;                     r0[0] = (1.0f + ex(bf_lo(gc.x))) * __builtin_amdgcn_rcpf(1.0f + ex(bf_lo(ga.x))); r0[1] = (1.0f + ex(bf_hi(gc.x))) * __builtin_amdgcn_rcpf(1.0f + ex(bf_hi(ga.x)));
;                     r0[2] = (1.0f + ex(bf_lo(gc.y))) * __builtin_amdgcn_rcpf(1.0f + ex(bf_lo(ga.y))); r0[3] = (1.0f + ex(bf_hi(gc.y))) * __builtin_amdgcn_rcpf(1.0f + ex(bf_hi(ga.y)));
;                     r1[0] = (1.0f + ex(bf_lo(gc.z))) * __builtin_amdgcn_rcpf(1.0f + ex(bf_lo(ga.z))); r1[1] = (1.0f + ex(bf_hi(gc.z))) * __builtin_amdgcn_rcpf(1.0f + ex(bf_hi(ga.z)));
;                     r1[2] = (1.0f + ex(bf_lo(gc.w))) * __builtin_amdgcn_rcpf(1.0f + ex(bf_lo(ga.w))); r1[3] = (1.0f + ex(bf_hi(gc.w))) * __builtin_amdgcn_rcpf(1.0f + ex(bf_hi(ga.w)));
;                     acc[ai][bj][m][0] *= r0; acc[ai][bj][m][1] *= r1; }
	v_rcp_f32_e32 v171, v1
	v_pk_add_f32 v[166:167], v[166:167], 1.0 op_sel_hi:[1,0]
	v_pk_add_f32 v[2:3], v[2:3], 1.0 op_sel_hi:[1,0]
	v_lshlrev_b32_e32 v1, 16, v168
	v_pk_mul_f32 v[2:3], v[2:3], v[160:161]
	v_pk_mul_f32 v[160:161], v[166:167], v[170:171]
	v_lshlrev_b32_e32 v166, 16, v172
	v_max_f32_e64 v166, -v166, -v166
	v_min_f32_e32 v166, 0x42700000, v166
	v_mul_f32_e32 v166, 0x3fb8aa3b, v166
	v_exp_f32_e32 v167, v166
	v_max_f32_e64 v1, -v1, -v1
	v_min_f32_e32 v1, 0x42700000, v1
	v_mul_f32_e32 v1, 0x3fb8aa3b, v1
	v_exp_f32_e32 v166, v1
	v_add_f32_e32 v1, 1.0, v167
	v_and_b32_e32 v167, 0xffff0000, v172
	v_max_f32_e64 v167, -v167, -v167
	v_min_f32_e32 v167, 0x42700000, v167
	v_mul_f32_e32 v167, 0x3fb8aa3b, v167
	v_rcp_f32_e32 v170, v1
	v_and_b32_e32 v1, 0xffff0000, v168
	v_exp_f32_e32 v168, v167
	v_max_f32_e64 v1, -v1, -v1
	v_min_f32_e32 v1, 0x42700000, v1
	v_mul_f32_e32 v1, 0x3fb8aa3b, v1
	v_exp_f32_e32 v167, v1
	v_add_f32_e32 v1, 1.0, v168
	v_lshlrev_b32_e32 v168, 16, v173
	v_max_f32_e64 v168, -v168, -v168
	v_min_f32_e32 v168, 0x42700000, v168
	v_mul_f32_e32 v168, 0x3fb8aa3b, v168
	v_rcp_f32_e32 v171, v1
	v_lshlrev_b32_e32 v1, 16, v169
	v_exp_f32_e32 v172, v168
	v_max_f32_e64 v1, -v1, -v1
	v_min_f32_e32 v1, 0x42700000, v1
	v_mul_f32_e32 v1, 0x3fb8aa3b, v1
	v_exp_f32_e32 v168, v1
	v_add_f32_e32 v1, 1.0, v172
	v_and_b32_e32 v172, 0xffff0000, v173
	v_max_f32_e64 v172, -v172, -v172
	v_min_f32_e32 v172, 0x42700000, v172
	v_mul_f32_e32 v172, 0x3fb8aa3b, v172
	v_exp_f32_e32 v173, v172
	v_pk_mul_f32 v[48:49], v[48:49], v[2:3]
	v_lshlrev_b32_e32 v2, 16, v178
	v_max_f32_e64 v2, -v2, -v2
	v_min_f32_e32 v2, 0x42700000, v2
	v_rcp_f32_e32 v172, v1
	v_add_f32_e32 v1, 1.0, v173
	v_mul_f32_e32 v2, 0x3fb8aa3b, v2
	v_rcp_f32_e32 v173, v1
	v_lshlrev_b32_e32 v1, 16, v174
	v_exp_f32_e32 v3, v2
	v_max_f32_e64 v1, -v1, -v1
	v_min_f32_e32 v1, 0x42700000, v1
	v_and_b32_e32 v169, 0xffff0000, v169
	v_mul_f32_e32 v1, 0x3fb8aa3b, v1
	v_max_f32_e64 v169, -v169, -v169
	v_exp_f32_e32 v2, v1
	v_add_f32_e32 v1, 1.0, v3
	v_and_b32_e32 v3, 0xffff0000, v178
	v_min_f32_e32 v169, 0x42700000, v169
	v_max_f32_e64 v3, -v3, -v3
	v_mul_f32_e32 v169, 0x3fb8aa3b, v169
	v_min_f32_e32 v3, 0x42700000, v3
	v_exp_f32_e32 v169, v169
	v_pk_add_f32 v[166:167], v[166:167], 1.0 op_sel_hi:[1,0]
	v_mul_f32_e32 v3, 0x3fb8aa3b, v3
	v_pk_mul_f32 v[166:167], v[166:167], v[170:171]
	v_pk_mul_f32 v[50:51], v[50:51], v[160:161]
	v_rcp_f32_e32 v160, v1
	v_and_b32_e32 v1, 0xffff0000, v174
	v_exp_f32_e32 v161, v3
	v_pk_mul_f32 v[44:45], v[44:45], v[166:167]
	v_max_f32_e64 v1, -v1, -v1
	v_lshlrev_b32_e32 v166, 16, v179
	v_min_f32_e32 v1, 0x42700000, v1
	v_max_f32_e64 v166, -v166, -v166
	v_pk_add_f32 v[168:169], v[168:169], 1.0 op_sel_hi:[1,0]
	v_mul_f32_e32 v1, 0x3fb8aa3b, v1
	v_min_f32_e32 v166, 0x42700000, v166
	v_pk_mul_f32 v[168:169], v[168:169], v[172:173]
	v_exp_f32_e32 v3, v1
	v_add_f32_e32 v1, 1.0, v161
	v_mul_f32_e32 v166, 0x3fb8aa3b, v166
	v_pk_mul_f32 v[46:47], v[46:47], v[168:169]
	v_rcp_f32_e32 v161, v1
	v_lshlrev_b32_e32 v1, 16, v175
	v_exp_f32_e32 v167, v166
	v_and_b32_e32 v168, 0xffff0000, v179
	v_max_f32_e64 v1, -v1, -v1
	v_max_f32_e64 v168, -v168, -v168
	v_min_f32_e32 v1, 0x42700000, v1
	v_min_f32_e32 v168, 0x42700000, v168
	v_mul_f32_e32 v1, 0x3fb8aa3b, v1
	v_mul_f32_e32 v168, 0x3fb8aa3b, v168
	v_exp_f32_e32 v166, v1
	v_add_f32_e32 v1, 1.0, v167
	v_and_b32_e32 v167, 0xffff0000, v175
	v_exp_f32_e32 v169, v168
	v_max_f32_e64 v167, -v167, -v167
	v_min_f32_e32 v167, 0x42700000, v167
	v_mul_f32_e32 v167, 0x3fb8aa3b, v167
	v_exp_f32_e32 v167, v167
	v_rcp_f32_e32 v168, v1
	v_add_f32_e32 v1, 1.0, v169
	v_rcp_f32_e32 v169, v1
	v_pk_add_f32 v[166:167], v[166:167], 1.0 op_sel_hi:[1,0]
	v_pk_add_f32 v[2:3], v[2:3], 1.0 op_sel_hi:[1,0]
	v_lshlrev_b32_e32 v1, 16, v176
	v_pk_mul_f32 v[2:3], v[2:3], v[160:161]
	v_pk_mul_f32 v[160:161], v[166:167], v[168:169]
	v_lshlrev_b32_e32 v166, 16, v180
	v_max_f32_e64 v166, -v166, -v166
	v_min_f32_e32 v166, 0x42700000, v166
	v_mul_f32_e32 v166, 0x3fb8aa3b, v166
	v_exp_f32_e32 v167, v166
	v_max_f32_e64 v1, -v1, -v1
	v_min_f32_e32 v1, 0x42700000, v1
	v_mul_f32_e32 v1, 0x3fb8aa3b, v1
	v_exp_f32_e32 v166, v1
	v_add_f32_e32 v1, 1.0, v167
	v_and_b32_e32 v167, 0xffff0000, v180
	v_max_f32_e64 v167, -v167, -v167
	v_min_f32_e32 v167, 0x42700000, v167
	v_mul_f32_e32 v167, 0x3fb8aa3b, v167
	v_rcp_f32_e32 v168, v1
	v_and_b32_e32 v1, 0xffff0000, v176
	v_exp_f32_e32 v169, v167
	v_max_f32_e64 v1, -v1, -v1
	v_lshlrev_b32_e32 v170, 16, v181
	v_min_f32_e32 v1, 0x42700000, v1
	v_max_f32_e64 v170, -v170, -v170
	v_mul_f32_e32 v1, 0x3fb8aa3b, v1
	v_min_f32_e32 v170, 0x42700000, v170
	v_exp_f32_e32 v167, v1
	v_add_f32_e32 v1, 1.0, v169
	v_mul_f32_e32 v170, 0x3fb8aa3b, v170
	v_rcp_f32_e32 v169, v1
	v_lshlrev_b32_e32 v1, 16, v177
	v_exp_f32_e32 v171, v170
	v_and_b32_e32 v172, 0xffff0000, v181
	v_max_f32_e64 v1, -v1, -v1
	v_max_f32_e64 v172, -v172, -v172
	v_min_f32_e32 v1, 0x42700000, v1
	v_min_f32_e32 v172, 0x42700000, v172
	v_mul_f32_e32 v1, 0x3fb8aa3b, v1
	v_mul_f32_e32 v172, 0x3fb8aa3b, v172
	v_exp_f32_e32 v170, v1
	v_add_f32_e32 v1, 1.0, v171
	v_and_b32_e32 v171, 0xffff0000, v177
	v_exp_f32_e32 v173, v172
	v_max_f32_e64 v171, -v171, -v171
	v_min_f32_e32 v171, 0x42700000, v171
	v_mul_f32_e32 v171, 0x3fb8aa3b, v171
	v_exp_f32_e32 v171, v171
	v_rcp_f32_e32 v172, v1
	v_add_f32_e32 v1, 1.0, v173
	v_rcp_f32_e32 v173, v1
	v_pk_add_f32 v[170:171], v[170:171], 1.0 op_sel_hi:[1,0]
	v_pk_add_f32 v[166:167], v[166:167], 1.0 op_sel_hi:[1,0]
	v_pk_mul_f32 v[42:43], v[42:43], v[160:161]
	v_pk_mul_f32 v[166:167], v[166:167], v[168:169]
	v_pk_mul_f32 v[168:169], v[170:171], v[172:173]
	v_pk_mul_f32 v[40:41], v[40:41], v[2:3]
	v_pk_mul_f32 v[38:39], v[38:39], v[168:169]
	v_pk_mul_f32 v[36:37], v[36:37], v[166:167]
	s_nop 0
	s_ashr_i32 s5, s4, 31
	v_lshl_add_u64 v[2:3], s[4:5], 1, v[154:155]
	v_add_co_u32_e32 v160, vcc, s63, v2
	s_mov_b32 s4, 0x1b8000
	s_nop 0
	v_addc_co_u32_e32 v161, vcc, 0, v3, vcc
	global_load_dwordx4 v[166:169], v[160:161], off
	global_load_dwordx4 v[170:173], v[160:161], off offset:-4096
	v_add_co_u32_e32 v2, vcc, s70, v2
	global_load_dwordx4 v[174:177], v[160:161], off offset:256
	s_nop 0
	v_addc_co_u32_e32 v3, vcc, 0, v3, vcc
	global_load_dwordx4 v[178:181], v[2:3], off offset:256
	s_waitcnt vmcnt(0)
; __device__ __forceinline__ float bf_lo(unsigned w) { return __uint_as_float(w << 16); }
; __device__ __forceinline__ float bf_hi(unsigned w) { return __uint_as_float(w & 0xffff0000u); }
;     static __device__ __forceinline__ float ex(float x) { return __expf(fminf(-x, 60.f)); }
;     __device__ __forceinline__ void mid(f32x4 (&acc)[2][2][4][2], const Unit& u, int wr, int wc, int fr, int fq) const {
;     ...
;                 int off = (ai * HALF + m * 16) * R_LD; asm volatile("" : "+s"(off) :: "memory");
;                 const bf16_t* rp = rp0 + off;
; #pragma unroll
;                 for (int bj = 0; bj < 2; ++bj) {
;                     const u32x4 ga = *(const u32x4*)(rp + 6144 + bj * HALF), gc = *(const u32x4*)(rp + 8192 + bj * HALF);
;                     f32x4 r0, r1;
;                     r0[0] = (1.0f + ex(bf_lo(gc.x))) * __builtin_amdgcn_rcpf(1.0f + ex(bf_lo(ga.x))); r0[1] = (1.0f + ex(bf_hi(gc.x))) * __builtin_amdgcn_rcpf(1.0f + ex(bf_hi(ga.x)));
;                     r0[2] = (1.0f + ex(bf_lo(gc.y))) * __builtin_amdgcn_rcpf(1.0f + ex(bf_lo(ga.y))); r0[3] = (1.0f + ex(bf_hi(gc.y))) * __builtin_amdgcn_rcpf(1.0f + ex(bf_hi(ga.y)));
;                     r1[0] = (1.0f + ex(bf_lo(gc.z))) * __builtin_amdgcn_rcpf(1.0f + ex(bf_lo(ga.z))); r1[1] = (1.0f + ex(bf_hi(gc.z))) * __builtin_amdgcn_rcpf(1.0f + ex(bf_hi(ga.z)));
;                     r1[2] = (1.0f + ex(bf_lo(gc.w))) * __builtin_amdgcn_rcpf(1.0f + ex(bf_lo(ga.w))); r1[3] = (1.0f + ex(bf_hi(gc.w))) * __builtin_amdgcn_rcpf(1.0f + ex(bf_hi(ga.w)));
;                     acc[ai][bj][m][0] *= r0; acc[ai][bj][m][1] *= r1; }
	v_lshlrev_b32_e32 v1, 16, v166
	v_lshlrev_b32_e32 v2, 16, v170
	v_max_f32_e64 v2, -v2, -v2
	v_min_f32_e32 v2, 0x42700000, v2
	v_mul_f32_e32 v2, 0x3fb8aa3b, v2
	v_exp_f32_e32 v3, v2
	v_max_f32_e64 v1, -v1, -v1
	v_min_f32_e32 v1, 0x42700000, v1
	v_mul_f32_e32 v1, 0x3fb8aa3b, v1
	v_exp_f32_e32 v2, v1
	v_add_f32_e32 v1, 1.0, v3
	v_and_b32_e32 v3, 0xffff0000, v170
	v_max_f32_e64 v3, -v3, -v3
	v_min_f32_e32 v3, 0x42700000, v3
	v_mul_f32_e32 v3, 0x3fb8aa3b, v3
	v_rcp_f32_e32 v160, v1
	v_and_b32_e32 v1, 0xffff0000, v166
	v_exp_f32_e32 v161, v3
	v_max_f32_e64 v1, -v1, -v1
	v_lshlrev_b32_e32 v166, 16, v171
	v_min_f32_e32 v1, 0x42700000, v1
	v_max_f32_e64 v166, -v166, -v166
	v_mul_f32_e32 v1, 0x3fb8aa3b, v1
	v_min_f32_e32 v166, 0x42700000, v166
	v_exp_f32_e32 v3, v1
	v_add_f32_e32 v1, 1.0, v161
	v_mul_f32_e32 v166, 0x3fb8aa3b, v166
	v_rcp_f32_e32 v161, v1
	v_lshlrev_b32_e32 v1, 16, v167
	v_exp_f32_e32 v170, v166
	v_max_f32_e64 v1, -v1, -v1
	v_min_f32_e32 v1, 0x42700000, v1
	v_mul_f32_e32 v1, 0x3fb8aa3b, v1
	v_exp_f32_e32 v166, v1
	v_add_f32_e32 v1, 1.0, v170
	v_and_b32_e32 v170, 0xffff0000, v171
	v_max_f32_e64 v170, -v170, -v170
	v_min_f32_e32 v170, 0x42700000, v170
	v_mul_f32_e32 v170, 0x3fb8aa3b, v170
	v_and_b32_e32 v167, 0xffff0000, v167
	v_exp_f32_e32 v171, v170
	v_max_f32_e64 v167, -v167, -v167
	v_min_f32_e32 v167, 0x42700000, v167
	v_mul_f32_e32 v167, 0x3fb8aa3b, v167
	v_exp_f32_e32 v167, v167
	v_rcp_f32_e32 v170, v1
	v_add_f32_e32 v1, 1.0, v171
	v_rcp_f32_e32 v171, v1
	v_pk_add_f32 v[166:167], v[166:167], 1.0 op_sel_hi:[1,0]
	v_pk_add_f32 v[2:3], v[2:3], 1.0 op_sel_hi:[1,0]
	v_lshlrev_b32_e32 v1, 16, v168
	v_pk_mul_f32 v[2:3], v[2:3], v[160:161]
	v_pk_mul_f32 v[160:161], v[166:167], v[170:171]
	v_lshlrev_b32_e32 v166, 16, v172
	v_max_f32_e64 v166, -v166, -v166
	v_min_f32_e32 v166, 0x42700000, v166
	v_mul_f32_e32 v166, 0x3fb8aa3b, v166
	v_exp_f32_e32 v167, v166
	v_max_f32_e64 v1, -v1, -v1
	v_min_f32_e32 v1, 0x42700000, v1
	v_mul_f32_e32 v1, 0x3fb8aa3b, v1
	v_exp_f32_e32 v166, v1
	v_add_f32_e32 v1, 1.0, v167
	v_and_b32_e32 v167, 0xffff0000, v172
	v_max_f32_e64 v167, -v167, -v167
	v_min_f32_e32 v167, 0x42700000, v167
	v_mul_f32_e32 v167, 0x3fb8aa3b, v167
	v_rcp_f32_e32 v170, v1
	v_and_b32_e32 v1, 0xffff0000, v168
	v_exp_f32_e32 v168, v167
	v_max_f32_e64 v1, -v1, -v1
	v_min_f32_e32 v1, 0x42700000, v1
	v_mul_f32_e32 v1, 0x3fb8aa3b, v1
	v_exp_f32_e32 v167, v1
	v_add_f32_e32 v1, 1.0, v168
	v_lshlrev_b32_e32 v168, 16, v173
	v_max_f32_e64 v168, -v168, -v168
	v_min_f32_e32 v168, 0x42700000, v168
	v_mul_f32_e32 v168, 0x3fb8aa3b, v168
	v_rcp_f32_e32 v171, v1
	v_lshlrev_b32_e32 v1, 16, v169
	v_exp_f32_e32 v172, v168
	v_max_f32_e64 v1, -v1, -v1
	v_min_f32_e32 v1, 0x42700000, v1
	v_mul_f32_e32 v1, 0x3fb8aa3b, v1
	v_exp_f32_e32 v168, v1
	v_add_f32_e32 v1, 1.0, v172
	v_and_b32_e32 v172, 0xffff0000, v173
	v_max_f32_e64 v172, -v172, -v172
	v_min_f32_e32 v172, 0x42700000, v172
	v_mul_f32_e32 v172, 0x3fb8aa3b, v172
	v_exp_f32_e32 v173, v172
	v_pk_mul_f32 v[32:33], v[32:33], v[2:3]
	v_lshlrev_b32_e32 v2, 16, v178
	v_max_f32_e64 v2, -v2, -v2
	v_min_f32_e32 v2, 0x42700000, v2
	v_rcp_f32_e32 v172, v1
	v_add_f32_e32 v1, 1.0, v173
	v_mul_f32_e32 v2, 0x3fb8aa3b, v2
	v_rcp_f32_e32 v173, v1
	v_lshlrev_b32_e32 v1, 16, v174
	v_exp_f32_e32 v3, v2
	v_max_f32_e64 v1, -v1, -v1
	v_min_f32_e32 v1, 0x42700000, v1
	v_and_b32_e32 v169, 0xffff0000, v169
	v_mul_f32_e32 v1, 0x3fb8aa3b, v1
	v_max_f32_e64 v169, -v169, -v169
	v_exp_f32_e32 v2, v1
	v_add_f32_e32 v1, 1.0, v3
	v_and_b32_e32 v3, 0xffff0000, v178
	v_min_f32_e32 v169, 0x42700000, v169
	v_max_f32_e64 v3, -v3, -v3
	v_mul_f32_e32 v169, 0x3fb8aa3b, v169
	v_min_f32_e32 v3, 0x42700000, v3
	v_exp_f32_e32 v169, v169
	v_pk_add_f32 v[166:167], v[166:167], 1.0 op_sel_hi:[1,0]
	v_mul_f32_e32 v3, 0x3fb8aa3b, v3
	v_pk_mul_f32 v[166:167], v[166:167], v[170:171]
	v_pk_mul_f32 v[34:35], v[34:35], v[160:161]
	v_rcp_f32_e32 v160, v1
	v_and_b32_e32 v1, 0xffff0000, v174
	v_exp_f32_e32 v161, v3
	v_pk_mul_f32 v[28:29], v[28:29], v[166:167]
	v_max_f32_e64 v1, -v1, -v1
	v_lshlrev_b32_e32 v166, 16, v179
	v_min_f32_e32 v1, 0x42700000, v1
	v_max_f32_e64 v166, -v166, -v166
	v_pk_add_f32 v[168:169], v[168:169], 1.0 op_sel_hi:[1,0]
	v_mul_f32_e32 v1, 0x3fb8aa3b, v1
	v_min_f32_e32 v166, 0x42700000, v166
	v_pk_mul_f32 v[168:169], v[168:169], v[172:173]
	v_exp_f32_e32 v3, v1
	v_add_f32_e32 v1, 1.0, v161
	v_mul_f32_e32 v166, 0x3fb8aa3b, v166
	v_pk_mul_f32 v[30:31], v[30:31], v[168:169]
	v_rcp_f32_e32 v161, v1
	v_lshlrev_b32_e32 v1, 16, v175
	v_exp_f32_e32 v167, v166
	v_and_b32_e32 v168, 0xffff0000, v179
	v_max_f32_e64 v1, -v1, -v1
	v_max_f32_e64 v168, -v168, -v168
	v_min_f32_e32 v1, 0x42700000, v1
	v_min_f32_e32 v168, 0x42700000, v168
	v_mul_f32_e32 v1, 0x3fb8aa3b, v1
	v_mul_f32_e32 v168, 0x3fb8aa3b, v168
	v_exp_f32_e32 v166, v1
	v_add_f32_e32 v1, 1.0, v167
	v_and_b32_e32 v167, 0xffff0000, v175
	v_exp_f32_e32 v169, v168
	v_max_f32_e64 v167, -v167, -v167
	v_min_f32_e32 v167, 0x42700000, v167
	v_mul_f32_e32 v167, 0x3fb8aa3b, v167
	v_exp_f32_e32 v167, v167
	v_rcp_f32_e32 v168, v1
	v_add_f32_e32 v1, 1.0, v169
	v_rcp_f32_e32 v169, v1
	v_pk_add_f32 v[166:167], v[166:167], 1.0 op_sel_hi:[1,0]
	v_pk_add_f32 v[2:3], v[2:3], 1.0 op_sel_hi:[1,0]
	v_lshlrev_b32_e32 v1, 16, v176
	v_pk_mul_f32 v[2:3], v[2:3], v[160:161]
	v_pk_mul_f32 v[160:161], v[166:167], v[168:169]
	v_lshlrev_b32_e32 v166, 16, v180
	v_max_f32_e64 v166, -v166, -v166
	v_min_f32_e32 v166, 0x42700000, v166
	v_mul_f32_e32 v166, 0x3fb8aa3b, v166
	v_exp_f32_e32 v167, v166
	v_max_f32_e64 v1, -v1, -v1
	v_min_f32_e32 v1, 0x42700000, v1
	v_mul_f32_e32 v1, 0x3fb8aa3b, v1
	v_exp_f32_e32 v166, v1
	v_add_f32_e32 v1, 1.0, v167
; __device__ __forceinline__ float bf_lo(unsigned w) { return __uint_as_float(w << 16); }
; __device__ __forceinline__ float bf_hi(unsigned w) { return __uint_as_float(w & 0xffff0000u); }
;     static __device__ __forceinline__ float ex(float x) { return __expf(fminf(-x, 60.f)); }
;     __device__ __forceinline__ void mid(f32x4 (&acc)[2][2][4][2], const Unit& u, int wr, int wc, int fr, int fq) const {
;     ...
;                 int off = (ai * HALF + m * 16) * R_LD; asm volatile("" : "+s"(off) :: "memory");
;                 const bf16_t* rp = rp0 + off;
; #pragma unroll
;                 for (int bj = 0; bj < 2; ++bj) {
;                     const u32x4 ga = *(const u32x4*)(rp + 6144 + bj * HALF), gc = *(const u32x4*)(rp + 8192 + bj * HALF);
;                     f32x4 r0, r1;
;                     r0[0] = (1.0f + ex(bf_lo(gc.x))) * __builtin_amdgcn_rcpf(1.0f + ex(bf_lo(ga.x))); r0[1] = (1.0f + ex(bf_hi(gc.x))) * __builtin_amdgcn_rcpf(1.0f + ex(bf_hi(ga.x)));
;                     r0[2] = (1.0f + ex(bf_lo(gc.y))) * __builtin_amdgcn_rcpf(1.0f + ex(bf_lo(ga.y))); r0[3] = (1.0f + ex(bf_hi(gc.y))) * __builtin_amdgcn_rcpf(1.0f + ex(bf_hi(ga.y)));
;                     r1[0] = (1.0f + ex(bf_lo(gc.z))) * __builtin_amdgcn_rcpf(1.0f + ex(bf_lo(ga.z))); r1[1] = (1.0f + ex(bf_hi(gc.z))) * __builtin_amdgcn_rcpf(1.0f + ex(bf_hi(ga.z)));
;                     r1[2] = (1.0f + ex(bf_lo(gc.w))) * __builtin_amdgcn_rcpf(1.0f + ex(bf_lo(ga.w))); r1[3] = (1.0f + ex(bf_hi(gc.w))) * __builtin_amdgcn_rcpf(1.0f + ex(bf_hi(ga.w)));
;                     acc[ai][bj][m][0] *= r0; acc[ai][bj][m][1] *= r1; }
	v_and_b32_e32 v167, 0xffff0000, v180
	v_max_f32_e64 v167, -v167, -v167
	v_min_f32_e32 v167, 0x42700000, v167
	v_mul_f32_e32 v167, 0x3fb8aa3b, v167
	v_rcp_f32_e32 v168, v1
	v_and_b32_e32 v1, 0xffff0000, v176
	v_exp_f32_e32 v169, v167
	v_max_f32_e64 v1, -v1, -v1
	v_lshlrev_b32_e32 v170, 16, v181
	v_min_f32_e32 v1, 0x42700000, v1
	v_max_f32_e64 v170, -v170, -v170
	v_mul_f32_e32 v1, 0x3fb8aa3b, v1
	v_min_f32_e32 v170, 0x42700000, v170
	v_exp_f32_e32 v167, v1
	v_add_f32_e32 v1, 1.0, v169
	v_mul_f32_e32 v170, 0x3fb8aa3b, v170
	v_rcp_f32_e32 v169, v1
	v_lshlrev_b32_e32 v1, 16, v177
	v_exp_f32_e32 v171, v170
	v_and_b32_e32 v172, 0xffff0000, v181
	v_max_f32_e64 v1, -v1, -v1
	v_max_f32_e64 v172, -v172, -v172
	v_min_f32_e32 v1, 0x42700000, v1
	v_min_f32_e32 v172, 0x42700000, v172
	v_mul_f32_e32 v1, 0x3fb8aa3b, v1
	v_mul_f32_e32 v172, 0x3fb8aa3b, v172
	v_exp_f32_e32 v170, v1
	v_add_f32_e32 v1, 1.0, v171
	v_and_b32_e32 v171, 0xffff0000, v177
	v_exp_f32_e32 v173, v172
	v_max_f32_e64 v171, -v171, -v171
	v_min_f32_e32 v171, 0x42700000, v171
	v_mul_f32_e32 v171, 0x3fb8aa3b, v171
	v_exp_f32_e32 v171, v171
	v_rcp_f32_e32 v172, v1
	v_add_f32_e32 v1, 1.0, v173
	v_rcp_f32_e32 v173, v1
	v_pk_add_f32 v[170:171], v[170:171], 1.0 op_sel_hi:[1,0]
	v_pk_add_f32 v[166:167], v[166:167], 1.0 op_sel_hi:[1,0]
	v_pk_mul_f32 v[26:27], v[26:27], v[160:161]
	v_pk_mul_f32 v[166:167], v[166:167], v[168:169]
	v_pk_mul_f32 v[168:169], v[170:171], v[172:173]
	v_pk_mul_f32 v[24:25], v[24:25], v[2:3]
	v_pk_mul_f32 v[22:23], v[22:23], v[168:169]
	v_pk_mul_f32 v[20:21], v[20:21], v[166:167]
	s_nop 0
	s_ashr_i32 s5, s4, 31
	v_lshl_add_u64 v[2:3], s[4:5], 1, v[154:155]
	v_add_co_u32_e32 v160, vcc, s63, v2
	s_mov_b32 s4, 32
	s_nop 0
	v_addc_co_u32_e32 v161, vcc, 0, v3, vcc
	global_load_dwordx4 v[166:169], v[160:161], off
	global_load_dwordx4 v[170:173], v[160:161], off offset:-4096
	v_add_co_u32_e32 v2, vcc, s70, v2
	global_load_dwordx4 v[174:177], v[160:161], off offset:256
	s_nop 0
	v_addc_co_u32_e32 v3, vcc, 0, v3, vcc
	global_load_dwordx4 v[178:181], v[2:3], off offset:256
	s_waitcnt vmcnt(0)
	v_lshlrev_b32_e32 v1, 16, v166
	v_lshlrev_b32_e32 v2, 16, v170
	v_max_f32_e64 v2, -v2, -v2
	v_min_f32_e32 v2, 0x42700000, v2
	v_mul_f32_e32 v2, 0x3fb8aa3b, v2
	v_exp_f32_e32 v3, v2
	v_max_f32_e64 v1, -v1, -v1
	v_min_f32_e32 v1, 0x42700000, v1
	v_mul_f32_e32 v1, 0x3fb8aa3b, v1
	v_exp_f32_e32 v2, v1
	v_add_f32_e32 v1, 1.0, v3
	v_and_b32_e32 v3, 0xffff0000, v170
	v_max_f32_e64 v3, -v3, -v3
	v_min_f32_e32 v3, 0x42700000, v3
	v_mul_f32_e32 v3, 0x3fb8aa3b, v3
	v_rcp_f32_e32 v160, v1
	v_and_b32_e32 v1, 0xffff0000, v166
	v_exp_f32_e32 v161, v3
	v_max_f32_e64 v1, -v1, -v1
	v_lshlrev_b32_e32 v166, 16, v171
	v_min_f32_e32 v1, 0x42700000, v1
	v_max_f32_e64 v166, -v166, -v166
	v_mul_f32_e32 v1, 0x3fb8aa3b, v1
	v_min_f32_e32 v166, 0x42700000, v166
	v_exp_f32_e32 v3, v1
	v_add_f32_e32 v1, 1.0, v161
	v_mul_f32_e32 v166, 0x3fb8aa3b, v166
	v_rcp_f32_e32 v161, v1
	v_lshlrev_b32_e32 v1, 16, v167
	v_exp_f32_e32 v170, v166
	v_max_f32_e64 v1, -v1, -v1
	v_min_f32_e32 v1, 0x42700000, v1
	v_mul_f32_e32 v1, 0x3fb8aa3b, v1
	v_exp_f32_e32 v166, v1
	v_add_f32_e32 v1, 1.0, v170
	v_and_b32_e32 v170, 0xffff0000, v171
	v_max_f32_e64 v170, -v170, -v170
	v_min_f32_e32 v170, 0x42700000, v170
	v_mul_f32_e32 v170, 0x3fb8aa3b, v170
	v_and_b32_e32 v167, 0xffff0000, v167
	v_exp_f32_e32 v171, v170
	v_max_f32_e64 v167, -v167, -v167
	v_min_f32_e32 v167, 0x42700000, v167
	v_mul_f32_e32 v167, 0x3fb8aa3b, v167
	v_exp_f32_e32 v167, v167
	v_rcp_f32_e32 v170, v1
	v_add_f32_e32 v1, 1.0, v171
	v_rcp_f32_e32 v171, v1
	v_pk_add_f32 v[166:167], v[166:167], 1.0 op_sel_hi:[1,0]
	v_pk_add_f32 v[2:3], v[2:3], 1.0 op_sel_hi:[1,0]
	v_lshlrev_b32_e32 v1, 16, v168
	v_pk_mul_f32 v[2:3], v[2:3], v[160:161]
	v_pk_mul_f32 v[160:161], v[166:167], v[170:171]
	v_lshlrev_b32_e32 v166, 16, v172
	v_max_f32_e64 v166, -v166, -v166
	v_min_f32_e32 v166, 0x42700000, v166
	v_mul_f32_e32 v166, 0x3fb8aa3b, v166
	v_exp_f32_e32 v167, v166
	v_max_f32_e64 v1, -v1, -v1
	v_min_f32_e32 v1, 0x42700000, v1
	v_mul_f32_e32 v1, 0x3fb8aa3b, v1
	v_exp_f32_e32 v166, v1
	v_add_f32_e32 v1, 1.0, v167
	v_and_b32_e32 v167, 0xffff0000, v172
	v_max_f32_e64 v167, -v167, -v167
	v_min_f32_e32 v167, 0x42700000, v167
	v_mul_f32_e32 v167, 0x3fb8aa3b, v167
	v_rcp_f32_e32 v170, v1
	v_and_b32_e32 v1, 0xffff0000, v168
	v_exp_f32_e32 v168, v167
	v_max_f32_e64 v1, -v1, -v1
	v_min_f32_e32 v1, 0x42700000, v1
	v_mul_f32_e32 v1, 0x3fb8aa3b, v1
	v_exp_f32_e32 v167, v1
	v_add_f32_e32 v1, 1.0, v168
	v_lshlrev_b32_e32 v168, 16, v173
	v_max_f32_e64 v168, -v168, -v168
	v_min_f32_e32 v168, 0x42700000, v168
	v_mul_f32_e32 v168, 0x3fb8aa3b, v168
; __device__ __forceinline__ float bf_lo(unsigned w) { return __uint_as_float(w << 16); }
; __device__ __forceinline__ float bf_hi(unsigned w) { return __uint_as_float(w & 0xffff0000u); }
;     static __device__ __forceinline__ float ex(float x) { return __expf(fminf(-x, 60.f)); }
;     __device__ __forceinline__ void mid(f32x4 (&acc)[2][2][4][2], const Unit& u, int wr, int wc, int fr, int fq) const {
;     ...
;                 int off = (ai * HALF + m * 16) * R_LD; asm volatile("" : "+s"(off) :: "memory");
;                 const bf16_t* rp = rp0 + off;
; #pragma unroll
;                 for (int bj = 0; bj < 2; ++bj) {
;                     const u32x4 ga = *(const u32x4*)(rp + 6144 + bj * HALF), gc = *(const u32x4*)(rp + 8192 + bj * HALF);
;                     f32x4 r0, r1;
;                     r0[0] = (1.0f + ex(bf_lo(gc.x))) * __builtin_amdgcn_rcpf(1.0f + ex(bf_lo(ga.x))); r0[1] = (1.0f + ex(bf_hi(gc.x))) * __builtin_amdgcn_rcpf(1.0f + ex(bf_hi(ga.x)));
;                     r0[2] = (1.0f + ex(bf_lo(gc.y))) * __builtin_amdgcn_rcpf(1.0f + ex(bf_lo(ga.y))); r0[3] = (1.0f + ex(bf_hi(gc.y))) * __builtin_amdgcn_rcpf(1.0f + ex(bf_hi(ga.y)));
;                     r1[0] = (1.0f + ex(bf_lo(gc.z))) * __builtin_amdgcn_rcpf(1.0f + ex(bf_lo(ga.z))); r1[1] = (1.0f + ex(bf_hi(gc.z))) * __builtin_amdgcn_rcpf(1.0f + ex(bf_hi(ga.z)));
;                     r1[2] = (1.0f + ex(bf_lo(gc.w))) * __builtin_amdgcn_rcpf(1.0f + ex(bf_lo(ga.w))); r1[3] = (1.0f + ex(bf_hi(gc.w))) * __builtin_amdgcn_rcpf(1.0f + ex(bf_hi(ga.w)));
;                     acc[ai][bj][m][0] *= r0; acc[ai][bj][m][1] *= r1; }
	v_rcp_f32_e32 v171, v1
	v_lshlrev_b32_e32 v1, 16, v169
	v_exp_f32_e32 v172, v168
	v_max_f32_e64 v1, -v1, -v1
	v_min_f32_e32 v1, 0x42700000, v1
	v_mul_f32_e32 v1, 0x3fb8aa3b, v1
	v_exp_f32_e32 v168, v1
	v_add_f32_e32 v1, 1.0, v172
	v_and_b32_e32 v172, 0xffff0000, v173
	v_max_f32_e64 v172, -v172, -v172
	v_min_f32_e32 v172, 0x42700000, v172
	v_mul_f32_e32 v172, 0x3fb8aa3b, v172
	v_exp_f32_e32 v173, v172
	v_pk_mul_f32 v[16:17], v[16:17], v[2:3]
	v_lshlrev_b32_e32 v2, 16, v178
	v_max_f32_e64 v2, -v2, -v2
	v_min_f32_e32 v2, 0x42700000, v2
	v_rcp_f32_e32 v172, v1
	v_add_f32_e32 v1, 1.0, v173
	v_mul_f32_e32 v2, 0x3fb8aa3b, v2
	v_rcp_f32_e32 v173, v1
	v_lshlrev_b32_e32 v1, 16, v174
	v_exp_f32_e32 v3, v2
	v_max_f32_e64 v1, -v1, -v1
	v_min_f32_e32 v1, 0x42700000, v1
	v_and_b32_e32 v169, 0xffff0000, v169
	v_mul_f32_e32 v1, 0x3fb8aa3b, v1
	v_max_f32_e64 v169, -v169, -v169
	v_exp_f32_e32 v2, v1
	v_add_f32_e32 v1, 1.0, v3
	v_and_b32_e32 v3, 0xffff0000, v178
	v_min_f32_e32 v169, 0x42700000, v169
	v_max_f32_e64 v3, -v3, -v3
	v_mul_f32_e32 v169, 0x3fb8aa3b, v169
	v_min_f32_e32 v3, 0x42700000, v3
	v_exp_f32_e32 v169, v169
	v_pk_add_f32 v[166:167], v[166:167], 1.0 op_sel_hi:[1,0]
	v_mul_f32_e32 v3, 0x3fb8aa3b, v3
	v_pk_mul_f32 v[166:167], v[166:167], v[170:171]
	v_pk_mul_f32 v[18:19], v[18:19], v[160:161]
	v_rcp_f32_e32 v160, v1
	v_and_b32_e32 v1, 0xffff0000, v174
	v_exp_f32_e32 v161, v3
	v_pk_mul_f32 v[12:13], v[12:13], v[166:167]
	v_max_f32_e64 v1, -v1, -v1
	v_lshlrev_b32_e32 v166, 16, v179
	v_min_f32_e32 v1, 0x42700000, v1
	v_max_f32_e64 v166, -v166, -v166
	v_pk_add_f32 v[168:169], v[168:169], 1.0 op_sel_hi:[1,0]
	v_mul_f32_e32 v1, 0x3fb8aa3b, v1
	v_min_f32_e32 v166, 0x42700000, v166
	v_pk_mul_f32 v[168:169], v[168:169], v[172:173]
	v_exp_f32_e32 v3, v1
	v_add_f32_e32 v1, 1.0, v161
	v_mul_f32_e32 v166, 0x3fb8aa3b, v166
	v_pk_mul_f32 v[14:15], v[14:15], v[168:169]
	v_rcp_f32_e32 v161, v1
	v_lshlrev_b32_e32 v1, 16, v175
	v_exp_f32_e32 v167, v166
	v_and_b32_e32 v168, 0xffff0000, v179
	v_max_f32_e64 v1, -v1, -v1
	v_max_f32_e64 v168, -v168, -v168
	v_min_f32_e32 v1, 0x42700000, v1
	v_min_f32_e32 v168, 0x42700000, v168
	v_mul_f32_e32 v1, 0x3fb8aa3b, v1
	v_mul_f32_e32 v168, 0x3fb8aa3b, v168
	v_exp_f32_e32 v166, v1
	v_add_f32_e32 v1, 1.0, v167
	v_and_b32_e32 v167, 0xffff0000, v175
	v_exp_f32_e32 v169, v168
	v_max_f32_e64 v167, -v167, -v167
	v_min_f32_e32 v167, 0x42700000, v167
	v_mul_f32_e32 v167, 0x3fb8aa3b, v167
	v_exp_f32_e32 v167, v167
	v_rcp_f32_e32 v168, v1
	v_add_f32_e32 v1, 1.0, v169
	v_rcp_f32_e32 v169, v1
	v_pk_add_f32 v[166:167], v[166:167], 1.0 op_sel_hi:[1,0]
	v_pk_add_f32 v[2:3], v[2:3], 1.0 op_sel_hi:[1,0]
	v_lshlrev_b32_e32 v1, 16, v176
	v_pk_mul_f32 v[2:3], v[2:3], v[160:161]
	v_pk_mul_f32 v[160:161], v[166:167], v[168:169]
	v_lshlrev_b32_e32 v166, 16, v180
	v_max_f32_e64 v166, -v166, -v166
	v_min_f32_e32 v166, 0x42700000, v166
	v_mul_f32_e32 v166, 0x3fb8aa3b, v166
	v_exp_f32_e32 v167, v166
	v_max_f32_e64 v1, -v1, -v1
	v_min_f32_e32 v1, 0x42700000, v1
	v_mul_f32_e32 v1, 0x3fb8aa3b, v1
	v_exp_f32_e32 v166, v1
	v_add_f32_e32 v1, 1.0, v167
	v_and_b32_e32 v167, 0xffff0000, v180
	v_max_f32_e64 v167, -v167, -v167
	v_min_f32_e32 v167, 0x42700000, v167
	v_mul_f32_e32 v167, 0x3fb8aa3b, v167
	v_rcp_f32_e32 v168, v1
	v_and_b32_e32 v1, 0xffff0000, v176
	v_exp_f32_e32 v169, v167
	v_max_f32_e64 v1, -v1, -v1
	v_lshlrev_b32_e32 v170, 16, v181
	v_min_f32_e32 v1, 0x42700000, v1
	v_max_f32_e64 v170, -v170, -v170
	v_mul_f32_e32 v1, 0x3fb8aa3b, v1
	v_min_f32_e32 v170, 0x42700000, v170
	v_exp_f32_e32 v167, v1
	v_add_f32_e32 v1, 1.0, v169
	v_mul_f32_e32 v170, 0x3fb8aa3b, v170
	v_rcp_f32_e32 v169, v1
	v_lshlrev_b32_e32 v1, 16, v177
	v_exp_f32_e32 v171, v170
	v_and_b32_e32 v172, 0xffff0000, v181
	v_max_f32_e64 v1, -v1, -v1
	v_max_f32_e64 v172, -v172, -v172
	v_min_f32_e32 v1, 0x42700000, v1
	v_min_f32_e32 v172, 0x42700000, v172
	v_mul_f32_e32 v1, 0x3fb8aa3b, v1
	v_mul_f32_e32 v172, 0x3fb8aa3b, v172
	v_exp_f32_e32 v170, v1
	v_add_f32_e32 v1, 1.0, v171
	v_and_b32_e32 v171, 0xffff0000, v177
	v_exp_f32_e32 v173, v172
	v_max_f32_e64 v171, -v171, -v171
	v_min_f32_e32 v171, 0x42700000, v171
	v_mul_f32_e32 v171, 0x3fb8aa3b, v171
	v_exp_f32_e32 v171, v171
	v_rcp_f32_e32 v172, v1
	v_add_f32_e32 v1, 1.0, v173
	v_rcp_f32_e32 v173, v1
	v_pk_add_f32 v[170:171], v[170:171], 1.0 op_sel_hi:[1,0]
	v_pk_add_f32 v[166:167], v[166:167], 1.0 op_sel_hi:[1,0]
	v_pk_mul_f32 v[10:11], v[10:11], v[160:161]
	v_pk_mul_f32 v[166:167], v[166:167], v[168:169]
	v_pk_mul_f32 v[168:169], v[170:171], v[172:173]
	v_pk_mul_f32 v[8:9], v[8:9], v[2:3]
	v_pk_mul_f32 v[6:7], v[6:7], v[168:169]
	v_pk_mul_f32 v[4:5], v[4:5], v[166:167]
	s_nop 0

; __device__ __forceinline__ unsigned cvt_pk_bf16(float lo, float hi) { unsigned r; asm volatile("v_cvt_pk_bf16_f32 %0, %1, %2" : "=v"(r) : "v"(lo), "v"(hi)); return r; }
; __device__ __forceinline__ float bf_lo(unsigned w) { return __uint_as_float(w << 16); }
; __device__ __forceinline__ float bf_hi(unsigned w) { return __uint_as_float(w & 0xffff0000u); }
;     static __device__ __forceinline__ float ex(float x) { return __expf(fminf(-x, 60.f)); }
;     __device__ __forceinline__ void operator()(const f32x4 (&acc)[2][2][4][2], const Unit& u, int wr, int wc, int fr, int fq) const {
;         const int row0 = u.pm * BM + wr * 64 + fr, col0 = u.pn * BM + wc * 32 + 8 * fq;
; #pragma unroll
;         for (int ai = 0; ai < 2; ++ai)
; #pragma unroll
;             for (int m = 0; m < 4; ++m) { const int row = row0 + ai * HALF + m * 16;
; #pragma unroll
;                 for (int bj = 0; bj < 2; ++bj) { const int col = col0 + bj * HALF;
;                     const u32x4 gc = *(const u32x4*)(R + (size_t)row * R_LD + 8192 + col);
;                     f32x4 s0, s1;
;                     s0[0] = __builtin_amdgcn_rcpf(1.0f + ex(bf_lo(gc.x))); s0[1] = __builtin_amdgcn_rcpf(1.0f + ex(bf_hi(gc.x))); s0[2] = __builtin_amdgcn_rcpf(1.0f + ex(bf_lo(gc.y))); s0[3] = __builtin_amdgcn_rcpf(1.0f + ex(bf_hi(gc.y)));
;                     s1[0] = __builtin_amdgcn_rcpf(1.0f + ex(bf_lo(gc.z))); s1[1] = __builtin_amdgcn_rcpf(1.0f + ex(bf_hi(gc.z))); s1[2] = __builtin_amdgcn_rcpf(1.0f + ex(bf_lo(gc.w))); s1[3] = __builtin_amdgcn_rcpf(1.0f + ex(bf_hi(gc.w)));
;                     const f32x4 v0 = acc[ai][bj][m][0] * s0, v1 = acc[ai][bj][m][1] * s1;
;                     u32x4 w; w.x = cvt_pk_bf16(v0[0], v0[1]); w.y = cvt_pk_bf16(v0[2], v0[3]); w.z = cvt_pk_bf16(v1[0], v1[1]); w.w = cvt_pk_bf16(v1[2], v1[3]);
;                     *(u32x4*)(O + (size_t)row * 2048 + col) = w; } }
.LBB0_791:
	v_lshl_add_u64 v[158:159], v[152:153], 0, s[6:7]
	v_lshlrev_b64 v[2:3], 1, v[150:151]
	v_lshl_add_u64 v[152:153], v[158:159], 0, v[2:3]
	global_load_dwordx4 v[154:157], v[152:153], off
	global_load_dwordx4 v[170:173], v[152:153], off offset:256
	s_mov_b64 s[20:21], 0x50000
	v_lshl_add_u64 v[174:175], v[152:153], 0, s[20:21]
	global_load_dwordx4 v[170:173], v[174:175], off
	global_load_dwordx4 v[170:173], v[174:175], off offset:256
	s_mov_b64 s[20:21], 0xa0000
	v_lshl_add_u64 v[174:175], v[152:153], 0, s[20:21]
	global_load_dwordx4 v[170:173], v[174:175], off
	global_load_dwordx4 v[170:173], v[174:175], off offset:256
	s_mov_b64 s[20:21], 0xf0000
	v_lshl_add_u64 v[174:175], v[152:153], 0, s[20:21]
	global_load_dwordx4 v[170:173], v[174:175], off
	global_load_dwordx4 v[170:173], v[174:175], off offset:256
	s_mov_b64 s[20:21], 0x280000
	v_lshl_add_u64 v[174:175], v[152:153], 0, s[20:21]
	global_load_dwordx4 v[170:173], v[174:175], off
	global_load_dwordx4 v[170:173], v[174:175], off offset:256
	s_mov_b64 s[20:21], 0x2d0000
	v_lshl_add_u64 v[174:175], v[152:153], 0, s[20:21]
	global_load_dwordx4 v[170:173], v[174:175], off
	global_load_dwordx4 v[170:173], v[174:175], off offset:256
	s_mov_b64 s[20:21], 0x320000
	v_lshl_add_u64 v[174:175], v[152:153], 0, s[20:21]
	global_load_dwordx4 v[170:173], v[174:175], off
	global_load_dwordx4 v[170:173], v[174:175], off offset:256
	s_mov_b64 s[20:21], 0x370000
	v_lshl_add_u64 v[174:175], v[152:153], 0, s[20:21]
	global_load_dwordx4 v[170:173], v[174:175], off
	global_load_dwordx4 v[170:173], v[174:175], off offset:256
	v_lshlrev_b64 v[152:153], 12, v[148:149]
	v_or_b32_e32 v150, 0x80, v150
	v_lshl_add_u64 v[152:153], s[10:11], 0, v[152:153]
	v_ashrrev_i32_e32 v151, 31, v150
	v_lshl_add_u64 v[152:153], v[152:153], 0, v[2:3]
	v_lshlrev_b64 v[150:151], 1, v[150:151]
	v_lshl_add_u64 v[158:159], v[158:159], 0, v[150:151]
	s_andn2_b64 vcc, exec, s[40:41]
	s_mov_b64 s[40:41], -1
	s_waitcnt vmcnt(0)
	v_lshlrev_b32_e32 v1, 16, v154
	v_and_b32_e32 v149, 0xffff0000, v154
	v_lshlrev_b32_e32 v154, 16, v155
	v_and_b32_e32 v155, 0xffff0000, v155
	v_lshlrev_b32_e32 v160, 16, v156
	v_and_b32_e32 v156, 0xffff0000, v156
	v_lshlrev_b32_e32 v161, 16, v157
	v_and_b32_e32 v157, 0xffff0000, v157
	v_max_f32_e64 v1, -v1, -v1
	v_max_f32_e64 v149, -v149, -v149
	v_max_f32_e64 v154, -v154, -v154
	v_max_f32_e64 v155, -v155, -v155
	v_max_f32_e64 v160, -v160, -v160
	v_max_f32_e64 v156, -v156, -v156
	v_max_f32_e64 v161, -v161, -v161
	v_max_f32_e64 v157, -v157, -v157
	v_min_f32_e32 v1, 0x42700000, v1
	v_min_f32_e32 v149, 0x42700000, v149
	v_min_f32_e32 v154, 0x42700000, v154
	v_min_f32_e32 v155, 0x42700000, v155
	v_min_f32_e32 v160, 0x42700000, v160
	v_min_f32_e32 v156, 0x42700000, v156
	v_min_f32_e32 v161, 0x42700000, v161
	v_min_f32_e32 v157, 0x42700000, v157
	v_mul_f32_e32 v1, 0x3fb8aa3b, v1
	v_mul_f32_e32 v149, 0x3fb8aa3b, v149
	v_mul_f32_e32 v154, 0x3fb8aa3b, v154
	v_mul_f32_e32 v155, 0x3fb8aa3b, v155
	v_mul_f32_e32 v160, 0x3fb8aa3b, v160
	v_mul_f32_e32 v156, 0x3fb8aa3b, v156
	v_mul_f32_e32 v161, 0x3fb8aa3b, v161
	v_mul_f32_e32 v157, 0x3fb8aa3b, v157
	v_exp_f32_e32 v1, v1
	v_exp_f32_e32 v149, v149
	v_exp_f32_e32 v154, v154
	v_exp_f32_e32 v155, v155
	v_exp_f32_e32 v160, v160
	v_exp_f32_e32 v156, v156
	v_exp_f32_e32 v161, v161
	v_exp_f32_e32 v157, v157
	v_add_f32_e32 v1, 1.0, v1
	v_add_f32_e32 v149, 1.0, v149
	v_add_f32_e32 v166, 1.0, v154
	v_add_f32_e32 v167, 1.0, v155
	v_add_f32_e32 v160, 1.0, v160
	v_add_f32_e32 v168, 1.0, v156
	v_add_f32_e32 v161, 1.0, v161
	v_add_f32_e32 v169, 1.0, v157
	v_rcp_f32_e32 v154, v1
	v_rcp_f32_e32 v155, v149
	v_rcp_f32_e32 v156, v166
	v_rcp_f32_e32 v157, v167
	v_rcp_f32_e32 v160, v160
	v_rcp_f32_e32 v166, v161
	v_rcp_f32_e32 v167, v169
	v_rcp_f32_e32 v161, v168
	v_pk_mul_f32 v[128:129], v[128:129], v[154:155]
	v_pk_mul_f32 v[130:131], v[130:131], v[156:157]
	v_pk_mul_f32 v[154:155], v[126:127], v[166:167]
	v_pk_mul_f32 v[126:127], v[124:125], v[160:161]
	v_cvt_pk_bf16_f32 v124, v128, v129
	v_cvt_pk_bf16_f32 v125, v130, v131
	v_or_b32_e32 v130, 16, v148
	v_cvt_pk_bf16_f32 v126, v126, v127
	v_cvt_pk_bf16_f32 v127, v154, v155
	global_store_dwordx4 v[152:153], v[124:127], off
	global_load_dwordx4 v[126:129], v[158:159], off
	s_waitcnt vmcnt(0)
	v_lshlrev_b32_e32 v1, 16, v126
	v_and_b32_e32 v126, 0xffff0000, v126
	v_lshlrev_b32_e32 v131, 16, v127
	v_and_b32_e32 v127, 0xffff0000, v127
	v_lshlrev_b32_e32 v158, 16, v129
	v_and_b32_e32 v129, 0xffff0000, v129
	v_lshlrev_b32_e32 v149, 16, v128
	v_and_b32_e32 v128, 0xffff0000, v128
	v_max_f32_e64 v1, -v1, -v1
	v_max_f32_e64 v126, -v126, -v126
	v_max_f32_e64 v127, -v127, -v127
	v_max_f32_e64 v158, -v158, -v158
	v_max_f32_e64 v129, -v129, -v129
	v_max_f32_e64 v131, -v131, -v131
	v_max_f32_e64 v149, -v149, -v149
	v_max_f32_e64 v128, -v128, -v128
	v_min_f32_e32 v1, 0x42700000, v1
	v_min_f32_e32 v126, 0x42700000, v126
	v_min_f32_e32 v127, 0x42700000, v127
	v_min_f32_e32 v158, 0x42700000, v158
	v_min_f32_e32 v129, 0x42700000, v129
	v_min_f32_e32 v131, 0x42700000, v131
	v_min_f32_e32 v149, 0x42700000, v149
	v_min_f32_e32 v128, 0x42700000, v128
	v_mul_f32_e32 v1, 0x3fb8aa3b, v1
	v_mul_f32_e32 v126, 0x3fb8aa3b, v126
	v_mul_f32_e32 v127, 0x3fb8aa3b, v127
	v_mul_f32_e32 v158, 0x3fb8aa3b, v158
	v_mul_f32_e32 v129, 0x3fb8aa3b, v129
	v_mul_f32_e32 v131, 0x3fb8aa3b, v131
	v_mul_f32_e32 v149, 0x3fb8aa3b, v149
	v_mul_f32_e32 v128, 0x3fb8aa3b, v128
	v_exp_f32_e32 v1, v1
	v_exp_f32_e32 v126, v126
	v_exp_f32_e32 v127, v127
	v_exp_f32_e32 v158, v158
	v_exp_f32_e32 v129, v129
	v_exp_f32_e32 v131, v131
	v_exp_f32_e32 v149, v149
	v_exp_f32_e32 v128, v128
	v_add_f32_e32 v1, 1.0, v1
	v_add_f32_e32 v159, 1.0, v126
	v_add_f32_e32 v160, 1.0, v127
	v_add_f32_e32 v161, 1.0, v158
	v_add_f32_e32 v167, 1.0, v129
	v_add_f32_e32 v131, 1.0, v131
	v_add_f32_e32 v149, 1.0, v149
	v_add_f32_e32 v166, 1.0, v128
	v_rcp_f32_e32 v126, v1
	v_rcp_f32_e32 v127, v159
	v_rcp_f32_e32 v129, v160
	v_rcp_f32_e32 v160, v161
	v_rcp_f32_e32 v161, v167
	v_mov_b64_e32 v[124:125], s[12:13]
	v_rcp_f32_e32 v128, v131
	v_rcp_f32_e32 v158, v149
	v_rcp_f32_e32 v159, v166
	v_mad_i64_i32 v[154:155], s[4:5], v130, s69, v[124:125]
	v_lshl_add_u64 v[154:155], v[154:155], 0, s[6:7]
	v_lshl_add_u64 v[156:157], v[154:155], 0, v[2:3]
	v_pk_mul_f32 v[120:121], v[120:121], v[126:127]
	v_pk_mul_f32 v[126:127], v[118:119], v[160:161]
	v_pk_mul_f32 v[122:123], v[122:123], v[128:129]
	v_pk_mul_f32 v[116:117], v[116:117], v[158:159]
	v_cvt_pk_bf16_f32 v118, v120, v121
	v_cvt_pk_bf16_f32 v119, v122, v123
	v_ashrrev_i32_e32 v131, 31, v130
	v_cvt_pk_bf16_f32 v120, v116, v117
	v_cvt_pk_bf16_f32 v121, v126, v127
	global_load_dwordx4 v[126:129], v[156:157], off
	v_lshlrev_b64 v[116:117], 12, v[130:131]
	global_store_dwordx4 v[152:153], v[118:121], off offset:256
	v_lshl_add_u64 v[116:117], s[10:11], 0, v[116:117]
	v_lshl_add_u64 v[116:117], v[116:117], 0, v[2:3]
	v_lshl_add_u64 v[122:123], v[154:155], 0, v[150:151]
	s_waitcnt vmcnt(0)
; __device__ __forceinline__ unsigned cvt_pk_bf16(float lo, float hi) { unsigned r; asm volatile("v_cvt_pk_bf16_f32 %0, %1, %2" : "=v"(r) : "v"(lo), "v"(hi)); return r; }
; __device__ __forceinline__ float bf_lo(unsigned w) { return __uint_as_float(w << 16); }
; __device__ __forceinline__ float bf_hi(unsigned w) { return __uint_as_float(w & 0xffff0000u); }
;     static __device__ __forceinline__ float ex(float x) { return __expf(fminf(-x, 60.f)); }
;     __device__ __forceinline__ void operator()(const f32x4 (&acc)[2][2][4][2], const Unit& u, int wr, int wc, int fr, int fq) const {
;     ...
;             for (int m = 0; m < 4; ++m) { const int row = row0 + ai * HALF + m * 16;
; #pragma unroll
;                 for (int bj = 0; bj < 2; ++bj) { const int col = col0 + bj * HALF;
;                     const u32x4 gc = *(const u32x4*)(R + (size_t)row * R_LD + 8192 + col);
;                     f32x4 s0, s1;
;                     s0[0] = __builtin_amdgcn_rcpf(1.0f + ex(bf_lo(gc.x))); s0[1] = __builtin_amdgcn_rcpf(1.0f + ex(bf_hi(gc.x))); s0[2] = __builtin_amdgcn_rcpf(1.0f + ex(bf_lo(gc.y))); s0[3] = __builtin_amdgcn_rcpf(1.0f + ex(bf_hi(gc.y)));
;                     s1[0] = __builtin_amdgcn_rcpf(1.0f + ex(bf_lo(gc.z))); s1[1] = __builtin_amdgcn_rcpf(1.0f + ex(bf_hi(gc.z))); s1[2] = __builtin_amdgcn_rcpf(1.0f + ex(bf_lo(gc.w))); s1[3] = __builtin_amdgcn_rcpf(1.0f + ex(bf_hi(gc.w)));
;                     const f32x4 v0 = acc[ai][bj][m][0] * s0, v1 = acc[ai][bj][m][1] * s1;
;                     u32x4 w; w.x = cvt_pk_bf16(v0[0], v0[1]); w.y = cvt_pk_bf16(v0[2], v0[3]); w.z = cvt_pk_bf16(v1[0], v1[1]); w.w = cvt_pk_bf16(v1[2], v1[3]);
;                     *(u32x4*)(O + (size_t)row * 2048 + col) = w; } }
	v_lshlrev_b32_e32 v1, 16, v126
	v_and_b32_e32 v118, 0xffff0000, v126
	v_lshlrev_b32_e32 v119, 16, v127
	v_and_b32_e32 v120, 0xffff0000, v127
	v_lshlrev_b32_e32 v121, 16, v128
	v_and_b32_e32 v126, 0xffff0000, v128
	v_lshlrev_b32_e32 v127, 16, v129
	v_and_b32_e32 v128, 0xffff0000, v129
	v_max_f32_e64 v1, -v1, -v1
	v_max_f32_e64 v118, -v118, -v118
	v_max_f32_e64 v121, -v121, -v121
	v_max_f32_e64 v126, -v126, -v126
	v_max_f32_e64 v127, -v127, -v127
	v_max_f32_e64 v128, -v128, -v128
	v_max_f32_e64 v119, -v119, -v119
	v_max_f32_e64 v120, -v120, -v120
	v_min_f32_e32 v1, 0x42700000, v1
	v_min_f32_e32 v118, 0x42700000, v118
	v_min_f32_e32 v121, 0x42700000, v121
	v_min_f32_e32 v126, 0x42700000, v126
	v_min_f32_e32 v127, 0x42700000, v127
	v_min_f32_e32 v128, 0x42700000, v128
	v_min_f32_e32 v119, 0x42700000, v119
	v_min_f32_e32 v120, 0x42700000, v120
	v_mul_f32_e32 v1, 0x3fb8aa3b, v1
	v_mul_f32_e32 v118, 0x3fb8aa3b, v118
	v_mul_f32_e32 v121, 0x3fb8aa3b, v121
	v_mul_f32_e32 v126, 0x3fb8aa3b, v126
	v_mul_f32_e32 v127, 0x3fb8aa3b, v127
	v_mul_f32_e32 v128, 0x3fb8aa3b, v128
	v_mul_f32_e32 v119, 0x3fb8aa3b, v119
	v_mul_f32_e32 v120, 0x3fb8aa3b, v120
	v_exp_f32_e32 v1, v1
	v_exp_f32_e32 v118, v118
	v_exp_f32_e32 v121, v121
	v_exp_f32_e32 v126, v126
	v_exp_f32_e32 v127, v127
	v_exp_f32_e32 v128, v128
	v_exp_f32_e32 v119, v119
	v_exp_f32_e32 v120, v120
	v_add_f32_e32 v1, 1.0, v1
	v_add_f32_e32 v129, 1.0, v118
	v_add_f32_e32 v149, 1.0, v121
	v_add_f32_e32 v152, 1.0, v126
	v_add_f32_e32 v127, 1.0, v127
	v_add_f32_e32 v153, 1.0, v128
	v_add_f32_e32 v130, 1.0, v119
	v_add_f32_e32 v131, 1.0, v120
	v_rcp_f32_e32 v118, v1
	v_rcp_f32_e32 v119, v129
	v_rcp_f32_e32 v126, v149
	v_rcp_f32_e32 v128, v127
	v_rcp_f32_e32 v129, v153
	v_rcp_f32_e32 v127, v152
	v_rcp_f32_e32 v120, v130
	v_rcp_f32_e32 v121, v131
	v_pk_mul_f32 v[112:113], v[112:113], v[118:119]
	v_pk_mul_f32 v[118:119], v[110:111], v[128:129]
	v_pk_mul_f32 v[110:111], v[108:109], v[126:127]
	v_pk_mul_f32 v[114:115], v[114:115], v[120:121]
	v_cvt_pk_bf16_f32 v108, v112, v113
	v_or_b32_e32 v112, 32, v148
	v_cvt_pk_bf16_f32 v109, v114, v115
	v_cvt_pk_bf16_f32 v110, v110, v111
	v_cvt_pk_bf16_f32 v111, v118, v119
	global_store_dwordx4 v[116:117], v[108:111], off
	global_load_dwordx4 v[108:111], v[122:123], off
	v_mad_i64_i32 v[114:115], s[4:5], v112, s69, v[124:125]
	v_lshl_add_u64 v[114:115], v[114:115], 0, s[6:7]
	v_lshl_add_u64 v[118:119], v[114:115], 0, v[2:3]
	s_waitcnt vmcnt(0)
	v_lshlrev_b32_e32 v1, 16, v108
	v_and_b32_e32 v108, 0xffff0000, v108
	v_lshlrev_b32_e32 v113, 16, v109
	v_and_b32_e32 v109, 0xffff0000, v109
	v_lshlrev_b32_e32 v121, 16, v111
	v_and_b32_e32 v111, 0xffff0000, v111
	v_lshlrev_b32_e32 v120, 16, v110
	v_and_b32_e32 v110, 0xffff0000, v110
	v_max_f32_e64 v1, -v1, -v1
	v_max_f32_e64 v108, -v108, -v108
	v_max_f32_e64 v113, -v113, -v113
	v_max_f32_e64 v109, -v109, -v109
	v_max_f32_e64 v121, -v121, -v121
	v_max_f32_e64 v111, -v111, -v111
	v_max_f32_e64 v120, -v120, -v120
	v_max_f32_e64 v110, -v110, -v110
	v_min_f32_e32 v1, 0x42700000, v1
	v_min_f32_e32 v108, 0x42700000, v108
	v_min_f32_e32 v113, 0x42700000, v113
	v_min_f32_e32 v109, 0x42700000, v109
	v_min_f32_e32 v121, 0x42700000, v121
	v_min_f32_e32 v111, 0x42700000, v111
	v_min_f32_e32 v120, 0x42700000, v120
	v_min_f32_e32 v110, 0x42700000, v110
	v_mul_f32_e32 v1, 0x3fb8aa3b, v1
	v_mul_f32_e32 v108, 0x3fb8aa3b, v108
	v_mul_f32_e32 v113, 0x3fb8aa3b, v113
	v_mul_f32_e32 v109, 0x3fb8aa3b, v109
	v_mul_f32_e32 v121, 0x3fb8aa3b, v121
	v_mul_f32_e32 v111, 0x3fb8aa3b, v111
	v_mul_f32_e32 v120, 0x3fb8aa3b, v120
	v_mul_f32_e32 v110, 0x3fb8aa3b, v110
	v_exp_f32_e32 v1, v1
	v_exp_f32_e32 v108, v108
	v_exp_f32_e32 v113, v113
	v_exp_f32_e32 v109, v109
	v_exp_f32_e32 v121, v121
	v_exp_f32_e32 v111, v111
	v_exp_f32_e32 v120, v120
	v_exp_f32_e32 v110, v110
	v_add_f32_e32 v1, 1.0, v1
	v_add_f32_e32 v122, 1.0, v108
	v_add_f32_e32 v113, 1.0, v113
	v_add_f32_e32 v123, 1.0, v109
	v_add_f32_e32 v121, 1.0, v121
	v_add_f32_e32 v127, 1.0, v111
	v_add_f32_e32 v120, 1.0, v120
	v_add_f32_e32 v126, 1.0, v110
	v_rcp_f32_e32 v108, v1
	v_rcp_f32_e32 v109, v122
	v_rcp_f32_e32 v110, v113
	v_rcp_f32_e32 v111, v123
	v_rcp_f32_e32 v122, v121
	v_rcp_f32_e32 v123, v127
	v_rcp_f32_e32 v120, v120
	v_rcp_f32_e32 v121, v126
	v_pk_mul_f32 v[106:107], v[106:107], v[110:111]
	v_pk_mul_f32 v[104:105], v[104:105], v[108:109]
	v_pk_mul_f32 v[108:109], v[102:103], v[122:123]
	v_pk_mul_f32 v[100:101], v[100:101], v[120:121]
	v_cvt_pk_bf16_f32 v102, v104, v105
	v_cvt_pk_bf16_f32 v103, v106, v107
	v_ashrrev_i32_e32 v113, 31, v112
	v_cvt_pk_bf16_f32 v104, v100, v101
	v_cvt_pk_bf16_f32 v105, v108, v109
	global_load_dwordx4 v[106:109], v[118:119], off
	v_lshl_add_u64 v[110:111], v[114:115], 0, v[150:151]
	global_store_dwordx4 v[116:117], v[102:105], off offset:256
	v_lshlrev_b64 v[100:101], 12, v[112:113]
	v_lshl_add_u64 v[100:101], s[10:11], 0, v[100:101]
	v_lshl_add_u64 v[100:101], v[100:101], 0, v[2:3]
	s_waitcnt vmcnt(0)
; __device__ __forceinline__ unsigned cvt_pk_bf16(float lo, float hi) { unsigned r; asm volatile("v_cvt_pk_bf16_f32 %0, %1, %2" : "=v"(r) : "v"(lo), "v"(hi)); return r; }
; __device__ __forceinline__ float bf_lo(unsigned w) { return __uint_as_float(w << 16); }
; __device__ __forceinline__ float bf_hi(unsigned w) { return __uint_as_float(w & 0xffff0000u); }
;     static __device__ __forceinline__ float ex(float x) { return __expf(fminf(-x, 60.f)); }
;     __device__ __forceinline__ void operator()(const f32x4 (&acc)[2][2][4][2], const Unit& u, int wr, int wc, int fr, int fq) const {
;     ...
;             for (int m = 0; m < 4; ++m) { const int row = row0 + ai * HALF + m * 16;
; #pragma unroll
;                 for (int bj = 0; bj < 2; ++bj) { const int col = col0 + bj * HALF;
;                     const u32x4 gc = *(const u32x4*)(R + (size_t)row * R_LD + 8192 + col);
;                     f32x4 s0, s1;
;                     s0[0] = __builtin_amdgcn_rcpf(1.0f + ex(bf_lo(gc.x))); s0[1] = __builtin_amdgcn_rcpf(1.0f + ex(bf_hi(gc.x))); s0[2] = __builtin_amdgcn_rcpf(1.0f + ex(bf_lo(gc.y))); s0[3] = __builtin_amdgcn_rcpf(1.0f + ex(bf_hi(gc.y)));
;                     s1[0] = __builtin_amdgcn_rcpf(1.0f + ex(bf_lo(gc.z))); s1[1] = __builtin_amdgcn_rcpf(1.0f + ex(bf_hi(gc.z))); s1[2] = __builtin_amdgcn_rcpf(1.0f + ex(bf_lo(gc.w))); s1[3] = __builtin_amdgcn_rcpf(1.0f + ex(bf_hi(gc.w)));
;                     const f32x4 v0 = acc[ai][bj][m][0] * s0, v1 = acc[ai][bj][m][1] * s1;
;                     u32x4 w; w.x = cvt_pk_bf16(v0[0], v0[1]); w.y = cvt_pk_bf16(v0[2], v0[3]); w.z = cvt_pk_bf16(v1[0], v1[1]); w.w = cvt_pk_bf16(v1[2], v1[3]);
;                     *(u32x4*)(O + (size_t)row * 2048 + col) = w; } }
	v_lshlrev_b32_e32 v1, 16, v106
	v_and_b32_e32 v102, 0xffff0000, v106
	v_lshlrev_b32_e32 v103, 16, v107
	v_and_b32_e32 v104, 0xffff0000, v107
	v_lshlrev_b32_e32 v105, 16, v108
	v_and_b32_e32 v106, 0xffff0000, v108
	v_lshlrev_b32_e32 v107, 16, v109
	v_and_b32_e32 v108, 0xffff0000, v109
	v_max_f32_e64 v1, -v1, -v1
	v_max_f32_e64 v102, -v102, -v102
	v_max_f32_e64 v105, -v105, -v105
	v_max_f32_e64 v106, -v106, -v106
	v_max_f32_e64 v107, -v107, -v107
	v_max_f32_e64 v108, -v108, -v108
	v_max_f32_e64 v103, -v103, -v103
	v_max_f32_e64 v104, -v104, -v104
	v_min_f32_e32 v1, 0x42700000, v1
	v_min_f32_e32 v102, 0x42700000, v102
	v_min_f32_e32 v105, 0x42700000, v105
	v_min_f32_e32 v106, 0x42700000, v106
	v_min_f32_e32 v107, 0x42700000, v107
	v_min_f32_e32 v108, 0x42700000, v108
	v_min_f32_e32 v103, 0x42700000, v103
	v_min_f32_e32 v104, 0x42700000, v104
	v_mul_f32_e32 v1, 0x3fb8aa3b, v1
	v_mul_f32_e32 v102, 0x3fb8aa3b, v102
	v_mul_f32_e32 v105, 0x3fb8aa3b, v105
	v_mul_f32_e32 v106, 0x3fb8aa3b, v106
	v_mul_f32_e32 v107, 0x3fb8aa3b, v107
	v_mul_f32_e32 v108, 0x3fb8aa3b, v108
	v_mul_f32_e32 v103, 0x3fb8aa3b, v103
	v_mul_f32_e32 v104, 0x3fb8aa3b, v104
	v_exp_f32_e32 v1, v1
	v_exp_f32_e32 v102, v102
	v_exp_f32_e32 v105, v105
	v_exp_f32_e32 v106, v106
	v_exp_f32_e32 v107, v107
	v_exp_f32_e32 v108, v108
	v_exp_f32_e32 v103, v103
	v_exp_f32_e32 v104, v104
	v_add_f32_e32 v1, 1.0, v1
	v_add_f32_e32 v109, 1.0, v102
	v_add_f32_e32 v114, 1.0, v105
	v_add_f32_e32 v115, 1.0, v106
	v_add_f32_e32 v107, 1.0, v107
	v_add_f32_e32 v116, 1.0, v108
	v_add_f32_e32 v112, 1.0, v103
	v_add_f32_e32 v113, 1.0, v104
	v_rcp_f32_e32 v102, v1
	v_rcp_f32_e32 v103, v109
	v_rcp_f32_e32 v106, v114
	v_rcp_f32_e32 v108, v107
	v_rcp_f32_e32 v109, v116
	v_rcp_f32_e32 v107, v115
	v_rcp_f32_e32 v104, v112
	v_rcp_f32_e32 v105, v113
	v_pk_mul_f32 v[96:97], v[96:97], v[102:103]
	v_pk_mul_f32 v[102:103], v[94:95], v[108:109]
	v_pk_mul_f32 v[94:95], v[92:93], v[106:107]
	v_pk_mul_f32 v[98:99], v[98:99], v[104:105]
	v_cvt_pk_bf16_f32 v92, v96, v97
	v_or_b32_e32 v96, 48, v148
	v_cvt_pk_bf16_f32 v93, v98, v99
	v_cvt_pk_bf16_f32 v94, v94, v95
	v_cvt_pk_bf16_f32 v95, v102, v103
	global_store_dwordx4 v[100:101], v[92:95], off
	global_load_dwordx4 v[92:95], v[110:111], off
	v_mad_i64_i32 v[98:99], s[4:5], v96, s69, v[124:125]
	v_lshl_add_u64 v[98:99], v[98:99], 0, s[6:7]
	v_lshl_add_u64 v[102:103], v[98:99], 0, v[2:3]
	s_waitcnt vmcnt(0)
	v_lshlrev_b32_e32 v1, 16, v92
	v_and_b32_e32 v92, 0xffff0000, v92
	v_lshlrev_b32_e32 v97, 16, v93
	v_and_b32_e32 v93, 0xffff0000, v93
	v_lshlrev_b32_e32 v105, 16, v95
	v_and_b32_e32 v95, 0xffff0000, v95
	v_lshlrev_b32_e32 v104, 16, v94
	v_and_b32_e32 v94, 0xffff0000, v94
	v_max_f32_e64 v1, -v1, -v1
	v_max_f32_e64 v92, -v92, -v92
	v_max_f32_e64 v97, -v97, -v97
	v_max_f32_e64 v93, -v93, -v93
	v_max_f32_e64 v105, -v105, -v105
	v_max_f32_e64 v95, -v95, -v95
	v_max_f32_e64 v104, -v104, -v104
	v_max_f32_e64 v94, -v94, -v94
	v_min_f32_e32 v1, 0x42700000, v1
	v_min_f32_e32 v92, 0x42700000, v92
	v_min_f32_e32 v97, 0x42700000, v97
	v_min_f32_e32 v93, 0x42700000, v93
	v_min_f32_e32 v105, 0x42700000, v105
	v_min_f32_e32 v95, 0x42700000, v95
	v_min_f32_e32 v104, 0x42700000, v104
	v_min_f32_e32 v94, 0x42700000, v94
	v_mul_f32_e32 v1, 0x3fb8aa3b, v1
	v_mul_f32_e32 v92, 0x3fb8aa3b, v92
	v_mul_f32_e32 v97, 0x3fb8aa3b, v97
	v_mul_f32_e32 v93, 0x3fb8aa3b, v93
	v_mul_f32_e32 v105, 0x3fb8aa3b, v105
	v_mul_f32_e32 v95, 0x3fb8aa3b, v95
	v_mul_f32_e32 v104, 0x3fb8aa3b, v104
	v_mul_f32_e32 v94, 0x3fb8aa3b, v94
	v_exp_f32_e32 v1, v1
	v_exp_f32_e32 v92, v92
	v_exp_f32_e32 v97, v97
	v_exp_f32_e32 v93, v93
	v_exp_f32_e32 v105, v105
	v_exp_f32_e32 v95, v95
	v_exp_f32_e32 v104, v104
	v_exp_f32_e32 v94, v94
	v_add_f32_e32 v1, 1.0, v1
	v_add_f32_e32 v106, 1.0, v92
	v_add_f32_e32 v97, 1.0, v97
	v_add_f32_e32 v107, 1.0, v93
	v_add_f32_e32 v105, 1.0, v105
	v_add_f32_e32 v109, 1.0, v95
	v_add_f32_e32 v104, 1.0, v104
	v_add_f32_e32 v108, 1.0, v94
	v_rcp_f32_e32 v92, v1
	v_rcp_f32_e32 v93, v106
	v_rcp_f32_e32 v94, v97
	v_rcp_f32_e32 v95, v107
	v_rcp_f32_e32 v106, v105
	v_rcp_f32_e32 v107, v109
	v_rcp_f32_e32 v104, v104
	v_rcp_f32_e32 v105, v108
	v_pk_mul_f32 v[90:91], v[90:91], v[94:95]
	v_pk_mul_f32 v[88:89], v[88:89], v[92:93]
	v_pk_mul_f32 v[92:93], v[86:87], v[106:107]
	v_pk_mul_f32 v[84:85], v[84:85], v[104:105]
	v_cvt_pk_bf16_f32 v86, v88, v89
	v_cvt_pk_bf16_f32 v87, v90, v91
	v_ashrrev_i32_e32 v97, 31, v96
	v_cvt_pk_bf16_f32 v88, v84, v85
	v_cvt_pk_bf16_f32 v89, v92, v93
	global_load_dwordx4 v[90:93], v[102:103], off
	v_lshl_add_u64 v[94:95], v[98:99], 0, v[150:151]
	global_store_dwordx4 v[100:101], v[86:89], off offset:256
	v_lshlrev_b64 v[84:85], 12, v[96:97]
	v_lshl_add_u64 v[84:85], s[10:11], 0, v[84:85]
	v_lshl_add_u64 v[84:85], v[84:85], 0, v[2:3]
	s_waitcnt vmcnt(0)
; __device__ __forceinline__ unsigned cvt_pk_bf16(float lo, float hi) { unsigned r; asm volatile("v_cvt_pk_bf16_f32 %0, %1, %2" : "=v"(r) : "v"(lo), "v"(hi)); return r; }
; __device__ __forceinline__ float bf_lo(unsigned w) { return __uint_as_float(w << 16); }
; __device__ __forceinline__ float bf_hi(unsigned w) { return __uint_as_float(w & 0xffff0000u); }
;     static __device__ __forceinline__ float ex(float x) { return __expf(fminf(-x, 60.f)); }
;     __device__ __forceinline__ void operator()(const f32x4 (&acc)[2][2][4][2], const Unit& u, int wr, int wc, int fr, int fq) const {
;     ...
;             for (int m = 0; m < 4; ++m) { const int row = row0 + ai * HALF + m * 16;
; #pragma unroll
;                 for (int bj = 0; bj < 2; ++bj) { const int col = col0 + bj * HALF;
;                     const u32x4 gc = *(const u32x4*)(R + (size_t)row * R_LD + 8192 + col);
;                     f32x4 s0, s1;
;                     s0[0] = __builtin_amdgcn_rcpf(1.0f + ex(bf_lo(gc.x))); s0[1] = __builtin_amdgcn_rcpf(1.0f + ex(bf_hi(gc.x))); s0[2] = __builtin_amdgcn_rcpf(1.0f + ex(bf_lo(gc.y))); s0[3] = __builtin_amdgcn_rcpf(1.0f + ex(bf_hi(gc.y)));
;                     s1[0] = __builtin_amdgcn_rcpf(1.0f + ex(bf_lo(gc.z))); s1[1] = __builtin_amdgcn_rcpf(1.0f + ex(bf_hi(gc.z))); s1[2] = __builtin_amdgcn_rcpf(1.0f + ex(bf_lo(gc.w))); s1[3] = __builtin_amdgcn_rcpf(1.0f + ex(bf_hi(gc.w)));
;                     const f32x4 v0 = acc[ai][bj][m][0] * s0, v1 = acc[ai][bj][m][1] * s1;
;                     u32x4 w; w.x = cvt_pk_bf16(v0[0], v0[1]); w.y = cvt_pk_bf16(v0[2], v0[3]); w.z = cvt_pk_bf16(v1[0], v1[1]); w.w = cvt_pk_bf16(v1[2], v1[3]);
;                     *(u32x4*)(O + (size_t)row * 2048 + col) = w; } }
	v_lshlrev_b32_e32 v1, 16, v90
	v_and_b32_e32 v86, 0xffff0000, v90
	v_lshlrev_b32_e32 v87, 16, v91
	v_and_b32_e32 v88, 0xffff0000, v91
	v_lshlrev_b32_e32 v89, 16, v92
	v_and_b32_e32 v90, 0xffff0000, v92
	v_lshlrev_b32_e32 v91, 16, v93
	v_and_b32_e32 v92, 0xffff0000, v93
	v_max_f32_e64 v1, -v1, -v1
	v_max_f32_e64 v86, -v86, -v86
	v_max_f32_e64 v89, -v89, -v89
	v_max_f32_e64 v90, -v90, -v90
	v_max_f32_e64 v91, -v91, -v91
	v_max_f32_e64 v92, -v92, -v92
	v_max_f32_e64 v87, -v87, -v87
	v_max_f32_e64 v88, -v88, -v88
	v_min_f32_e32 v1, 0x42700000, v1
	v_min_f32_e32 v86, 0x42700000, v86
	v_min_f32_e32 v89, 0x42700000, v89
	v_min_f32_e32 v90, 0x42700000, v90
	v_min_f32_e32 v91, 0x42700000, v91
	v_min_f32_e32 v92, 0x42700000, v92
	v_min_f32_e32 v87, 0x42700000, v87
	v_min_f32_e32 v88, 0x42700000, v88
	v_mul_f32_e32 v1, 0x3fb8aa3b, v1
	v_mul_f32_e32 v86, 0x3fb8aa3b, v86
	v_mul_f32_e32 v89, 0x3fb8aa3b, v89
	v_mul_f32_e32 v90, 0x3fb8aa3b, v90
	v_mul_f32_e32 v91, 0x3fb8aa3b, v91
	v_mul_f32_e32 v92, 0x3fb8aa3b, v92
	v_mul_f32_e32 v87, 0x3fb8aa3b, v87
	v_mul_f32_e32 v88, 0x3fb8aa3b, v88
	v_exp_f32_e32 v1, v1
	v_exp_f32_e32 v86, v86
	v_exp_f32_e32 v89, v89
	v_exp_f32_e32 v90, v90
	v_exp_f32_e32 v91, v91
	v_exp_f32_e32 v92, v92
	v_exp_f32_e32 v87, v87
	v_exp_f32_e32 v88, v88
	v_add_f32_e32 v1, 1.0, v1
	v_add_f32_e32 v93, 1.0, v86
	v_add_f32_e32 v98, 1.0, v89
	v_add_f32_e32 v99, 1.0, v90
	v_add_f32_e32 v91, 1.0, v91
	v_add_f32_e32 v100, 1.0, v92
	v_add_f32_e32 v96, 1.0, v87
	v_add_f32_e32 v97, 1.0, v88
	v_rcp_f32_e32 v86, v1
	v_rcp_f32_e32 v87, v93
	v_rcp_f32_e32 v90, v98
	v_rcp_f32_e32 v92, v91
	v_rcp_f32_e32 v93, v100
	v_rcp_f32_e32 v91, v99
	v_rcp_f32_e32 v88, v96
	v_rcp_f32_e32 v89, v97
	v_pk_mul_f32 v[80:81], v[80:81], v[86:87]
	v_pk_mul_f32 v[86:87], v[78:79], v[92:93]
	v_pk_mul_f32 v[78:79], v[76:77], v[90:91]
	v_pk_mul_f32 v[82:83], v[82:83], v[88:89]
	v_cvt_pk_bf16_f32 v76, v80, v81
	v_add_u32_e32 v80, 0x80, v148
	v_cvt_pk_bf16_f32 v77, v82, v83
	v_cvt_pk_bf16_f32 v78, v78, v79
	v_cvt_pk_bf16_f32 v79, v86, v87
	global_store_dwordx4 v[84:85], v[76:79], off
	global_load_dwordx4 v[76:79], v[94:95], off
	v_mad_i64_i32 v[82:83], s[4:5], v80, s69, v[124:125]
	v_lshl_add_u64 v[82:83], v[82:83], 0, s[6:7]
	v_lshl_add_u64 v[86:87], v[82:83], 0, v[2:3]
	s_waitcnt vmcnt(0)
	v_lshlrev_b32_e32 v1, 16, v76
	v_and_b32_e32 v76, 0xffff0000, v76
	v_lshlrev_b32_e32 v81, 16, v77
	v_and_b32_e32 v77, 0xffff0000, v77
	v_lshlrev_b32_e32 v89, 16, v79
	v_and_b32_e32 v79, 0xffff0000, v79
	v_lshlrev_b32_e32 v88, 16, v78
	v_and_b32_e32 v78, 0xffff0000, v78
	v_max_f32_e64 v1, -v1, -v1
	v_max_f32_e64 v76, -v76, -v76
	v_max_f32_e64 v81, -v81, -v81
	v_max_f32_e64 v77, -v77, -v77
	v_max_f32_e64 v89, -v89, -v89
	v_max_f32_e64 v79, -v79, -v79
	v_max_f32_e64 v88, -v88, -v88
	v_max_f32_e64 v78, -v78, -v78
	v_min_f32_e32 v1, 0x42700000, v1
	v_min_f32_e32 v76, 0x42700000, v76
	v_min_f32_e32 v81, 0x42700000, v81
	v_min_f32_e32 v77, 0x42700000, v77
	v_min_f32_e32 v89, 0x42700000, v89
	v_min_f32_e32 v79, 0x42700000, v79
	v_min_f32_e32 v88, 0x42700000, v88
	v_min_f32_e32 v78, 0x42700000, v78
	v_mul_f32_e32 v1, 0x3fb8aa3b, v1
	v_mul_f32_e32 v76, 0x3fb8aa3b, v76
	v_mul_f32_e32 v81, 0x3fb8aa3b, v81
	v_mul_f32_e32 v77, 0x3fb8aa3b, v77
	v_mul_f32_e32 v89, 0x3fb8aa3b, v89
	v_mul_f32_e32 v79, 0x3fb8aa3b, v79
	v_mul_f32_e32 v88, 0x3fb8aa3b, v88
	v_mul_f32_e32 v78, 0x3fb8aa3b, v78
	v_exp_f32_e32 v1, v1
	v_exp_f32_e32 v76, v76
	v_exp_f32_e32 v81, v81
	v_exp_f32_e32 v77, v77
	v_exp_f32_e32 v89, v89
	v_exp_f32_e32 v79, v79
	v_exp_f32_e32 v88, v88
	v_exp_f32_e32 v78, v78
	v_add_f32_e32 v1, 1.0, v1
	v_add_f32_e32 v90, 1.0, v76
	v_add_f32_e32 v81, 1.0, v81
	v_add_f32_e32 v91, 1.0, v77
	v_add_f32_e32 v89, 1.0, v89
	v_add_f32_e32 v93, 1.0, v79
	v_add_f32_e32 v88, 1.0, v88
	v_add_f32_e32 v92, 1.0, v78
	v_rcp_f32_e32 v76, v1
	v_rcp_f32_e32 v77, v90
	v_rcp_f32_e32 v78, v81
	v_rcp_f32_e32 v79, v91
	v_rcp_f32_e32 v90, v89
	v_rcp_f32_e32 v91, v93
	v_rcp_f32_e32 v88, v88
	v_rcp_f32_e32 v89, v92
	v_pk_mul_f32 v[74:75], v[74:75], v[78:79]
	v_pk_mul_f32 v[72:73], v[72:73], v[76:77]
	v_pk_mul_f32 v[76:77], v[70:71], v[90:91]
	v_pk_mul_f32 v[68:69], v[68:69], v[88:89]
	v_cvt_pk_bf16_f32 v70, v72, v73
	v_cvt_pk_bf16_f32 v71, v74, v75
	v_ashrrev_i32_e32 v81, 31, v80
	v_cvt_pk_bf16_f32 v72, v68, v69
	v_cvt_pk_bf16_f32 v73, v76, v77
	global_load_dwordx4 v[74:77], v[86:87], off
	v_lshl_add_u64 v[78:79], v[82:83], 0, v[150:151]
	global_store_dwordx4 v[84:85], v[70:73], off offset:256
	v_lshlrev_b64 v[68:69], 12, v[80:81]
	v_lshl_add_u64 v[68:69], s[10:11], 0, v[68:69]
	v_lshl_add_u64 v[68:69], v[68:69], 0, v[2:3]
	s_waitcnt vmcnt(0)
; __device__ __forceinline__ unsigned cvt_pk_bf16(float lo, float hi) { unsigned r; asm volatile("v_cvt_pk_bf16_f32 %0, %1, %2" : "=v"(r) : "v"(lo), "v"(hi)); return r; }
; __device__ __forceinline__ float bf_lo(unsigned w) { return __uint_as_float(w << 16); }
; __device__ __forceinline__ float bf_hi(unsigned w) { return __uint_as_float(w & 0xffff0000u); }
;     static __device__ __forceinline__ float ex(float x) { return __expf(fminf(-x, 60.f)); }
;     __device__ __forceinline__ void operator()(const f32x4 (&acc)[2][2][4][2], const Unit& u, int wr, int wc, int fr, int fq) const {
;     ...
;             for (int m = 0; m < 4; ++m) { const int row = row0 + ai * HALF + m * 16;
; #pragma unroll
;                 for (int bj = 0; bj < 2; ++bj) { const int col = col0 + bj * HALF;
;                     const u32x4 gc = *(const u32x4*)(R + (size_t)row * R_LD + 8192 + col);
;                     f32x4 s0, s1;
;                     s0[0] = __builtin_amdgcn_rcpf(1.0f + ex(bf_lo(gc.x))); s0[1] = __builtin_amdgcn_rcpf(1.0f + ex(bf_hi(gc.x))); s0[2] = __builtin_amdgcn_rcpf(1.0f + ex(bf_lo(gc.y))); s0[3] = __builtin_amdgcn_rcpf(1.0f + ex(bf_hi(gc.y)));
;                     s1[0] = __builtin_amdgcn_rcpf(1.0f + ex(bf_lo(gc.z))); s1[1] = __builtin_amdgcn_rcpf(1.0f + ex(bf_hi(gc.z))); s1[2] = __builtin_amdgcn_rcpf(1.0f + ex(bf_lo(gc.w))); s1[3] = __builtin_amdgcn_rcpf(1.0f + ex(bf_hi(gc.w)));
;                     const f32x4 v0 = acc[ai][bj][m][0] * s0, v1 = acc[ai][bj][m][1] * s1;
;                     u32x4 w; w.x = cvt_pk_bf16(v0[0], v0[1]); w.y = cvt_pk_bf16(v0[2], v0[3]); w.z = cvt_pk_bf16(v1[0], v1[1]); w.w = cvt_pk_bf16(v1[2], v1[3]);
;                     *(u32x4*)(O + (size_t)row * 2048 + col) = w; } }
	v_lshlrev_b32_e32 v1, 16, v74
	v_and_b32_e32 v70, 0xffff0000, v74
	v_lshlrev_b32_e32 v71, 16, v75
	v_and_b32_e32 v72, 0xffff0000, v75
	v_lshlrev_b32_e32 v73, 16, v76
	v_and_b32_e32 v74, 0xffff0000, v76
	v_lshlrev_b32_e32 v75, 16, v77
	v_and_b32_e32 v76, 0xffff0000, v77
	v_max_f32_e64 v1, -v1, -v1
	v_max_f32_e64 v70, -v70, -v70
	v_max_f32_e64 v73, -v73, -v73
	v_max_f32_e64 v74, -v74, -v74
	v_max_f32_e64 v75, -v75, -v75
	v_max_f32_e64 v76, -v76, -v76
	v_max_f32_e64 v71, -v71, -v71
	v_max_f32_e64 v72, -v72, -v72
	v_min_f32_e32 v1, 0x42700000, v1
	v_min_f32_e32 v70, 0x42700000, v70
	v_min_f32_e32 v73, 0x42700000, v73
	v_min_f32_e32 v74, 0x42700000, v74
	v_min_f32_e32 v75, 0x42700000, v75
	v_min_f32_e32 v76, 0x42700000, v76
	v_min_f32_e32 v71, 0x42700000, v71
	v_min_f32_e32 v72, 0x42700000, v72
	v_mul_f32_e32 v1, 0x3fb8aa3b, v1
	v_mul_f32_e32 v70, 0x3fb8aa3b, v70
	v_mul_f32_e32 v73, 0x3fb8aa3b, v73
	v_mul_f32_e32 v74, 0x3fb8aa3b, v74
	v_mul_f32_e32 v75, 0x3fb8aa3b, v75
	v_mul_f32_e32 v76, 0x3fb8aa3b, v76
	v_mul_f32_e32 v71, 0x3fb8aa3b, v71
	v_mul_f32_e32 v72, 0x3fb8aa3b, v72
	v_exp_f32_e32 v1, v1
	v_exp_f32_e32 v70, v70
	v_exp_f32_e32 v73, v73
	v_exp_f32_e32 v74, v74
	v_exp_f32_e32 v75, v75
	v_exp_f32_e32 v76, v76
	v_exp_f32_e32 v71, v71
	v_exp_f32_e32 v72, v72
	v_add_f32_e32 v1, 1.0, v1
	v_add_f32_e32 v77, 1.0, v70
	v_add_f32_e32 v82, 1.0, v73
	v_add_f32_e32 v83, 1.0, v74
	v_add_f32_e32 v75, 1.0, v75
	v_add_f32_e32 v84, 1.0, v76
	v_add_f32_e32 v80, 1.0, v71
	v_add_f32_e32 v81, 1.0, v72
	v_rcp_f32_e32 v70, v1
	v_rcp_f32_e32 v71, v77
	v_rcp_f32_e32 v74, v82
	v_rcp_f32_e32 v76, v75
	v_rcp_f32_e32 v77, v84
	v_rcp_f32_e32 v75, v83
	v_rcp_f32_e32 v72, v80
	v_rcp_f32_e32 v73, v81
	v_pk_mul_f32 v[64:65], v[64:65], v[70:71]
	v_pk_mul_f32 v[70:71], v[62:63], v[76:77]
	v_pk_mul_f32 v[62:63], v[60:61], v[74:75]
	v_pk_mul_f32 v[66:67], v[66:67], v[72:73]
	v_cvt_pk_bf16_f32 v60, v64, v65
	v_add_u32_e32 v64, 0x90, v148
	v_cvt_pk_bf16_f32 v61, v66, v67
	v_cvt_pk_bf16_f32 v62, v62, v63
	v_cvt_pk_bf16_f32 v63, v70, v71
	global_store_dwordx4 v[68:69], v[60:63], off
	global_load_dwordx4 v[60:63], v[78:79], off
	v_mad_i64_i32 v[66:67], s[4:5], v64, s69, v[124:125]
	v_lshl_add_u64 v[66:67], v[66:67], 0, s[6:7]
	v_lshl_add_u64 v[70:71], v[66:67], 0, v[2:3]
	s_waitcnt vmcnt(0)
	v_lshlrev_b32_e32 v1, 16, v60
	v_and_b32_e32 v60, 0xffff0000, v60
	v_lshlrev_b32_e32 v65, 16, v61
	v_and_b32_e32 v61, 0xffff0000, v61
	v_lshlrev_b32_e32 v73, 16, v63
	v_and_b32_e32 v63, 0xffff0000, v63
	v_lshlrev_b32_e32 v72, 16, v62
	v_and_b32_e32 v62, 0xffff0000, v62
	v_max_f32_e64 v1, -v1, -v1
	v_max_f32_e64 v60, -v60, -v60
	v_max_f32_e64 v65, -v65, -v65
	v_max_f32_e64 v61, -v61, -v61
	v_max_f32_e64 v73, -v73, -v73
	v_max_f32_e64 v63, -v63, -v63
	v_max_f32_e64 v72, -v72, -v72
	v_max_f32_e64 v62, -v62, -v62
	v_min_f32_e32 v1, 0x42700000, v1
	v_min_f32_e32 v60, 0x42700000, v60
	v_min_f32_e32 v65, 0x42700000, v65
	v_min_f32_e32 v61, 0x42700000, v61
	v_min_f32_e32 v73, 0x42700000, v73
	v_min_f32_e32 v63, 0x42700000, v63
	v_min_f32_e32 v72, 0x42700000, v72
	v_min_f32_e32 v62, 0x42700000, v62
	v_mul_f32_e32 v1, 0x3fb8aa3b, v1
	v_mul_f32_e32 v60, 0x3fb8aa3b, v60
	v_mul_f32_e32 v65, 0x3fb8aa3b, v65
	v_mul_f32_e32 v61, 0x3fb8aa3b, v61
	v_mul_f32_e32 v73, 0x3fb8aa3b, v73
	v_mul_f32_e32 v63, 0x3fb8aa3b, v63
	v_mul_f32_e32 v72, 0x3fb8aa3b, v72
	v_mul_f32_e32 v62, 0x3fb8aa3b, v62
	v_exp_f32_e32 v1, v1
	v_exp_f32_e32 v60, v60
	v_exp_f32_e32 v65, v65
	v_exp_f32_e32 v61, v61
	v_exp_f32_e32 v73, v73
	v_exp_f32_e32 v63, v63
	v_exp_f32_e32 v72, v72
	v_exp_f32_e32 v62, v62
	v_add_f32_e32 v1, 1.0, v1
	v_add_f32_e32 v74, 1.0, v60
	v_add_f32_e32 v65, 1.0, v65
	v_add_f32_e32 v75, 1.0, v61
	v_add_f32_e32 v73, 1.0, v73
	v_add_f32_e32 v77, 1.0, v63
	v_add_f32_e32 v72, 1.0, v72
	v_add_f32_e32 v76, 1.0, v62
	v_rcp_f32_e32 v60, v1
	v_rcp_f32_e32 v61, v74
	v_rcp_f32_e32 v62, v65
	v_rcp_f32_e32 v63, v75
	v_rcp_f32_e32 v74, v73
	v_rcp_f32_e32 v75, v77
	v_rcp_f32_e32 v72, v72
	v_rcp_f32_e32 v73, v76
	v_pk_mul_f32 v[58:59], v[58:59], v[62:63]
	v_pk_mul_f32 v[56:57], v[56:57], v[60:61]
	v_pk_mul_f32 v[60:61], v[54:55], v[74:75]
	v_pk_mul_f32 v[52:53], v[52:53], v[72:73]
	v_cvt_pk_bf16_f32 v54, v56, v57
	v_cvt_pk_bf16_f32 v55, v58, v59
	v_ashrrev_i32_e32 v65, 31, v64
	v_cvt_pk_bf16_f32 v56, v52, v53
	v_cvt_pk_bf16_f32 v57, v60, v61
	global_load_dwordx4 v[58:61], v[70:71], off
	v_lshl_add_u64 v[62:63], v[66:67], 0, v[150:151]
	global_store_dwordx4 v[68:69], v[54:57], off offset:256
	v_lshlrev_b64 v[52:53], 12, v[64:65]
	v_lshl_add_u64 v[52:53], s[10:11], 0, v[52:53]
	v_lshl_add_u64 v[52:53], v[52:53], 0, v[2:3]
	s_waitcnt vmcnt(0)
; __device__ __forceinline__ unsigned cvt_pk_bf16(float lo, float hi) { unsigned r; asm volatile("v_cvt_pk_bf16_f32 %0, %1, %2" : "=v"(r) : "v"(lo), "v"(hi)); return r; }
; __device__ __forceinline__ float bf_lo(unsigned w) { return __uint_as_float(w << 16); }
; __device__ __forceinline__ float bf_hi(unsigned w) { return __uint_as_float(w & 0xffff0000u); }
;     static __device__ __forceinline__ float ex(float x) { return __expf(fminf(-x, 60.f)); }
;     __device__ __forceinline__ void operator()(const f32x4 (&acc)[2][2][4][2], const Unit& u, int wr, int wc, int fr, int fq) const {
;     ...
;                 for (int bj = 0; bj < 2; ++bj) { const int col = col0 + bj * HALF;
;                     const u32x4 gc = *(const u32x4*)(R + (size_t)row * R_LD + 8192 + col);
;                     f32x4 s0, s1;
;                     s0[0] = __builtin_amdgcn_rcpf(1.0f + ex(bf_lo(gc.x))); s0[1] = __builtin_amdgcn_rcpf(1.0f + ex(bf_hi(gc.x))); s0[2] = __builtin_amdgcn_rcpf(1.0f + ex(bf_lo(gc.y))); s0[3] = __builtin_amdgcn_rcpf(1.0f + ex(bf_hi(gc.y)));
;                     s1[0] = __builtin_amdgcn_rcpf(1.0f + ex(bf_lo(gc.z))); s1[1] = __builtin_amdgcn_rcpf(1.0f + ex(bf_hi(gc.z))); s1[2] = __builtin_amdgcn_rcpf(1.0f + ex(bf_lo(gc.w))); s1[3] = __builtin_amdgcn_rcpf(1.0f + ex(bf_hi(gc.w)));
;                     const f32x4 v0 = acc[ai][bj][m][0] * s0, v1 = acc[ai][bj][m][1] * s1;
;                     u32x4 w; w.x = cvt_pk_bf16(v0[0], v0[1]); w.y = cvt_pk_bf16(v0[2], v0[3]); w.z = cvt_pk_bf16(v1[0], v1[1]); w.w = cvt_pk_bf16(v1[2], v1[3]);
;                     *(u32x4*)(O + (size_t)row * 2048 + col) = w; } }
	v_lshlrev_b32_e32 v1, 16, v58
	v_and_b32_e32 v54, 0xffff0000, v58
	v_lshlrev_b32_e32 v55, 16, v59
	v_and_b32_e32 v56, 0xffff0000, v59
	v_lshlrev_b32_e32 v57, 16, v60
	v_and_b32_e32 v58, 0xffff0000, v60
	v_lshlrev_b32_e32 v59, 16, v61
	v_and_b32_e32 v60, 0xffff0000, v61
	v_max_f32_e64 v1, -v1, -v1
	v_max_f32_e64 v54, -v54, -v54
	v_max_f32_e64 v57, -v57, -v57
	v_max_f32_e64 v58, -v58, -v58
	v_max_f32_e64 v59, -v59, -v59
	v_max_f32_e64 v60, -v60, -v60
	v_max_f32_e64 v55, -v55, -v55
	v_max_f32_e64 v56, -v56, -v56
	v_min_f32_e32 v1, 0x42700000, v1
	v_min_f32_e32 v54, 0x42700000, v54
	v_min_f32_e32 v57, 0x42700000, v57
	v_min_f32_e32 v58, 0x42700000, v58
	v_min_f32_e32 v59, 0x42700000, v59
	v_min_f32_e32 v60, 0x42700000, v60
	v_min_f32_e32 v55, 0x42700000, v55
	v_min_f32_e32 v56, 0x42700000, v56
	v_mul_f32_e32 v1, 0x3fb8aa3b, v1
	v_mul_f32_e32 v54, 0x3fb8aa3b, v54
	v_mul_f32_e32 v57, 0x3fb8aa3b, v57
	v_mul_f32_e32 v58, 0x3fb8aa3b, v58
	v_mul_f32_e32 v59, 0x3fb8aa3b, v59
	v_mul_f32_e32 v60, 0x3fb8aa3b, v60
	v_mul_f32_e32 v55, 0x3fb8aa3b, v55
	v_mul_f32_e32 v56, 0x3fb8aa3b, v56
	v_exp_f32_e32 v1, v1
	v_exp_f32_e32 v54, v54
	v_exp_f32_e32 v57, v57
	v_exp_f32_e32 v58, v58
	v_exp_f32_e32 v59, v59
	v_exp_f32_e32 v60, v60
	v_exp_f32_e32 v55, v55
	v_exp_f32_e32 v56, v56
	v_add_f32_e32 v1, 1.0, v1
	v_add_f32_e32 v61, 1.0, v54
	v_add_f32_e32 v66, 1.0, v57
	v_add_f32_e32 v67, 1.0, v58
	v_add_f32_e32 v59, 1.0, v59
	v_add_f32_e32 v68, 1.0, v60
	v_add_f32_e32 v64, 1.0, v55
	v_add_f32_e32 v65, 1.0, v56
	v_rcp_f32_e32 v54, v1
	v_rcp_f32_e32 v55, v61
	v_rcp_f32_e32 v58, v66
	v_rcp_f32_e32 v60, v59
	v_rcp_f32_e32 v61, v68
	v_rcp_f32_e32 v59, v67
	v_rcp_f32_e32 v56, v64
	v_rcp_f32_e32 v57, v65
	v_pk_mul_f32 v[48:49], v[48:49], v[54:55]
	v_pk_mul_f32 v[54:55], v[46:47], v[60:61]
	v_pk_mul_f32 v[46:47], v[44:45], v[58:59]
	v_pk_mul_f32 v[50:51], v[50:51], v[56:57]
	v_cvt_pk_bf16_f32 v44, v48, v49
	v_add_u32_e32 v48, 0xa0, v148
	v_cvt_pk_bf16_f32 v45, v50, v51
	v_cvt_pk_bf16_f32 v46, v46, v47
	v_cvt_pk_bf16_f32 v47, v54, v55
	global_store_dwordx4 v[52:53], v[44:47], off
	global_load_dwordx4 v[44:47], v[62:63], off
	v_mad_i64_i32 v[50:51], s[4:5], v48, s69, v[124:125]
	v_lshl_add_u64 v[50:51], v[50:51], 0, s[6:7]
	v_lshl_add_u64 v[54:55], v[50:51], 0, v[2:3]
	s_waitcnt vmcnt(0)
	v_lshlrev_b32_e32 v1, 16, v44
	v_and_b32_e32 v44, 0xffff0000, v44
	v_lshlrev_b32_e32 v49, 16, v45
	v_and_b32_e32 v45, 0xffff0000, v45
	v_lshlrev_b32_e32 v57, 16, v47
	v_and_b32_e32 v47, 0xffff0000, v47
	v_lshlrev_b32_e32 v56, 16, v46
	v_and_b32_e32 v46, 0xffff0000, v46
	v_max_f32_e64 v1, -v1, -v1
	v_max_f32_e64 v44, -v44, -v44
	v_max_f32_e64 v49, -v49, -v49
	v_max_f32_e64 v45, -v45, -v45
	v_max_f32_e64 v57, -v57, -v57
	v_max_f32_e64 v47, -v47, -v47
	v_max_f32_e64 v56, -v56, -v56
	v_max_f32_e64 v46, -v46, -v46
	v_min_f32_e32 v1, 0x42700000, v1
	v_min_f32_e32 v44, 0x42700000, v44
	v_min_f32_e32 v49, 0x42700000, v49
	v_min_f32_e32 v45, 0x42700000, v45
	v_min_f32_e32 v57, 0x42700000, v57
	v_min_f32_e32 v47, 0x42700000, v47
	v_min_f32_e32 v56, 0x42700000, v56
	v_min_f32_e32 v46, 0x42700000, v46
	v_mul_f32_e32 v1, 0x3fb8aa3b, v1
	v_mul_f32_e32 v44, 0x3fb8aa3b, v44
	v_mul_f32_e32 v49, 0x3fb8aa3b, v49
	v_mul_f32_e32 v45, 0x3fb8aa3b, v45
	v_mul_f32_e32 v57, 0x3fb8aa3b, v57
	v_mul_f32_e32 v47, 0x3fb8aa3b, v47
	v_mul_f32_e32 v56, 0x3fb8aa3b, v56
	v_mul_f32_e32 v46, 0x3fb8aa3b, v46
	v_exp_f32_e32 v1, v1
	v_exp_f32_e32 v44, v44
	v_exp_f32_e32 v49, v49
	v_exp_f32_e32 v45, v45
	v_exp_f32_e32 v57, v57
	v_exp_f32_e32 v47, v47
	v_exp_f32_e32 v56, v56
	v_exp_f32_e32 v46, v46
	v_add_f32_e32 v1, 1.0, v1
	v_add_f32_e32 v58, 1.0, v44
	v_add_f32_e32 v49, 1.0, v49
	v_add_f32_e32 v59, 1.0, v45
	v_add_f32_e32 v57, 1.0, v57
	v_add_f32_e32 v61, 1.0, v47
	v_add_f32_e32 v56, 1.0, v56
	v_add_f32_e32 v60, 1.0, v46
	v_rcp_f32_e32 v44, v1
	v_rcp_f32_e32 v45, v58
	v_rcp_f32_e32 v46, v49
	v_rcp_f32_e32 v47, v59
	v_rcp_f32_e32 v58, v57
	v_rcp_f32_e32 v59, v61
	v_rcp_f32_e32 v56, v56
	v_rcp_f32_e32 v57, v60
	v_pk_mul_f32 v[42:43], v[42:43], v[46:47]
	v_pk_mul_f32 v[40:41], v[40:41], v[44:45]
	v_pk_mul_f32 v[44:45], v[38:39], v[58:59]
	v_pk_mul_f32 v[36:37], v[36:37], v[56:57]
	v_cvt_pk_bf16_f32 v38, v40, v41
	v_cvt_pk_bf16_f32 v39, v42, v43
	v_ashrrev_i32_e32 v49, 31, v48
	v_cvt_pk_bf16_f32 v40, v36, v37
	v_cvt_pk_bf16_f32 v41, v44, v45
	global_load_dwordx4 v[42:45], v[54:55], off
	v_lshl_add_u64 v[46:47], v[50:51], 0, v[150:151]
	global_store_dwordx4 v[52:53], v[38:41], off offset:256
	v_lshlrev_b64 v[36:37], 12, v[48:49]
	v_lshl_add_u64 v[36:37], s[10:11], 0, v[36:37]
	v_lshl_add_u64 v[36:37], v[36:37], 0, v[2:3]
	s_waitcnt vmcnt(0)
; __device__ __forceinline__ unsigned cvt_pk_bf16(float lo, float hi) { unsigned r; asm volatile("v_cvt_pk_bf16_f32 %0, %1, %2" : "=v"(r) : "v"(lo), "v"(hi)); return r; }
; __device__ __forceinline__ float bf_lo(unsigned w) { return __uint_as_float(w << 16); }
; __device__ __forceinline__ float bf_hi(unsigned w) { return __uint_as_float(w & 0xffff0000u); }
;     static __device__ __forceinline__ float ex(float x) { return __expf(fminf(-x, 60.f)); }
;     __device__ __forceinline__ void operator()(const f32x4 (&acc)[2][2][4][2], const Unit& u, int wr, int wc, int fr, int fq) const {
;     ...
;                 for (int bj = 0; bj < 2; ++bj) { const int col = col0 + bj * HALF;
;                     const u32x4 gc = *(const u32x4*)(R + (size_t)row * R_LD + 8192 + col);
;                     f32x4 s0, s1;
;                     s0[0] = __builtin_amdgcn_rcpf(1.0f + ex(bf_lo(gc.x))); s0[1] = __builtin_amdgcn_rcpf(1.0f + ex(bf_hi(gc.x))); s0[2] = __builtin_amdgcn_rcpf(1.0f + ex(bf_lo(gc.y))); s0[3] = __builtin_amdgcn_rcpf(1.0f + ex(bf_hi(gc.y)));
;                     s1[0] = __builtin_amdgcn_rcpf(1.0f + ex(bf_lo(gc.z))); s1[1] = __builtin_amdgcn_rcpf(1.0f + ex(bf_hi(gc.z))); s1[2] = __builtin_amdgcn_rcpf(1.0f + ex(bf_lo(gc.w))); s1[3] = __builtin_amdgcn_rcpf(1.0f + ex(bf_hi(gc.w)));
;                     const f32x4 v0 = acc[ai][bj][m][0] * s0, v1 = acc[ai][bj][m][1] * s1;
;                     u32x4 w; w.x = cvt_pk_bf16(v0[0], v0[1]); w.y = cvt_pk_bf16(v0[2], v0[3]); w.z = cvt_pk_bf16(v1[0], v1[1]); w.w = cvt_pk_bf16(v1[2], v1[3]);
;                     *(u32x4*)(O + (size_t)row * 2048 + col) = w; } }
	v_lshlrev_b32_e32 v1, 16, v42
	v_and_b32_e32 v38, 0xffff0000, v42
	v_lshlrev_b32_e32 v39, 16, v43
	v_and_b32_e32 v40, 0xffff0000, v43
	v_lshlrev_b32_e32 v41, 16, v44
	v_and_b32_e32 v42, 0xffff0000, v44
	v_lshlrev_b32_e32 v43, 16, v45
	v_and_b32_e32 v44, 0xffff0000, v45
	v_max_f32_e64 v1, -v1, -v1
	v_max_f32_e64 v38, -v38, -v38
	v_max_f32_e64 v41, -v41, -v41
	v_max_f32_e64 v42, -v42, -v42
	v_max_f32_e64 v43, -v43, -v43
	v_max_f32_e64 v44, -v44, -v44
	v_max_f32_e64 v39, -v39, -v39
	v_max_f32_e64 v40, -v40, -v40
	v_min_f32_e32 v1, 0x42700000, v1
	v_min_f32_e32 v38, 0x42700000, v38
	v_min_f32_e32 v41, 0x42700000, v41
	v_min_f32_e32 v42, 0x42700000, v42
	v_min_f32_e32 v43, 0x42700000, v43
	v_min_f32_e32 v44, 0x42700000, v44
	v_min_f32_e32 v39, 0x42700000, v39
	v_min_f32_e32 v40, 0x42700000, v40
	v_mul_f32_e32 v1, 0x3fb8aa3b, v1
	v_mul_f32_e32 v38, 0x3fb8aa3b, v38
	v_mul_f32_e32 v41, 0x3fb8aa3b, v41
	v_mul_f32_e32 v42, 0x3fb8aa3b, v42
	v_mul_f32_e32 v43, 0x3fb8aa3b, v43
	v_mul_f32_e32 v44, 0x3fb8aa3b, v44
	v_mul_f32_e32 v39, 0x3fb8aa3b, v39
	v_mul_f32_e32 v40, 0x3fb8aa3b, v40
	v_exp_f32_e32 v1, v1
	v_exp_f32_e32 v38, v38
	v_exp_f32_e32 v41, v41
	v_exp_f32_e32 v42, v42
	v_exp_f32_e32 v43, v43
	v_exp_f32_e32 v44, v44
	v_exp_f32_e32 v39, v39
	v_exp_f32_e32 v40, v40
	v_add_f32_e32 v1, 1.0, v1
	v_add_f32_e32 v45, 1.0, v38
	v_add_f32_e32 v50, 1.0, v41
	v_add_f32_e32 v51, 1.0, v42
	v_add_f32_e32 v43, 1.0, v43
	v_add_f32_e32 v52, 1.0, v44
	v_add_f32_e32 v48, 1.0, v39
	v_add_f32_e32 v49, 1.0, v40
	v_rcp_f32_e32 v38, v1
	v_rcp_f32_e32 v39, v45
	v_rcp_f32_e32 v42, v50
	v_rcp_f32_e32 v44, v43
	v_rcp_f32_e32 v45, v52
	v_rcp_f32_e32 v43, v51
	v_rcp_f32_e32 v40, v48
	v_rcp_f32_e32 v41, v49
	v_pk_mul_f32 v[32:33], v[32:33], v[38:39]
	v_pk_mul_f32 v[38:39], v[30:31], v[44:45]
	v_pk_mul_f32 v[30:31], v[28:29], v[42:43]
	v_pk_mul_f32 v[34:35], v[34:35], v[40:41]
	v_cvt_pk_bf16_f32 v28, v32, v33
	v_add_u32_e32 v32, 0xb0, v148
	v_cvt_pk_bf16_f32 v29, v34, v35
	v_cvt_pk_bf16_f32 v30, v30, v31
	v_cvt_pk_bf16_f32 v31, v38, v39
	global_store_dwordx4 v[36:37], v[28:31], off
	global_load_dwordx4 v[28:31], v[46:47], off
	v_mad_i64_i32 v[34:35], s[4:5], v32, s69, v[124:125]
	v_lshl_add_u64 v[34:35], v[34:35], 0, s[6:7]
	v_lshl_add_u64 v[38:39], v[34:35], 0, v[2:3]
	s_waitcnt vmcnt(0)
	v_lshlrev_b32_e32 v1, 16, v28
	v_and_b32_e32 v28, 0xffff0000, v28
	v_lshlrev_b32_e32 v33, 16, v29
	v_and_b32_e32 v29, 0xffff0000, v29
	v_lshlrev_b32_e32 v40, 16, v30
	v_and_b32_e32 v30, 0xffff0000, v30
	v_lshlrev_b32_e32 v41, 16, v31
	v_and_b32_e32 v31, 0xffff0000, v31
	v_max_f32_e64 v1, -v1, -v1
	v_max_f32_e64 v28, -v28, -v28
	v_max_f32_e64 v33, -v33, -v33
	v_max_f32_e64 v29, -v29, -v29
	v_max_f32_e64 v40, -v40, -v40
	v_max_f32_e64 v30, -v30, -v30
	v_max_f32_e64 v41, -v41, -v41
	v_max_f32_e64 v31, -v31, -v31
	v_min_f32_e32 v1, 0x42700000, v1
	v_min_f32_e32 v28, 0x42700000, v28
	v_min_f32_e32 v33, 0x42700000, v33
	v_min_f32_e32 v29, 0x42700000, v29
	v_min_f32_e32 v40, 0x42700000, v40
	v_min_f32_e32 v30, 0x42700000, v30
	v_min_f32_e32 v41, 0x42700000, v41
	v_min_f32_e32 v31, 0x42700000, v31
	v_mul_f32_e32 v1, 0x3fb8aa3b, v1
	v_mul_f32_e32 v28, 0x3fb8aa3b, v28
	v_mul_f32_e32 v33, 0x3fb8aa3b, v33
	v_mul_f32_e32 v29, 0x3fb8aa3b, v29
	v_mul_f32_e32 v40, 0x3fb8aa3b, v40
	v_mul_f32_e32 v30, 0x3fb8aa3b, v30
	v_mul_f32_e32 v41, 0x3fb8aa3b, v41
	v_mul_f32_e32 v31, 0x3fb8aa3b, v31
	v_exp_f32_e32 v1, v1
	v_exp_f32_e32 v28, v28
	v_exp_f32_e32 v33, v33
	v_exp_f32_e32 v29, v29
	v_exp_f32_e32 v40, v40
	v_exp_f32_e32 v30, v30
	v_exp_f32_e32 v41, v41
	v_exp_f32_e32 v31, v31
	v_add_f32_e32 v1, 1.0, v1
	v_add_f32_e32 v42, 1.0, v28
	v_add_f32_e32 v33, 1.0, v33
	v_add_f32_e32 v43, 1.0, v29
	v_add_f32_e32 v40, 1.0, v40
	v_add_f32_e32 v44, 1.0, v30
	v_add_f32_e32 v41, 1.0, v41
	v_add_f32_e32 v45, 1.0, v31
	v_rcp_f32_e32 v28, v1
	v_rcp_f32_e32 v29, v42
	v_rcp_f32_e32 v30, v33
	v_rcp_f32_e32 v31, v43
	v_rcp_f32_e32 v40, v40
	v_rcp_f32_e32 v42, v41
	v_rcp_f32_e32 v43, v45
	v_rcp_f32_e32 v41, v44
	v_pk_mul_f32 v[26:27], v[26:27], v[30:31]
	v_pk_mul_f32 v[24:25], v[24:25], v[28:29]
	v_pk_mul_f32 v[28:29], v[22:23], v[42:43]
	v_pk_mul_f32 v[22:23], v[20:21], v[40:41]
	v_cvt_pk_bf16_f32 v20, v24, v25
	v_cvt_pk_bf16_f32 v21, v26, v27
	v_ashrrev_i32_e32 v33, 31, v32
	v_cvt_pk_bf16_f32 v22, v22, v23
	v_cvt_pk_bf16_f32 v23, v28, v29
	global_load_dwordx4 v[24:27], v[38:39], off
	v_lshlrev_b64 v[28:29], 12, v[32:33]
	v_lshl_add_u64 v[28:29], s[10:11], 0, v[28:29]
	v_lshl_add_u64 v[28:29], v[28:29], 0, v[2:3]
	global_store_dwordx4 v[36:37], v[20:23], off offset:256
	v_lshl_add_u64 v[30:31], v[34:35], 0, v[150:151]
	s_waitcnt vmcnt(0)
; __device__ __forceinline__ unsigned cvt_pk_bf16(float lo, float hi) { unsigned r; asm volatile("v_cvt_pk_bf16_f32 %0, %1, %2" : "=v"(r) : "v"(lo), "v"(hi)); return r; }
; #define PG8_BAR __builtin_amdgcn_s_barrier()
;     static __device__ __forceinline__ float ex(float x) { return __expf(fminf(-x, 60.f)); }
;     __device__ __forceinline__ void operator()(const f32x4 (&acc)[2][2][4][2], const Unit& u, int wr, int wc, int fr, int fq) const {
;     ...
;                 for (int bj = 0; bj < 2; ++bj) { const int col = col0 + bj * HALF;
;                     const u32x4 gc = *(const u32x4*)(R + (size_t)row * R_LD + 8192 + col);
;                     f32x4 s0, s1;
;                     s0[0] = __builtin_amdgcn_rcpf(1.0f + ex(bf_lo(gc.x))); s0[1] = __builtin_amdgcn_rcpf(1.0f + ex(bf_hi(gc.x))); s0[2] = __builtin_amdgcn_rcpf(1.0f + ex(bf_lo(gc.y))); s0[3] = __builtin_amdgcn_rcpf(1.0f + ex(bf_hi(gc.y)));
;                     s1[0] = __builtin_amdgcn_rcpf(1.0f + ex(bf_lo(gc.z))); s1[1] = __builtin_amdgcn_rcpf(1.0f + ex(bf_hi(gc.z))); s1[2] = __builtin_amdgcn_rcpf(1.0f + ex(bf_lo(gc.w))); s1[3] = __builtin_amdgcn_rcpf(1.0f + ex(bf_hi(gc.w)));
;                     const f32x4 v0 = acc[ai][bj][m][0] * s0, v1 = acc[ai][bj][m][1] * s1;
;                     u32x4 w; w.x = cvt_pk_bf16(v0[0], v0[1]); w.y = cvt_pk_bf16(v0[2], v0[3]); w.z = cvt_pk_bf16(v1[0], v1[1]); w.w = cvt_pk_bf16(v1[2], v1[3]);
;                     *(u32x4*)(O + (size_t)row * 2048 + col) = w; } }
; template <class Epi, class Sched, bool ALIGN_EPI = false, bool SP2 = false>
; __device__ __forceinline__ void gemm_phase(PG8_LAS unsigned char* lds, const Gemm g, const Sched& S, const Epi& E, const int tid_in) {
;     ...
;         if constexpr (ALIGN_EPI) { if (wr == 0) PG8_BAR; }
;         if constexpr (!Epi::AFTER_DRAIN) { E(acc, cur, wr, wc, fr, fq); S.done(cur); }
;         if (!has_next) break;
; #pragma unroll
;         for (int a = 0; a < 2; ++a)
; #pragma unroll
;             for (int b = 0; b < 2; ++b)
; #pragma unroll
;                 for (int m = 0; m < 4; ++m)
; #pragma unroll
;                     for (int n = 0; n < 2; ++n) acc[a][b][m][n] = (f32x4){0.f, 0.f, 0.f, 0.f};
;         cur = nxt; cA = nA; cB = nB; ++ui; if constexpr (Sched::GATHER) { vc[0][0] = vn[0][0]; vc[0][1] = vn[0][1]; vc[1][0] = vn[1][0]; vc[1][1] = vn[1][1]; }
;         if constexpr (ALIGN_EPI) { if (wr == 1) PG8_BAR; }
	v_lshlrev_b32_e32 v1, 16, v24
	v_and_b32_e32 v2, 0xffff0000, v24
	v_lshlrev_b32_e32 v21, 16, v26
	v_and_b32_e32 v22, 0xffff0000, v26
	v_lshlrev_b32_e32 v23, 16, v27
	v_and_b32_e32 v24, 0xffff0000, v27
	v_lshlrev_b32_e32 v3, 16, v25
	v_and_b32_e32 v20, 0xffff0000, v25
	v_max_f32_e64 v1, -v1, -v1
	v_max_f32_e64 v2, -v2, -v2
	v_max_f32_e64 v21, -v21, -v21
	v_max_f32_e64 v22, -v22, -v22
	v_max_f32_e64 v23, -v23, -v23
	v_max_f32_e64 v24, -v24, -v24
	v_max_f32_e64 v3, -v3, -v3
	v_max_f32_e64 v20, -v20, -v20
	v_min_f32_e32 v1, 0x42700000, v1
	v_min_f32_e32 v2, 0x42700000, v2
	v_min_f32_e32 v21, 0x42700000, v21
	v_min_f32_e32 v22, 0x42700000, v22
	v_min_f32_e32 v23, 0x42700000, v23
	v_min_f32_e32 v24, 0x42700000, v24
	v_min_f32_e32 v3, 0x42700000, v3
	v_min_f32_e32 v20, 0x42700000, v20
	v_mul_f32_e32 v1, 0x3fb8aa3b, v1
	v_mul_f32_e32 v2, 0x3fb8aa3b, v2
	v_mul_f32_e32 v21, 0x3fb8aa3b, v21
	v_mul_f32_e32 v22, 0x3fb8aa3b, v22
	v_mul_f32_e32 v23, 0x3fb8aa3b, v23
	v_mul_f32_e32 v24, 0x3fb8aa3b, v24
	v_mul_f32_e32 v3, 0x3fb8aa3b, v3
	v_mul_f32_e32 v20, 0x3fb8aa3b, v20
	v_exp_f32_e32 v1, v1
	v_exp_f32_e32 v2, v2
	v_exp_f32_e32 v21, v21
	v_exp_f32_e32 v22, v22
	v_exp_f32_e32 v23, v23
	v_exp_f32_e32 v24, v24
	v_exp_f32_e32 v3, v3
	v_exp_f32_e32 v20, v20
	v_add_f32_e32 v1, 1.0, v1
	v_add_f32_e32 v25, 1.0, v2
	v_add_f32_e32 v32, 1.0, v21
	v_add_f32_e32 v33, 1.0, v22
	v_add_f32_e32 v23, 1.0, v23
	v_add_f32_e32 v34, 1.0, v24
	v_add_f32_e32 v26, 1.0, v3
	v_add_f32_e32 v27, 1.0, v20
	v_rcp_f32_e32 v2, v1
	v_rcp_f32_e32 v3, v25
	v_rcp_f32_e32 v22, v32
	v_rcp_f32_e32 v24, v23
	v_rcp_f32_e32 v25, v34
	v_rcp_f32_e32 v23, v33
	v_rcp_f32_e32 v20, v26
	v_rcp_f32_e32 v21, v27
	v_pk_mul_f32 v[2:3], v[16:17], v[2:3]
	v_pk_mul_f32 v[16:17], v[14:15], v[24:25]
	v_pk_mul_f32 v[14:15], v[12:13], v[22:23]
	v_pk_mul_f32 v[18:19], v[18:19], v[20:21]
	v_cvt_pk_bf16_f32 v12, v2, v3
	s_nop 0
	v_cvt_pk_bf16_f32 v13, v18, v19
	v_cvt_pk_bf16_f32 v14, v14, v15
	v_cvt_pk_bf16_f32 v15, v16, v17
	global_store_dwordx4 v[28:29], v[12:15], off
	global_load_dwordx4 v[12:15], v[30:31], off
	s_waitcnt vmcnt(0)
	v_lshlrev_b32_e32 v1, 16, v12
	v_and_b32_e32 v2, 0xffff0000, v12
	v_lshlrev_b32_e32 v3, 16, v13
	v_and_b32_e32 v12, 0xffff0000, v13
	v_lshlrev_b32_e32 v13, 16, v14
	v_and_b32_e32 v14, 0xffff0000, v14
	v_lshlrev_b32_e32 v16, 16, v15
	v_and_b32_e32 v15, 0xffff0000, v15
	v_max_f32_e64 v1, -v1, -v1
	v_max_f32_e64 v2, -v2, -v2
	v_max_f32_e64 v13, -v13, -v13
	v_max_f32_e64 v14, -v14, -v14
	v_max_f32_e64 v15, -v15, -v15
	v_max_f32_e64 v3, -v3, -v3
	v_max_f32_e64 v12, -v12, -v12
	v_max_f32_e64 v16, -v16, -v16
	v_min_f32_e32 v1, 0x42700000, v1
	v_min_f32_e32 v2, 0x42700000, v2
	v_min_f32_e32 v13, 0x42700000, v13
	v_min_f32_e32 v14, 0x42700000, v14
	v_min_f32_e32 v15, 0x42700000, v15
	v_min_f32_e32 v3, 0x42700000, v3
	v_min_f32_e32 v12, 0x42700000, v12
	v_min_f32_e32 v16, 0x42700000, v16
	v_mul_f32_e32 v1, 0x3fb8aa3b, v1
	v_mul_f32_e32 v2, 0x3fb8aa3b, v2
	v_mul_f32_e32 v13, 0x3fb8aa3b, v13
	v_mul_f32_e32 v14, 0x3fb8aa3b, v14
	v_mul_f32_e32 v15, 0x3fb8aa3b, v15
	v_mul_f32_e32 v3, 0x3fb8aa3b, v3
	v_mul_f32_e32 v12, 0x3fb8aa3b, v12
	v_mul_f32_e32 v16, 0x3fb8aa3b, v16
	v_exp_f32_e32 v1, v1
	v_exp_f32_e32 v2, v2
	v_exp_f32_e32 v13, v13
	v_exp_f32_e32 v14, v14
	v_exp_f32_e32 v15, v15
	v_exp_f32_e32 v3, v3
	v_exp_f32_e32 v12, v12
	v_exp_f32_e32 v16, v16
	v_add_f32_e32 v1, 1.0, v1
	v_add_f32_e32 v17, 1.0, v2
	v_add_f32_e32 v20, 1.0, v13
	v_add_f32_e32 v21, 1.0, v14
	v_add_f32_e32 v15, 1.0, v15
	v_add_f32_e32 v18, 1.0, v3
	v_add_f32_e32 v19, 1.0, v12
	v_add_f32_e32 v16, 1.0, v16
	v_rcp_f32_e32 v2, v1
	v_rcp_f32_e32 v3, v17
	v_rcp_f32_e32 v14, v20
	v_rcp_f32_e32 v17, v15
	v_rcp_f32_e32 v15, v21
	v_rcp_f32_e32 v12, v18
	v_rcp_f32_e32 v13, v19
	v_rcp_f32_e32 v16, v16
	v_pk_mul_f32 v[2:3], v[8:9], v[2:3]
	v_pk_mul_f32 v[4:5], v[4:5], v[14:15]
	v_pk_mul_f32 v[10:11], v[10:11], v[12:13]
	v_pk_mul_f32 v[6:7], v[6:7], v[16:17]
	v_cvt_pk_bf16_f32 v2, v2, v3
	v_cvt_pk_bf16_f32 v3, v10, v11
	v_cvt_pk_bf16_f32 v4, v4, v5
	s_nop 0
	v_cvt_pk_bf16_f32 v5, v6, v7
	global_store_dwordx4 v[28:29], v[2:5], off offset:256
	s_cbranch_vccnz .LBB0_773
	s_andn2_b64 vcc, exec, s[8:9]
	s_cbranch_vccnz .LBB0_772
	s_barrier
	s_branch .LBB0_772
